# c3 + leading half starts its epilogue during the trailing half's last MFMA block (loop-bottom barrier rotated, one barrier after the epilogue)
# baseline (speedup 1.0000x reference)
; #define PG8_STAGE(bufoff, gbase, voff) do { _Pragma("unroll") for (int _i = 0; _i < 2; ++_i) \
;         __builtin_amdgcn_global_load_lds((const unsigned*)((const char*)(gbase) + (voff)[_i]), (PG8_LAS unsigned*)(lds + (bufoff) + ldsw + _i * 8192), 16, 0, 0); } while (0)
; #define PG8_LDA(dst, b, h) do { _Pragma("unroll") for (int m = 0; m < 4; ++m) Frag<F8>::load(dst[m], lds + PG8_SA(b, h) + aoff + m * 2048); } while (0)
; #define PG8_LDB(dst, b, h) do { _Pragma("unroll") for (int n = 0; n < 2; ++n) Frag<F8>::load(dst[n], lds + PG8_SB(b, h) + boff + n * 2048); } while (0)
; #define PG8_MMA(ai, bj, At, Bt) do { __builtin_amdgcn_s_setprio(3); _Pragma("unroll") for (int m = 0; m < 4; ++m) _Pragma("unroll") for (int n = 0; n < 2; ++n) Frag<F8>::mma(acc[ai][bj][m][n], Bt[n], At[m]); \
;         __builtin_amdgcn_s_setprio(0); } while (0)
; #define PG8_WAIT_V(n) asm volatile("s_waitcnt vmcnt(" #n ")" ::: "memory")
; #define PG8_WAIT_L(n) asm volatile("s_waitcnt lgkmcnt(" #n ")" ::: "memory")
; #define PG8_BAR __builtin_amdgcn_s_barrier()
; #define PG8_SCHED __builtin_amdgcn_sched_barrier(0)
; template <class Epi, class Sched, bool ALIGN_EPI = false, bool SP2 = false, bool F8 = false>
; __device__ __forceinline__ void gemm_phase(PG8_LAS unsigned char* lds, const Gemm g, const Sched& S, const Epi& E) {
;     ...
;         for (int t = 0; t < nt; t += 2) {
;             const bool last = (t == nt - 2);
;             const char* a1 = cA + (size_t)(t + 1) * kstep;
;             const char* a2 = last ? nA : cA + (size_t)(t + 2) * kstep; const char* b2 = last ? nB : cB + (size_t)(t + 2) * kstep;
;             const char* a3 = a2 + kstep; const char* b3 = b2 + kstep;
;             if (last && has_next) S.a_ready(nxt);
;             if constexpr (SP2) {
;             PG8_LDB(B0, 0, 0); PG8_LDB(B1, 0, 1); PG8_SCHED; PG8_LDA(At, 0, 0); PG8_STAGE(PG8_SA(1, 1), a1 + hstep, voffA);
;             PG8_WAIT_V(8); PG8_WAIT_L(0); PG8_BAR; PG8_MMA(0, 0, At, B0); PG8_MMA(0, 1, At, B1); PG8_BAR; PG8_SCHED;
;             PG8_LDA(At, 0, 1); PG8_STAGE(PG8_SB(0, 0), b2, voffB); PG8_STAGE(PG8_SB(0, 1), b2 + hstep, voffB); PG8_STAGE(PG8_SA(0, 0), a2, voffA);
;             PG8_WAIT_V(8); PG8_WAIT_L(0); PG8_BAR; PG8_MMA(1, 0, At, B0); PG8_MMA(1, 1, At, B1); PG8_BAR; PG8_SCHED;
.LBB0_150:
	s_ashr_i32 s25, s24, 31
	s_lshl_b64 s[4:5], s[24:25], 18
	s_add_u32 s38, s77, s4
	s_addc_u32 s39, s78, s5
	s_and_b64 s[4:5], s[8:9], exec
	s_cselect_b32 s25, s39, s71
	s_cselect_b32 s91, s38, s70
	s_ashr_i32 s31, s30, 31
	s_lshl_b64 s[4:5], s[30:31], 18
	s_add_u32 s42, s79, s4
	s_addc_u32 s43, s80, s5
	s_and_b64 s[4:5], s[8:9], exec
	s_cselect_b32 s31, s43, s73
	s_cselect_b32 s92, s42, s72
	s_add_u32 s70, s70, 0x20080
	s_addc_u32 s71, s71, 0
	s_add_u32 s93, s72, 0x100
	s_addc_u32 s95, s73, 0
	s_mov_b32 s96, -2
	ds_read_b128 v[18:21], v194
	ds_read_b128 v[22:25], v194 offset:1024
	ds_read_b128 v[26:29], v194 offset:2048
	ds_read_b128 v[30:33], v194 offset:3072
	ds_read_b128 v[2:5], v195
	ds_read_b128 v[6:9], v195 offset:1024
	ds_read_b128 v[10:13], v195 offset:2048
	ds_read_b128 v[14:17], v195 offset:3072
	s_add_u32 s0, s70, 0xfffe0080
	s_addc_u32 s1, s71, -1
	s_cmp_eq_u32 s96, 4
	s_cselect_b32 s75, s25, s1
	s_cselect_b32 s74, s91, s0
	s_cselect_b32 s73, s31, s95
	s_cselect_b32 s72, s92, s93
	v_lshl_add_u64 v[224:225], s[70:71], 0, v[174:175]
	s_add_i32 m0, s45, 0xc000
	ds_read_b128 v[182:185], v196
	ds_read_b128 v[186:189], v196 offset:1024
	ds_read_b128 v[200:203], v196 offset:2048
	ds_read_b128 v[204:207], v196 offset:3072
	ds_read_b128 v[208:211], v196 offset:4096
	ds_read_b128 v[212:215], v196 offset:5120
	ds_read_b128 v[216:219], v196 offset:6144
	ds_read_b128 v[220:223], v196 offset:7168
	global_load_lds_dwordx4 v[224:225], off
	v_lshl_add_u64 v[224:225], s[70:71], 0, v[176:177]
	s_add_i32 m0, s45, 0xe000
	s_nop 0
	global_load_lds_dwordx4 v[224:225], off
	s_waitcnt vmcnt(8)
	s_waitcnt lgkmcnt(0)
	s_barrier
	s_setprio 3
	s_waitcnt lgkmcnt(0)
	v_mfma_scale_f32_16x16x128_f8f6f4 v[158:161], v[18:25], v[182:189], 0, v197, v197 op_sel_hi:[0, 0, 0]
	v_mfma_scale_f32_16x16x128_f8f6f4 v[154:157], v[26:33], v[182:189], 0, v197, v197 op_sel_hi:[0, 0, 0]
	v_mfma_scale_f32_16x16x128_f8f6f4 v[150:153], v[18:25], v[200:207], 0, v197, v197 op_sel_hi:[0, 0, 0]
	v_mfma_scale_f32_16x16x128_f8f6f4 v[142:145], v[26:33], v[200:207], 0, v197, v197 op_sel_hi:[0, 0, 0]
	v_mfma_scale_f32_16x16x128_f8f6f4 v[130:133], v[18:25], v[208:215], 0, v197, v197 op_sel_hi:[0, 0, 0]
	v_mfma_scale_f32_16x16x128_f8f6f4 v[122:125], v[26:33], v[208:215], 0, v197, v197 op_sel_hi:[0, 0, 0]
	v_mfma_scale_f32_16x16x128_f8f6f4 v[118:121], v[18:25], v[216:223], 0, v197, v197 op_sel_hi:[0, 0, 0]
	v_mfma_scale_f32_16x16x128_f8f6f4 v[110:113], v[26:33], v[216:223], 0, v197, v197 op_sel_hi:[0, 0, 0]
	s_setprio 0
	s_setprio 3
	v_mfma_scale_f32_16x16x128_f8f6f4 v[146:149], v[2:9], v[182:189], 0, v197, v197 op_sel_hi:[0, 0, 0]
	v_mfma_scale_f32_16x16x128_f8f6f4 v[138:141], v[10:17], v[182:189], 0, v197, v197 op_sel_hi:[0, 0, 0]
	v_mfma_scale_f32_16x16x128_f8f6f4 v[134:137], v[2:9], v[200:207], 0, v197, v197 op_sel_hi:[0, 0, 0]
	v_mfma_scale_f32_16x16x128_f8f6f4 v[126:129], v[10:17], v[200:207], 0, v197, v197 op_sel_hi:[0, 0, 0]
	v_mfma_scale_f32_16x16x128_f8f6f4 v[114:117], v[2:9], v[208:215], 0, v197, v197 op_sel_hi:[0, 0, 0]
	v_mfma_scale_f32_16x16x128_f8f6f4 v[106:109], v[10:17], v[208:215], 0, v197, v197 op_sel_hi:[0, 0, 0]
	v_mfma_scale_f32_16x16x128_f8f6f4 v[102:105], v[2:9], v[216:223], 0, v197, v197 op_sel_hi:[0, 0, 0]
	v_mfma_scale_f32_16x16x128_f8f6f4 v[98:101], v[10:17], v[216:223], 0, v197, v197 op_sel_hi:[0, 0, 0]
	s_setprio 0
	s_barrier
	s_add_i32 s0, s87, s76
	v_lshl_add_u64 v[182:183], s[72:73], 0, v[170:171]
	s_mov_b32 m0, s0
	ds_read_b128 v[200:203], v196 offset:16384
	ds_read_b128 v[204:207], v196 offset:17408
	ds_read_b128 v[208:211], v196 offset:18432
	ds_read_b128 v[212:215], v196 offset:19456
	ds_read_b128 v[216:219], v196 offset:20480
	ds_read_b128 v[220:223], v196 offset:21504
	ds_read_b128 v[224:227], v196 offset:22528
	ds_read_b128 v[228:231], v196 offset:23552
	global_load_lds_dwordx4 v[182:183], off
	s_add_i32 m0, s0, 0x2000
	s_add_u32 s4, s72, 0x20000
	v_lshl_add_u64 v[184:185], s[72:73], 0, v[166:167]
	s_addc_u32 s5, s73, 0
	s_add_i32 s0, s88, s76
	global_load_lds_dwordx4 v[184:185], off
	v_lshl_add_u64 v[186:187], s[4:5], 0, v[170:171]
	s_mov_b32 m0, s0
	v_lshl_add_u64 v[188:189], s[74:75], 0, v[168:169]
	global_load_lds_dwordx4 v[186:187], off
	v_lshl_add_u64 v[186:187], s[4:5], 0, v[166:167]
	s_add_i32 m0, s0, 0x2000
	s_nop 0
	global_load_lds_dwordx4 v[186:187], off
	v_lshl_add_u64 v[186:187], s[74:75], 0, v[172:173]
	s_mov_b32 m0, s45
	s_nop 0
	global_load_lds_dwordx4 v[186:187], off
	s_mov_b32 m0, s82
	s_nop 0
	global_load_lds_dwordx4 v[188:189], off
	s_waitcnt vmcnt(8)
	s_waitcnt lgkmcnt(0)
	s_barrier
	s_setprio 3
	s_waitcnt lgkmcnt(0)
	v_mfma_scale_f32_16x16x128_f8f6f4 v[94:97], v[18:25], v[200:207], 0, v197, v197 op_sel_hi:[0, 0, 0]
	v_mfma_scale_f32_16x16x128_f8f6f4 v[90:93], v[26:33], v[200:207], 0, v197, v197 op_sel_hi:[0, 0, 0]
	v_mfma_scale_f32_16x16x128_f8f6f4 v[86:89], v[18:25], v[208:215], 0, v197, v197 op_sel_hi:[0, 0, 0]
	v_mfma_scale_f32_16x16x128_f8f6f4 v[82:85], v[26:33], v[208:215], 0, v197, v197 op_sel_hi:[0, 0, 0]
	v_mfma_scale_f32_16x16x128_f8f6f4 v[70:73], v[18:25], v[216:223], 0, v197, v197 op_sel_hi:[0, 0, 0]
	v_mfma_scale_f32_16x16x128_f8f6f4 v[66:69], v[26:33], v[216:223], 0, v197, v197 op_sel_hi:[0, 0, 0]
	v_mfma_scale_f32_16x16x128_f8f6f4 v[54:57], v[18:25], v[224:231], 0, v197, v197 op_sel_hi:[0, 0, 0]
	v_mfma_scale_f32_16x16x128_f8f6f4 v[50:53], v[26:33], v[224:231], 0, v197, v197 op_sel_hi:[0, 0, 0]
	s_setprio 0
	s_setprio 3
	v_mfma_scale_f32_16x16x128_f8f6f4 v[78:81], v[2:9], v[200:207], 0, v197, v197 op_sel_hi:[0, 0, 0]
	v_mfma_scale_f32_16x16x128_f8f6f4 v[74:77], v[10:17], v[200:207], 0, v197, v197 op_sel_hi:[0, 0, 0]
	v_mfma_scale_f32_16x16x128_f8f6f4 v[62:65], v[2:9], v[208:215], 0, v197, v197 op_sel_hi:[0, 0, 0]
	v_mfma_scale_f32_16x16x128_f8f6f4 v[58:61], v[10:17], v[208:215], 0, v197, v197 op_sel_hi:[0, 0, 0]
	v_mfma_scale_f32_16x16x128_f8f6f4 v[46:49], v[2:9], v[216:223], 0, v197, v197 op_sel_hi:[0, 0, 0]
	v_mfma_scale_f32_16x16x128_f8f6f4 v[42:45], v[10:17], v[216:223], 0, v197, v197 op_sel_hi:[0, 0, 0]
	v_mfma_scale_f32_16x16x128_f8f6f4 v[38:41], v[2:9], v[224:231], 0, v197, v197 op_sel_hi:[0, 0, 0]
	v_mfma_scale_f32_16x16x128_f8f6f4 v[34:37], v[10:17], v[224:231], 0, v197, v197 op_sel_hi:[0, 0, 0]
	s_setprio 0
	s_barrier
; #define PG8_STAGE(bufoff, gbase, voff) do { _Pragma("unroll") for (int _i = 0; _i < 2; ++_i) \
;         __builtin_amdgcn_global_load_lds((const unsigned*)((const char*)(gbase) + (voff)[_i]), (PG8_LAS unsigned*)(lds + (bufoff) + ldsw + _i * 8192), 16, 0, 0); } while (0)
; #define PG8_LDA(dst, b, h) do { _Pragma("unroll") for (int m = 0; m < 4; ++m) Frag<F8>::load(dst[m], lds + PG8_SA(b, h) + aoff + m * 2048); } while (0)
; #define PG8_LDB(dst, b, h) do { _Pragma("unroll") for (int n = 0; n < 2; ++n) Frag<F8>::load(dst[n], lds + PG8_SB(b, h) + boff + n * 2048); } while (0)
; #define PG8_MMA(ai, bj, At, Bt) do { __builtin_amdgcn_s_setprio(3); _Pragma("unroll") for (int m = 0; m < 4; ++m) _Pragma("unroll") for (int n = 0; n < 2; ++n) Frag<F8>::mma(acc[ai][bj][m][n], Bt[n], At[m]); \
;         __builtin_amdgcn_s_setprio(0); } while (0)
; #define PG8_WAIT_V(n) asm volatile("s_waitcnt vmcnt(" #n ")" ::: "memory")
; #define PG8_WAIT_L(n) asm volatile("s_waitcnt lgkmcnt(" #n ")" ::: "memory")
; #define PG8_BAR __builtin_amdgcn_s_barrier()
; #define PG8_SCHED __builtin_amdgcn_sched_barrier(0)
; template <class Epi, class Sched, bool ALIGN_EPI = false, bool SP2 = false, bool F8 = false>
; __device__ __forceinline__ void gemm_phase(PG8_LAS unsigned char* lds, const Gemm g, const Sched& S, const Epi& E) {
;     ...
;             PG8_LDB(B0, 1, 0); PG8_LDB(B1, 1, 1); PG8_SCHED; PG8_LDA(At, 1, 0); PG8_STAGE(PG8_SA(0, 1), a2 + hstep, voffA);
;             PG8_WAIT_V(8); PG8_WAIT_L(0); PG8_BAR; PG8_MMA(0, 0, At, B0); PG8_MMA(0, 1, At, B1); PG8_BAR; PG8_SCHED;
;             PG8_LDA(At, 1, 1); PG8_STAGE(PG8_SB(1, 0), b3, voffB); PG8_STAGE(PG8_SB(1, 1), b3 + hstep, voffB); PG8_STAGE(PG8_SA(1, 0), a3, voffA);
;             PG8_WAIT_V(8); PG8_WAIT_L(0); PG8_BAR; PG8_MMA(1, 0, At, B0); PG8_MMA(1, 1, At, B1); PG8_BAR; PG8_SCHED;
	s_add_i32 s0, 0, 0x18000
	s_add_i32 s1, 0, 0x1c000
	v_add_u32_e32 v14, s0, v190
	v_add_u32_e32 v30, s1, v190
	ds_read_b128 v[2:5], v14
	ds_read_b128 v[6:9], v14 offset:1024
	ds_read_b128 v[10:13], v14 offset:2048
	ds_read_b128 v[14:17], v14 offset:3072
	ds_read_b128 v[18:21], v30
	ds_read_b128 v[22:25], v30 offset:1024
	ds_read_b128 v[26:29], v30 offset:2048
	ds_read_b128 v[30:33], v30 offset:3072
	s_add_u32 s4, s74, 0x20000
	s_addc_u32 s5, s75, 0
	s_mov_b32 m0, s83
	v_lshl_add_u64 v[232:233], s[4:5], 0, v[172:173]
	ds_read_b128 v[200:203], v196 offset:32768
	ds_read_b128 v[204:207], v196 offset:33792
	ds_read_b128 v[208:211], v196 offset:34816
	ds_read_b128 v[212:215], v196 offset:35840
	ds_read_b128 v[216:219], v196 offset:36864
	ds_read_b128 v[220:223], v196 offset:37888
	ds_read_b128 v[224:227], v196 offset:38912
	ds_read_b128 v[228:231], v196 offset:39936
	global_load_lds_dwordx4 v[232:233], off
	v_lshl_add_u64 v[232:233], s[4:5], 0, v[168:169]
	s_mov_b32 m0, s84
	s_nop 0
	global_load_lds_dwordx4 v[232:233], off
	s_waitcnt vmcnt(8)
	s_waitcnt lgkmcnt(0)
	s_barrier
	s_setprio 3
	s_waitcnt lgkmcnt(0)
	v_mfma_scale_f32_16x16x128_f8f6f4 v[158:161], v[2:9], v[200:207], v[158:161], v197, v197 op_sel_hi:[0,0,0]
	v_mfma_scale_f32_16x16x128_f8f6f4 v[154:157], v[10:17], v[200:207], v[154:157], v197, v197 op_sel_hi:[0,0,0]
	v_mfma_scale_f32_16x16x128_f8f6f4 v[150:153], v[2:9], v[208:215], v[150:153], v197, v197 op_sel_hi:[0,0,0]
	v_mfma_scale_f32_16x16x128_f8f6f4 v[142:145], v[10:17], v[208:215], v[142:145], v197, v197 op_sel_hi:[0,0,0]
	v_mfma_scale_f32_16x16x128_f8f6f4 v[130:133], v[2:9], v[216:223], v[130:133], v197, v197 op_sel_hi:[0,0,0]
	v_mfma_scale_f32_16x16x128_f8f6f4 v[122:125], v[10:17], v[216:223], v[122:125], v197, v197 op_sel_hi:[0,0,0]
	v_mfma_scale_f32_16x16x128_f8f6f4 v[118:121], v[2:9], v[224:231], v[118:121], v197, v197 op_sel_hi:[0,0,0]
	v_mfma_scale_f32_16x16x128_f8f6f4 v[110:113], v[10:17], v[224:231], v[110:113], v197, v197 op_sel_hi:[0,0,0]
	s_setprio 0
	s_setprio 3
	v_mfma_scale_f32_16x16x128_f8f6f4 v[146:149], v[18:25], v[200:207], v[146:149], v197, v197 op_sel_hi:[0,0,0]
	v_mfma_scale_f32_16x16x128_f8f6f4 v[138:141], v[26:33], v[200:207], v[138:141], v197, v197 op_sel_hi:[0,0,0]
	v_mfma_scale_f32_16x16x128_f8f6f4 v[134:137], v[18:25], v[208:215], v[134:137], v197, v197 op_sel_hi:[0,0,0]
	v_mfma_scale_f32_16x16x128_f8f6f4 v[126:129], v[26:33], v[208:215], v[126:129], v197, v197 op_sel_hi:[0,0,0]
	v_mfma_scale_f32_16x16x128_f8f6f4 v[114:117], v[18:25], v[216:223], v[114:117], v197, v197 op_sel_hi:[0,0,0]
	v_mfma_scale_f32_16x16x128_f8f6f4 v[106:109], v[26:33], v[216:223], v[106:109], v197, v197 op_sel_hi:[0,0,0]
	v_mfma_scale_f32_16x16x128_f8f6f4 v[102:105], v[18:25], v[224:231], v[102:105], v197, v197 op_sel_hi:[0,0,0]
	v_mfma_scale_f32_16x16x128_f8f6f4 v[98:101], v[26:33], v[224:231], v[98:101], v197, v197 op_sel_hi:[0,0,0]
	s_setprio 0
	s_barrier
	s_add_i32 s0, s0, s76
	v_lshl_add_u64 v[182:183], v[182:183], 0, s[18:19]
	s_mov_b32 m0, s0
	ds_read_b128 v[200:203], v196 offset:49152
	ds_read_b128 v[204:207], v196 offset:50176
	ds_read_b128 v[208:211], v196 offset:51200
	ds_read_b128 v[212:215], v196 offset:52224
	ds_read_b128 v[216:219], v196 offset:53248
	ds_read_b128 v[220:223], v196 offset:54272
	ds_read_b128 v[224:227], v196 offset:55296
	ds_read_b128 v[228:231], v196 offset:56320
	global_load_lds_dwordx4 v[182:183], off
	s_add_i32 m0, s0, 0x2000
	s_add_u32 s4, s72, 0x20080
	v_lshl_add_u64 v[182:183], v[184:185], 0, s[18:19]
	s_addc_u32 s5, s73, 0
	s_add_i32 s0, s1, s76
	global_load_lds_dwordx4 v[182:183], off
	v_lshl_add_u64 v[182:183], s[4:5], 0, v[170:171]
	s_mov_b32 m0, s0
	s_nop 0
	global_load_lds_dwordx4 v[182:183], off
	v_lshl_add_u64 v[182:183], s[4:5], 0, v[166:167]
	s_add_i32 m0, s0, 0x2000
	s_nop 0
	global_load_lds_dwordx4 v[182:183], off
	v_lshl_add_u64 v[182:183], v[186:187], 0, s[18:19]
	s_mov_b32 m0, s85
	s_nop 0
	global_load_lds_dwordx4 v[182:183], off
	v_lshl_add_u64 v[182:183], v[188:189], 0, s[18:19]
	s_mov_b32 m0, s86
	s_nop 0
	global_load_lds_dwordx4 v[182:183], off
	s_waitcnt vmcnt(8)
	s_waitcnt lgkmcnt(0)
	s_barrier
	s_setprio 3
	s_waitcnt lgkmcnt(0)
	v_mfma_scale_f32_16x16x128_f8f6f4 v[94:97], v[2:9], v[200:207], v[94:97], v197, v197 op_sel_hi:[0,0,0]
	v_mfma_scale_f32_16x16x128_f8f6f4 v[90:93], v[10:17], v[200:207], v[90:93], v197, v197 op_sel_hi:[0,0,0]
	v_mfma_scale_f32_16x16x128_f8f6f4 v[86:89], v[2:9], v[208:215], v[86:89], v197, v197 op_sel_hi:[0,0,0]
	v_mfma_scale_f32_16x16x128_f8f6f4 v[82:85], v[10:17], v[208:215], v[82:85], v197, v197 op_sel_hi:[0,0,0]
	v_mfma_scale_f32_16x16x128_f8f6f4 v[70:73], v[2:9], v[216:223], v[70:73], v197, v197 op_sel_hi:[0,0,0]
	v_mfma_scale_f32_16x16x128_f8f6f4 v[66:69], v[10:17], v[216:223], v[66:69], v197, v197 op_sel_hi:[0,0,0]
	v_mfma_scale_f32_16x16x128_f8f6f4 v[54:57], v[2:9], v[224:231], v[54:57], v197, v197 op_sel_hi:[0,0,0]
	v_mfma_scale_f32_16x16x128_f8f6f4 v[50:53], v[10:17], v[224:231], v[50:53], v197, v197 op_sel_hi:[0,0,0]
	s_setprio 0
	s_setprio 3
	v_mfma_scale_f32_16x16x128_f8f6f4 v[78:81], v[18:25], v[200:207], v[78:81], v197, v197 op_sel_hi:[0,0,0]
	v_mfma_scale_f32_16x16x128_f8f6f4 v[74:77], v[26:33], v[200:207], v[74:77], v197, v197 op_sel_hi:[0,0,0]
	v_mfma_scale_f32_16x16x128_f8f6f4 v[62:65], v[18:25], v[208:215], v[62:65], v197, v197 op_sel_hi:[0,0,0]
	v_mfma_scale_f32_16x16x128_f8f6f4 v[58:61], v[26:33], v[208:215], v[58:61], v197, v197 op_sel_hi:[0,0,0]
	v_mfma_scale_f32_16x16x128_f8f6f4 v[46:49], v[18:25], v[216:223], v[46:49], v197, v197 op_sel_hi:[0,0,0]
	v_mfma_scale_f32_16x16x128_f8f6f4 v[42:45], v[26:33], v[216:223], v[42:45], v197, v197 op_sel_hi:[0,0,0]
	v_mfma_scale_f32_16x16x128_f8f6f4 v[38:41], v[18:25], v[224:231], v[38:41], v197, v197 op_sel_hi:[0,0,0]
	v_mfma_scale_f32_16x16x128_f8f6f4 v[34:37], v[26:33], v[224:231], v[34:37], v197, v197 op_sel_hi:[0,0,0]
	s_setprio 0
	s_add_i32 s96, s96, 2
	s_add_u32 s70, s70, 0x100
	s_addc_u32 s71, s71, 0
	s_add_u32 s93, s93, 0x100
	s_addc_u32 s95, s95, 0
	s_cmp_gt_u32 s96, 5
	s_cbranch_scc1 .Lpeel_exit_0
; #define PG8_STAGE(bufoff, gbase, voff) do { _Pragma("unroll") for (int _i = 0; _i < 2; ++_i) \
;         __builtin_amdgcn_global_load_lds((const unsigned*)((const char*)(gbase) + (voff)[_i]), (PG8_LAS unsigned*)(lds + (bufoff) + ldsw + _i * 8192), 16, 0, 0); } while (0)
; #define PG8_LDA(dst, b, h) do { _Pragma("unroll") for (int m = 0; m < 4; ++m) Frag<F8>::load(dst[m], lds + PG8_SA(b, h) + aoff + m * 2048); } while (0)
; #define PG8_LDB(dst, b, h) do { _Pragma("unroll") for (int n = 0; n < 2; ++n) Frag<F8>::load(dst[n], lds + PG8_SB(b, h) + boff + n * 2048); } while (0)
; #define PG8_MMA(ai, bj, At, Bt) do { __builtin_amdgcn_s_setprio(3); _Pragma("unroll") for (int m = 0; m < 4; ++m) _Pragma("unroll") for (int n = 0; n < 2; ++n) Frag<F8>::mma(acc[ai][bj][m][n], Bt[n], At[m]); \
;         __builtin_amdgcn_s_setprio(0); } while (0)
; #define PG8_WAIT_V(n) asm volatile("s_waitcnt vmcnt(" #n ")" ::: "memory")
; #define PG8_WAIT_L(n) asm volatile("s_waitcnt lgkmcnt(" #n ")" ::: "memory")
; #define PG8_BAR __builtin_amdgcn_s_barrier()
; #define PG8_SCHED __builtin_amdgcn_sched_barrier(0)
; template <class Epi, class Sched, bool ALIGN_EPI = false, bool SP2 = false, bool F8 = false>
; __device__ __forceinline__ void gemm_phase(PG8_LAS unsigned char* lds, const Gemm g, const Sched& S, const Epi& E) {
;     ...
;             PG8_LDB(B0, 0, 0); PG8_LDB(B1, 0, 1); PG8_SCHED; PG8_LDA(At, 0, 0); PG8_STAGE(PG8_SA(1, 1), a1 + hstep, voffA);
;             PG8_WAIT_V(8); PG8_WAIT_L(0); PG8_BAR; PG8_MMA(0, 0, At, B0); PG8_MMA(0, 1, At, B1); PG8_BAR; PG8_SCHED;
;             PG8_LDA(At, 0, 1); PG8_STAGE(PG8_SB(0, 0), b2, voffB); PG8_STAGE(PG8_SB(0, 1), b2 + hstep, voffB); PG8_STAGE(PG8_SA(0, 0), a2, voffA);
;             PG8_WAIT_V(8); PG8_WAIT_L(0); PG8_BAR; PG8_MMA(1, 0, At, B0); PG8_MMA(1, 1, At, B1); PG8_BAR; PG8_SCHED;
.LBB0_151:
	s_barrier
	ds_read_b128 v[18:21], v194
	ds_read_b128 v[22:25], v194 offset:1024
	ds_read_b128 v[26:29], v194 offset:2048
	ds_read_b128 v[30:33], v194 offset:3072
	ds_read_b128 v[2:5], v195
	ds_read_b128 v[6:9], v195 offset:1024
	ds_read_b128 v[10:13], v195 offset:2048
	ds_read_b128 v[14:17], v195 offset:3072
	s_add_u32 s0, s70, 0xfffe0080
	s_addc_u32 s1, s71, -1
	s_cmp_eq_u32 s96, 4
	s_cselect_b32 s75, s25, s1
	s_cselect_b32 s74, s91, s0
	s_cselect_b32 s73, s31, s95
	s_cselect_b32 s72, s92, s93
	v_lshl_add_u64 v[224:225], s[70:71], 0, v[174:175]
	s_add_i32 m0, s45, 0xc000
	ds_read_b128 v[182:185], v196
	ds_read_b128 v[186:189], v196 offset:1024
	ds_read_b128 v[200:203], v196 offset:2048
	ds_read_b128 v[204:207], v196 offset:3072
	ds_read_b128 v[208:211], v196 offset:4096
	ds_read_b128 v[212:215], v196 offset:5120
	ds_read_b128 v[216:219], v196 offset:6144
	ds_read_b128 v[220:223], v196 offset:7168
	global_load_lds_dwordx4 v[224:225], off
	v_lshl_add_u64 v[224:225], s[70:71], 0, v[176:177]
	s_add_i32 m0, s45, 0xe000
	s_nop 0
	global_load_lds_dwordx4 v[224:225], off
	s_waitcnt vmcnt(8)
	s_waitcnt lgkmcnt(0)
	s_barrier
	s_setprio 3
	s_waitcnt lgkmcnt(0)
	v_mfma_scale_f32_16x16x128_f8f6f4 v[158:161], v[18:25], v[182:189], v[158:161], v197, v197 op_sel_hi:[0,0,0]
	v_mfma_scale_f32_16x16x128_f8f6f4 v[154:157], v[26:33], v[182:189], v[154:157], v197, v197 op_sel_hi:[0,0,0]
	v_mfma_scale_f32_16x16x128_f8f6f4 v[150:153], v[18:25], v[200:207], v[150:153], v197, v197 op_sel_hi:[0,0,0]
	v_mfma_scale_f32_16x16x128_f8f6f4 v[142:145], v[26:33], v[200:207], v[142:145], v197, v197 op_sel_hi:[0,0,0]
	v_mfma_scale_f32_16x16x128_f8f6f4 v[130:133], v[18:25], v[208:215], v[130:133], v197, v197 op_sel_hi:[0,0,0]
	v_mfma_scale_f32_16x16x128_f8f6f4 v[122:125], v[26:33], v[208:215], v[122:125], v197, v197 op_sel_hi:[0,0,0]
	v_mfma_scale_f32_16x16x128_f8f6f4 v[118:121], v[18:25], v[216:223], v[118:121], v197, v197 op_sel_hi:[0,0,0]
	v_mfma_scale_f32_16x16x128_f8f6f4 v[110:113], v[26:33], v[216:223], v[110:113], v197, v197 op_sel_hi:[0,0,0]
	s_setprio 0
	s_setprio 3
	v_mfma_scale_f32_16x16x128_f8f6f4 v[146:149], v[2:9], v[182:189], v[146:149], v197, v197 op_sel_hi:[0,0,0]
	v_mfma_scale_f32_16x16x128_f8f6f4 v[138:141], v[10:17], v[182:189], v[138:141], v197, v197 op_sel_hi:[0,0,0]
	v_mfma_scale_f32_16x16x128_f8f6f4 v[134:137], v[2:9], v[200:207], v[134:137], v197, v197 op_sel_hi:[0,0,0]
	v_mfma_scale_f32_16x16x128_f8f6f4 v[126:129], v[10:17], v[200:207], v[126:129], v197, v197 op_sel_hi:[0,0,0]
	v_mfma_scale_f32_16x16x128_f8f6f4 v[114:117], v[2:9], v[208:215], v[114:117], v197, v197 op_sel_hi:[0,0,0]
	v_mfma_scale_f32_16x16x128_f8f6f4 v[106:109], v[10:17], v[208:215], v[106:109], v197, v197 op_sel_hi:[0,0,0]
	v_mfma_scale_f32_16x16x128_f8f6f4 v[102:105], v[2:9], v[216:223], v[102:105], v197, v197 op_sel_hi:[0,0,0]
	v_mfma_scale_f32_16x16x128_f8f6f4 v[98:101], v[10:17], v[216:223], v[98:101], v197, v197 op_sel_hi:[0,0,0]
	s_setprio 0
	s_barrier
	s_add_i32 s0, s87, s76
	v_lshl_add_u64 v[182:183], s[72:73], 0, v[170:171]
	s_mov_b32 m0, s0
	ds_read_b128 v[200:203], v196 offset:16384
	ds_read_b128 v[204:207], v196 offset:17408
	ds_read_b128 v[208:211], v196 offset:18432
	ds_read_b128 v[212:215], v196 offset:19456
	ds_read_b128 v[216:219], v196 offset:20480
	ds_read_b128 v[220:223], v196 offset:21504
	ds_read_b128 v[224:227], v196 offset:22528
	ds_read_b128 v[228:231], v196 offset:23552
	global_load_lds_dwordx4 v[182:183], off
	s_add_i32 m0, s0, 0x2000
	s_add_u32 s4, s72, 0x20000
	v_lshl_add_u64 v[184:185], s[72:73], 0, v[166:167]
	s_addc_u32 s5, s73, 0
	s_add_i32 s0, s88, s76
	global_load_lds_dwordx4 v[184:185], off
	v_lshl_add_u64 v[186:187], s[4:5], 0, v[170:171]
	s_mov_b32 m0, s0
	v_lshl_add_u64 v[188:189], s[74:75], 0, v[168:169]
	global_load_lds_dwordx4 v[186:187], off
	v_lshl_add_u64 v[186:187], s[4:5], 0, v[166:167]
	s_add_i32 m0, s0, 0x2000
	s_nop 0
	global_load_lds_dwordx4 v[186:187], off
	v_lshl_add_u64 v[186:187], s[74:75], 0, v[172:173]
	s_mov_b32 m0, s45
	s_nop 0
	global_load_lds_dwordx4 v[186:187], off
	s_mov_b32 m0, s82
	s_nop 0
	global_load_lds_dwordx4 v[188:189], off
	s_waitcnt vmcnt(8)
	s_waitcnt lgkmcnt(0)
	s_barrier
	s_setprio 3
	s_waitcnt lgkmcnt(0)
	v_mfma_scale_f32_16x16x128_f8f6f4 v[94:97], v[18:25], v[200:207], v[94:97], v197, v197 op_sel_hi:[0,0,0]
	v_mfma_scale_f32_16x16x128_f8f6f4 v[90:93], v[26:33], v[200:207], v[90:93], v197, v197 op_sel_hi:[0,0,0]
	v_mfma_scale_f32_16x16x128_f8f6f4 v[86:89], v[18:25], v[208:215], v[86:89], v197, v197 op_sel_hi:[0,0,0]
	v_mfma_scale_f32_16x16x128_f8f6f4 v[82:85], v[26:33], v[208:215], v[82:85], v197, v197 op_sel_hi:[0,0,0]
	v_mfma_scale_f32_16x16x128_f8f6f4 v[70:73], v[18:25], v[216:223], v[70:73], v197, v197 op_sel_hi:[0,0,0]
	v_mfma_scale_f32_16x16x128_f8f6f4 v[66:69], v[26:33], v[216:223], v[66:69], v197, v197 op_sel_hi:[0,0,0]
	v_mfma_scale_f32_16x16x128_f8f6f4 v[54:57], v[18:25], v[224:231], v[54:57], v197, v197 op_sel_hi:[0,0,0]
	v_mfma_scale_f32_16x16x128_f8f6f4 v[50:53], v[26:33], v[224:231], v[50:53], v197, v197 op_sel_hi:[0,0,0]
	s_setprio 0
	s_setprio 3
	v_mfma_scale_f32_16x16x128_f8f6f4 v[78:81], v[2:9], v[200:207], v[78:81], v197, v197 op_sel_hi:[0,0,0]
	v_mfma_scale_f32_16x16x128_f8f6f4 v[74:77], v[10:17], v[200:207], v[74:77], v197, v197 op_sel_hi:[0,0,0]
	v_mfma_scale_f32_16x16x128_f8f6f4 v[62:65], v[2:9], v[208:215], v[62:65], v197, v197 op_sel_hi:[0,0,0]
	v_mfma_scale_f32_16x16x128_f8f6f4 v[58:61], v[10:17], v[208:215], v[58:61], v197, v197 op_sel_hi:[0,0,0]
	v_mfma_scale_f32_16x16x128_f8f6f4 v[46:49], v[2:9], v[216:223], v[46:49], v197, v197 op_sel_hi:[0,0,0]
	v_mfma_scale_f32_16x16x128_f8f6f4 v[42:45], v[10:17], v[216:223], v[42:45], v197, v197 op_sel_hi:[0,0,0]
	v_mfma_scale_f32_16x16x128_f8f6f4 v[38:41], v[2:9], v[224:231], v[38:41], v197, v197 op_sel_hi:[0,0,0]
	v_mfma_scale_f32_16x16x128_f8f6f4 v[34:37], v[10:17], v[224:231], v[34:37], v197, v197 op_sel_hi:[0,0,0]
	s_setprio 0
	s_barrier
; #define PG8_STAGE(bufoff, gbase, voff) do { _Pragma("unroll") for (int _i = 0; _i < 2; ++_i) \
;         __builtin_amdgcn_global_load_lds((const unsigned*)((const char*)(gbase) + (voff)[_i]), (PG8_LAS unsigned*)(lds + (bufoff) + ldsw + _i * 8192), 16, 0, 0); } while (0)
; #define PG8_LDA(dst, b, h) do { _Pragma("unroll") for (int m = 0; m < 4; ++m) Frag<F8>::load(dst[m], lds + PG8_SA(b, h) + aoff + m * 2048); } while (0)
; #define PG8_LDB(dst, b, h) do { _Pragma("unroll") for (int n = 0; n < 2; ++n) Frag<F8>::load(dst[n], lds + PG8_SB(b, h) + boff + n * 2048); } while (0)
; #define PG8_WAIT_V(n) asm volatile("s_waitcnt vmcnt(" #n ")" ::: "memory")
; #define PG8_BAR __builtin_amdgcn_s_barrier()
; template <class Epi, class Sched, bool ALIGN_EPI = false, bool SP2 = false, bool F8 = false>
; __device__ __forceinline__ void gemm_phase(PG8_LAS unsigned char* lds, const Gemm g, const Sched& S, const Epi& E) {
;     ...
;         for (int t = 0; t < nt; t += 2) {
;             const bool last = (t == nt - 2);
;             const char* a1 = cA + (size_t)(t + 1) * kstep;
;             const char* a2 = last ? nA : cA + (size_t)(t + 2) * kstep; const char* b2 = last ? nB : cB + (size_t)(t + 2) * kstep;
;             const char* a3 = a2 + kstep; const char* b3 = b2 + kstep;
;             if (last && has_next) S.a_ready(nxt);
;             if constexpr (SP2) {
;             PG8_LDB(B0, 0, 0); PG8_LDB(B1, 0, 1); PG8_SCHED; PG8_LDA(At, 0, 0); PG8_STAGE(PG8_SA(1, 1), a1 + hstep, voffA);
;             PG8_WAIT_V(8); PG8_WAIT_L(0); PG8_BAR; PG8_MMA(0, 0, At, B0); PG8_MMA(0, 1, At, B1); PG8_BAR; PG8_SCHED;
;             PG8_LDA(At, 0, 1); PG8_STAGE(PG8_SB(0, 0), b2, voffB); PG8_STAGE(PG8_SB(0, 1), b2 + hstep, voffB); PG8_STAGE(PG8_SA(0, 0), a2, voffA);
;             PG8_WAIT_V(8); PG8_WAIT_L(0); PG8_BAR; PG8_MMA(1, 0, At, B0); PG8_MMA(1, 1, At, B1); PG8_BAR; PG8_SCHED;
;             PG8_LDB(B0, 1, 0); PG8_LDB(B1, 1, 1); PG8_SCHED; PG8_LDA(At, 1, 0); PG8_STAGE(PG8_SA(0, 1), a2 + hstep, voffA);
;             PG8_WAIT_V(8); PG8_WAIT_L(0); PG8_BAR; PG8_MMA(0, 0, At, B0); PG8_MMA(0, 1, At, B1); PG8_BAR; PG8_SCHED;
;             PG8_LDA(At, 1, 1); PG8_STAGE(PG8_SB(1, 0), b3, voffB); PG8_STAGE(PG8_SB(1, 1), b3 + hstep, voffB); PG8_STAGE(PG8_SA(1, 0), a3, voffA);
;             PG8_WAIT_V(8); PG8_WAIT_L(0); PG8_BAR; PG8_MMA(1, 0, At, B0); PG8_MMA(1, 1, At, B1); PG8_BAR; PG8_SCHED;
	s_add_i32 s0, 0, 0x18000
	s_add_i32 s1, 0, 0x1c000
	v_add_u32_e32 v14, s0, v190
	v_add_u32_e32 v30, s1, v190
	ds_read_b128 v[2:5], v14
	ds_read_b128 v[6:9], v14 offset:1024
	ds_read_b128 v[10:13], v14 offset:2048
	ds_read_b128 v[14:17], v14 offset:3072
	ds_read_b128 v[18:21], v30
	ds_read_b128 v[22:25], v30 offset:1024
	ds_read_b128 v[26:29], v30 offset:2048
	ds_read_b128 v[30:33], v30 offset:3072
	s_add_u32 s4, s74, 0x20000
	s_addc_u32 s5, s75, 0
	s_mov_b32 m0, s83
	v_lshl_add_u64 v[232:233], s[4:5], 0, v[172:173]
	ds_read_b128 v[200:203], v196 offset:32768
	ds_read_b128 v[204:207], v196 offset:33792
	ds_read_b128 v[208:211], v196 offset:34816
	ds_read_b128 v[212:215], v196 offset:35840
	ds_read_b128 v[216:219], v196 offset:36864
	ds_read_b128 v[220:223], v196 offset:37888
	ds_read_b128 v[224:227], v196 offset:38912
	ds_read_b128 v[228:231], v196 offset:39936
	global_load_lds_dwordx4 v[232:233], off
	v_lshl_add_u64 v[232:233], s[4:5], 0, v[168:169]
	s_mov_b32 m0, s84
	s_nop 0
	global_load_lds_dwordx4 v[232:233], off
	s_waitcnt vmcnt(8)
	s_waitcnt lgkmcnt(0)
	s_barrier
	s_setprio 3
	s_waitcnt lgkmcnt(0)
	v_mfma_scale_f32_16x16x128_f8f6f4 v[158:161], v[2:9], v[200:207], v[158:161], v197, v197 op_sel_hi:[0,0,0]
	v_mfma_scale_f32_16x16x128_f8f6f4 v[154:157], v[10:17], v[200:207], v[154:157], v197, v197 op_sel_hi:[0,0,0]
	v_mfma_scale_f32_16x16x128_f8f6f4 v[150:153], v[2:9], v[208:215], v[150:153], v197, v197 op_sel_hi:[0,0,0]
	v_mfma_scale_f32_16x16x128_f8f6f4 v[142:145], v[10:17], v[208:215], v[142:145], v197, v197 op_sel_hi:[0,0,0]
	v_mfma_scale_f32_16x16x128_f8f6f4 v[130:133], v[2:9], v[216:223], v[130:133], v197, v197 op_sel_hi:[0,0,0]
	v_mfma_scale_f32_16x16x128_f8f6f4 v[122:125], v[10:17], v[216:223], v[122:125], v197, v197 op_sel_hi:[0,0,0]
	v_mfma_scale_f32_16x16x128_f8f6f4 v[118:121], v[2:9], v[224:231], v[118:121], v197, v197 op_sel_hi:[0,0,0]
	v_mfma_scale_f32_16x16x128_f8f6f4 v[110:113], v[10:17], v[224:231], v[110:113], v197, v197 op_sel_hi:[0,0,0]
	s_setprio 0
	s_setprio 3
	v_mfma_scale_f32_16x16x128_f8f6f4 v[146:149], v[18:25], v[200:207], v[146:149], v197, v197 op_sel_hi:[0,0,0]
	v_mfma_scale_f32_16x16x128_f8f6f4 v[138:141], v[26:33], v[200:207], v[138:141], v197, v197 op_sel_hi:[0,0,0]
	v_mfma_scale_f32_16x16x128_f8f6f4 v[134:137], v[18:25], v[208:215], v[134:137], v197, v197 op_sel_hi:[0,0,0]
	v_mfma_scale_f32_16x16x128_f8f6f4 v[126:129], v[26:33], v[208:215], v[126:129], v197, v197 op_sel_hi:[0,0,0]
	v_mfma_scale_f32_16x16x128_f8f6f4 v[114:117], v[18:25], v[216:223], v[114:117], v197, v197 op_sel_hi:[0,0,0]
	v_mfma_scale_f32_16x16x128_f8f6f4 v[106:109], v[26:33], v[216:223], v[106:109], v197, v197 op_sel_hi:[0,0,0]
	v_mfma_scale_f32_16x16x128_f8f6f4 v[102:105], v[18:25], v[224:231], v[102:105], v197, v197 op_sel_hi:[0,0,0]
	v_mfma_scale_f32_16x16x128_f8f6f4 v[98:101], v[26:33], v[224:231], v[98:101], v197, v197 op_sel_hi:[0,0,0]
	s_setprio 0
	s_barrier
	s_add_i32 s0, s0, s76
	v_lshl_add_u64 v[182:183], v[182:183], 0, s[18:19]
	s_mov_b32 m0, s0
	ds_read_b128 v[200:203], v196 offset:49152
	ds_read_b128 v[204:207], v196 offset:50176
	ds_read_b128 v[208:211], v196 offset:51200
	ds_read_b128 v[212:215], v196 offset:52224
	ds_read_b128 v[216:219], v196 offset:53248
	ds_read_b128 v[220:223], v196 offset:54272
	ds_read_b128 v[224:227], v196 offset:55296
	ds_read_b128 v[228:231], v196 offset:56320
	global_load_lds_dwordx4 v[182:183], off
	s_add_i32 m0, s0, 0x2000
	s_add_u32 s4, s72, 0x20080
	v_lshl_add_u64 v[182:183], v[184:185], 0, s[18:19]
	s_addc_u32 s5, s73, 0
	s_add_i32 s0, s1, s76
	global_load_lds_dwordx4 v[182:183], off
	v_lshl_add_u64 v[182:183], s[4:5], 0, v[170:171]
	s_mov_b32 m0, s0
	s_nop 0
	global_load_lds_dwordx4 v[182:183], off
	v_lshl_add_u64 v[182:183], s[4:5], 0, v[166:167]
	s_add_i32 m0, s0, 0x2000
	s_nop 0
	global_load_lds_dwordx4 v[182:183], off
	v_lshl_add_u64 v[182:183], v[186:187], 0, s[18:19]
	s_mov_b32 m0, s85
	s_nop 0
	global_load_lds_dwordx4 v[182:183], off
	v_lshl_add_u64 v[182:183], v[188:189], 0, s[18:19]
	s_mov_b32 m0, s86
	s_nop 0
	global_load_lds_dwordx4 v[182:183], off
	s_waitcnt vmcnt(8)
	s_waitcnt lgkmcnt(0)
	s_barrier
	s_setprio 3
	s_waitcnt lgkmcnt(0)
	v_mfma_scale_f32_16x16x128_f8f6f4 v[94:97], v[2:9], v[200:207], v[94:97], v197, v197 op_sel_hi:[0,0,0]
	v_mfma_scale_f32_16x16x128_f8f6f4 v[90:93], v[10:17], v[200:207], v[90:93], v197, v197 op_sel_hi:[0,0,0]
	v_mfma_scale_f32_16x16x128_f8f6f4 v[86:89], v[2:9], v[208:215], v[86:89], v197, v197 op_sel_hi:[0,0,0]
	v_mfma_scale_f32_16x16x128_f8f6f4 v[82:85], v[10:17], v[208:215], v[82:85], v197, v197 op_sel_hi:[0,0,0]
	v_mfma_scale_f32_16x16x128_f8f6f4 v[70:73], v[2:9], v[216:223], v[70:73], v197, v197 op_sel_hi:[0,0,0]
	v_mfma_scale_f32_16x16x128_f8f6f4 v[66:69], v[10:17], v[216:223], v[66:69], v197, v197 op_sel_hi:[0,0,0]
	v_mfma_scale_f32_16x16x128_f8f6f4 v[54:57], v[2:9], v[224:231], v[54:57], v197, v197 op_sel_hi:[0,0,0]
	v_mfma_scale_f32_16x16x128_f8f6f4 v[50:53], v[10:17], v[224:231], v[50:53], v197, v197 op_sel_hi:[0,0,0]
	s_setprio 0
	s_setprio 3
	v_mfma_scale_f32_16x16x128_f8f6f4 v[78:81], v[18:25], v[200:207], v[78:81], v197, v197 op_sel_hi:[0,0,0]
	v_mfma_scale_f32_16x16x128_f8f6f4 v[74:77], v[26:33], v[200:207], v[74:77], v197, v197 op_sel_hi:[0,0,0]
	v_mfma_scale_f32_16x16x128_f8f6f4 v[62:65], v[18:25], v[208:215], v[62:65], v197, v197 op_sel_hi:[0,0,0]
	v_mfma_scale_f32_16x16x128_f8f6f4 v[58:61], v[26:33], v[208:215], v[58:61], v197, v197 op_sel_hi:[0,0,0]
	v_mfma_scale_f32_16x16x128_f8f6f4 v[46:49], v[18:25], v[216:223], v[46:49], v197, v197 op_sel_hi:[0,0,0]
	v_mfma_scale_f32_16x16x128_f8f6f4 v[42:45], v[26:33], v[216:223], v[42:45], v197, v197 op_sel_hi:[0,0,0]
	v_mfma_scale_f32_16x16x128_f8f6f4 v[38:41], v[18:25], v[224:231], v[38:41], v197, v197 op_sel_hi:[0,0,0]
	v_mfma_scale_f32_16x16x128_f8f6f4 v[34:37], v[26:33], v[224:231], v[34:37], v197, v197 op_sel_hi:[0,0,0]
	s_setprio 0
	s_add_i32 s96, s96, 2
	s_add_u32 s70, s70, 0x100
	s_addc_u32 s71, s71, 0
	s_add_u32 s93, s93, 0x100
	s_addc_u32 s95, s95, 0
	s_cmp_gt_u32 s96, 5
	s_cbranch_scc0 .LBB0_151

; __device__ __forceinline__ unsigned cvt_pk_bf16(float lo, float hi) { const f32x2 v = {lo, hi}; const bf16x2_t b = __builtin_convertvector(v, bf16x2_t); return __builtin_bit_cast(unsigned, b); }
; __device__ __forceinline__ unsigned long long rt() { return __builtin_amdgcn_s_memrealtime(); }
;     __device__ __forceinline__ void operator()(const f32x4 (&acc)[2][2][4][2], const Unit& u, int wr, int wc, int fr, int fq) const {
;         const int row0 = u.pm * BM + wr * 64 + fr, col0 = u.pn * BM + wc * 32 + 8 * fq;
;         const float sc0 = ((smask >> (2 * u.pn)) & 1u) ? sval : 1.0f, sc1 = ((smask >> (2 * u.pn + 1)) & 1u) ? sval : 1.0f;
; #pragma unroll
;         for (int ai = 0; ai < 2; ++ai)
; #pragma unroll
;             for (int m = 0; m < 4; ++m) { bf16_t* rowp = O + (size_t)(row0 + ai * HALF + m * 16) * ldc + col0;
;                 const float rs = rt ? rt[ai * HALF + wr * 64 + m * 16 + fr] : 1.0f;
; #pragma unroll
;                 for (int bj = 0; bj < 2; ++bj) { const float sc = (bj ? sc1 : sc0) * rs; const f32x4 v0 = acc[ai][bj][m][0] * sc, v1 = acc[ai][bj][m][1] * sc;
;                     u32x4 w; w.x = cvt_pk_bf16(v0[0], v0[1]); w.y = cvt_pk_bf16(v0[2], v0[3]); w.z = cvt_pk_bf16(v1[0], v1[1]); w.w = cvt_pk_bf16(v1[2], v1[3]);
;                     *(u32x4*)(rowp + bj * HALF) = w; } }
.LBB0_154:
	s_nop 15
	s_nop 15
	s_lshl_b32 s0, s90, 1
	s_lshl_b32 s1, 1, s0
	s_and_b32 s1, s1, 0x415
	s_cmp_eq_u32 s1, 0
	s_cselect_b64 s[4:5], -1, 0
	s_lshl_b32 s0, 2, s0
	ds_read2_b32 v[10:11], v191 offset1:16
	s_and_b32 s0, s0, 0x22a
	v_lshl_or_b32 v4, s90, 8, v193
	s_cmp_eq_u32 s0, 0
	v_lshl_add_u32 v20, s44, 8, v165
	v_cndmask_b32_e64 v21, v198, 1.0, s[4:5]
	s_cselect_b64 s[4:5], -1, 0
	v_ashrrev_i32_e32 v5, 31, v4
	v_mov_b64_e32 v[2:3], s[16:17]
	v_cndmask_b32_e64 v22, v198, 1.0, s[4:5]
	v_mad_i64_i32 v[6:7], s[4:5], v20, s89, v[2:3]
	v_lshlrev_b64 v[4:5], 1, v[4:5]
	v_lshl_add_u64 v[12:13], v[6:7], 0, v[4:5]
	s_waitcnt lgkmcnt(0)
	v_mul_f32_e32 v6, v21, v10
	v_pk_mul_f32 v[8:9], v[160:161], v[6:7] op_sel_hi:[1,0]
	v_pk_mul_f32 v[14:15], v[158:159], v[6:7] op_sel_hi:[1,0]
	v_pk_mul_f32 v[16:17], v[156:157], v[6:7] op_sel_hi:[1,0]
	v_pk_mul_f32 v[18:19], v[154:155], v[6:7] op_sel_hi:[1,0]
	v_cvt_pk_bf16_f32 v6, v14, v15
	v_cvt_pk_bf16_f32 v7, v8, v9
	v_cvt_pk_bf16_f32 v8, v18, v19
	v_cvt_pk_bf16_f32 v9, v16, v17
	global_store_dwordx4 v[12:13], v[6:9], off
	s_andn2_b64 vcc, exec, s[8:9]
	s_mov_b64 s[8:9], -1
	v_mul_f32_e32 v6, v22, v10
	v_pk_mul_f32 v[8:9], v[148:149], v[6:7] op_sel_hi:[1,0]
	v_pk_mul_f32 v[14:15], v[146:147], v[6:7] op_sel_hi:[1,0]
	v_pk_mul_f32 v[16:17], v[140:141], v[6:7] op_sel_hi:[1,0]
	v_pk_mul_f32 v[18:19], v[138:139], v[6:7] op_sel_hi:[1,0]
	v_cvt_pk_bf16_f32 v6, v14, v15
	v_cvt_pk_bf16_f32 v7, v8, v9
	v_cvt_pk_bf16_f32 v8, v18, v19
	v_cvt_pk_bf16_f32 v9, v16, v17
	global_store_dwordx4 v[12:13], v[6:9], off offset:256
	ds_read_b32 v23, v191 offset:704
	s_nop 0
	v_or_b32_e32 v6, 16, v20
	v_mad_i64_i32 v[6:7], s[4:5], v6, s89, v[2:3]
	v_lshl_add_u64 v[12:13], v[6:7], 0, v[4:5]
	v_mul_f32_e32 v6, v21, v11
	v_pk_mul_f32 v[8:9], v[152:153], v[6:7] op_sel_hi:[1,0]
	v_pk_mul_f32 v[14:15], v[150:151], v[6:7] op_sel_hi:[1,0]
	v_pk_mul_f32 v[16:17], v[144:145], v[6:7] op_sel_hi:[1,0]
	v_pk_mul_f32 v[18:19], v[142:143], v[6:7] op_sel_hi:[1,0]
	v_cvt_pk_bf16_f32 v6, v14, v15
	v_cvt_pk_bf16_f32 v7, v8, v9
	v_cvt_pk_bf16_f32 v8, v18, v19
	v_cvt_pk_bf16_f32 v9, v16, v17
	global_store_dwordx4 v[12:13], v[6:9], off
	s_nop 1
	v_mul_f32_e32 v6, v22, v11
	v_pk_mul_f32 v[10:11], v[134:135], v[6:7] op_sel_hi:[1,0]
	v_pk_mul_f32 v[8:9], v[136:137], v[6:7] op_sel_hi:[1,0]
	v_pk_mul_f32 v[14:15], v[128:129], v[6:7] op_sel_hi:[1,0]
	v_pk_mul_f32 v[16:17], v[126:127], v[6:7] op_sel_hi:[1,0]
	v_cvt_pk_bf16_f32 v6, v10, v11
	ds_read2_b32 v[10:11], v191 offset0:32 offset1:48
	v_cvt_pk_bf16_f32 v7, v8, v9
	v_cvt_pk_bf16_f32 v8, v16, v17
	v_cvt_pk_bf16_f32 v9, v14, v15
	global_store_dwordx4 v[12:13], v[6:9], off offset:256
	s_nop 1
	v_or_b32_e32 v6, 32, v20
	v_mad_i64_i32 v[6:7], s[4:5], v6, s89, v[2:3]
	v_lshl_add_u64 v[12:13], v[6:7], 0, v[4:5]
	s_waitcnt lgkmcnt(0)
	v_mul_f32_e32 v6, v21, v10
	v_pk_mul_f32 v[8:9], v[132:133], v[6:7] op_sel_hi:[1,0]
	v_pk_mul_f32 v[14:15], v[130:131], v[6:7] op_sel_hi:[1,0]
	v_pk_mul_f32 v[16:17], v[124:125], v[6:7] op_sel_hi:[1,0]
	v_pk_mul_f32 v[18:19], v[122:123], v[6:7] op_sel_hi:[1,0]
	v_cvt_pk_bf16_f32 v6, v14, v15
	v_cvt_pk_bf16_f32 v7, v8, v9
	v_cvt_pk_bf16_f32 v8, v18, v19
	v_cvt_pk_bf16_f32 v9, v16, v17
	global_store_dwordx4 v[12:13], v[6:9], off
	s_nop 1
	v_mul_f32_e32 v6, v22, v10
	v_pk_mul_f32 v[8:9], v[116:117], v[6:7] op_sel_hi:[1,0]
	v_pk_mul_f32 v[14:15], v[114:115], v[6:7] op_sel_hi:[1,0]
	v_pk_mul_f32 v[16:17], v[108:109], v[6:7] op_sel_hi:[1,0]
	v_pk_mul_f32 v[18:19], v[106:107], v[6:7] op_sel_hi:[1,0]
	v_cvt_pk_bf16_f32 v6, v14, v15
	v_cvt_pk_bf16_f32 v7, v8, v9
	v_cvt_pk_bf16_f32 v8, v18, v19
	v_cvt_pk_bf16_f32 v9, v16, v17
	global_store_dwordx4 v[12:13], v[6:9], off offset:256
	s_nop 1
	v_or_b32_e32 v6, 48, v20
	v_mad_i64_i32 v[6:7], s[4:5], v6, s89, v[2:3]
	v_lshl_add_u64 v[12:13], v[6:7], 0, v[4:5]
	v_mul_f32_e32 v6, v21, v11
	v_pk_mul_f32 v[8:9], v[120:121], v[6:7] op_sel_hi:[1,0]
	v_pk_mul_f32 v[14:15], v[118:119], v[6:7] op_sel_hi:[1,0]
	v_pk_mul_f32 v[16:17], v[112:113], v[6:7] op_sel_hi:[1,0]
	v_pk_mul_f32 v[18:19], v[110:111], v[6:7] op_sel_hi:[1,0]
	v_cvt_pk_bf16_f32 v6, v14, v15
	v_cvt_pk_bf16_f32 v7, v8, v9
	v_cvt_pk_bf16_f32 v8, v18, v19
	v_cvt_pk_bf16_f32 v9, v16, v17
	global_store_dwordx4 v[12:13], v[6:9], off
	ds_read_b32 v18, v192
	s_nop 0
	v_mul_f32_e32 v6, v22, v11
	v_pk_mul_f32 v[8:9], v[104:105], v[6:7] op_sel_hi:[1,0]
	v_pk_mul_f32 v[10:11], v[102:103], v[6:7] op_sel_hi:[1,0]
	v_pk_mul_f32 v[14:15], v[100:101], v[6:7] op_sel_hi:[1,0]
	v_pk_mul_f32 v[16:17], v[98:99], v[6:7] op_sel_hi:[1,0]
	v_cvt_pk_bf16_f32 v6, v10, v11
	v_cvt_pk_bf16_f32 v7, v8, v9
	v_cvt_pk_bf16_f32 v8, v16, v17
	v_cvt_pk_bf16_f32 v9, v14, v15
	global_store_dwordx4 v[12:13], v[6:9], off offset:256
	s_nop 1
	v_add_u32_e32 v6, 0x80, v20
	v_mad_i64_i32 v[6:7], s[4:5], v6, s89, v[2:3]
	v_lshl_add_u64 v[10:11], v[6:7], 0, v[4:5]
	s_waitcnt lgkmcnt(0)
; __device__ __forceinline__ unsigned cvt_pk_bf16(float lo, float hi) { const f32x2 v = {lo, hi}; const bf16x2_t b = __builtin_convertvector(v, bf16x2_t); return __builtin_bit_cast(unsigned, b); }
; #define PG8_BAR __builtin_amdgcn_s_barrier()
; __device__ __forceinline__ unsigned long long rt() { return __builtin_amdgcn_s_memrealtime(); }
;     __device__ __forceinline__ void operator()(const f32x4 (&acc)[2][2][4][2], const Unit& u, int wr, int wc, int fr, int fq) const {
;     ...
;         for (int ai = 0; ai < 2; ++ai)
; #pragma unroll
;             for (int m = 0; m < 4; ++m) { bf16_t* rowp = O + (size_t)(row0 + ai * HALF + m * 16) * ldc + col0;
;                 const float rs = rt ? rt[ai * HALF + wr * 64 + m * 16 + fr] : 1.0f;
; #pragma unroll
;                 for (int bj = 0; bj < 2; ++bj) { const float sc = (bj ? sc1 : sc0) * rs; const f32x4 v0 = acc[ai][bj][m][0] * sc, v1 = acc[ai][bj][m][1] * sc;
;                     u32x4 w; w.x = cvt_pk_bf16(v0[0], v0[1]); w.y = cvt_pk_bf16(v0[2], v0[3]); w.z = cvt_pk_bf16(v1[0], v1[1]); w.w = cvt_pk_bf16(v1[2], v1[3]);
;                     *(u32x4*)(rowp + bj * HALF) = w; } }
; template <class Epi, class Sched, bool ALIGN_EPI = false, bool SP2 = false, bool F8 = false>
; __device__ __forceinline__ void gemm_phase(PG8_LAS unsigned char* lds, const Gemm g, const Sched& S, const Epi& E) {
;     ...
;         if (!has_next) break;
; #pragma unroll
;         for (int a = 0; a < 2; ++a)
; #pragma unroll
;             for (int b = 0; b < 2; ++b)
; #pragma unroll
;                 for (int m = 0; m < 4; ++m)
; #pragma unroll
;                     for (int n = 0; n < 2; ++n) acc[a][b][m][n] = (f32x4){0.f, 0.f, 0.f, 0.f};
;         cur = nxt; cA = nA; cB = nB; ++ui;
;         if constexpr (ALIGN_EPI) { if (wr == 1) PG8_BAR; }
	v_mul_f32_e32 v6, v21, v18
	v_pk_mul_f32 v[8:9], v[96:97], v[6:7] op_sel_hi:[1,0]
	v_pk_mul_f32 v[12:13], v[94:95], v[6:7] op_sel_hi:[1,0]
	v_pk_mul_f32 v[14:15], v[92:93], v[6:7] op_sel_hi:[1,0]
	v_pk_mul_f32 v[16:17], v[90:91], v[6:7] op_sel_hi:[1,0]
	v_cvt_pk_bf16_f32 v6, v12, v13
	v_cvt_pk_bf16_f32 v7, v8, v9
	v_cvt_pk_bf16_f32 v8, v16, v17
	v_cvt_pk_bf16_f32 v9, v14, v15
	global_store_dwordx4 v[10:11], v[6:9], off
	s_nop 1
	v_mul_f32_e32 v6, v22, v18
	v_pk_mul_f32 v[8:9], v[80:81], v[6:7] op_sel_hi:[1,0]
	v_pk_mul_f32 v[12:13], v[78:79], v[6:7] op_sel_hi:[1,0]
	v_pk_mul_f32 v[14:15], v[76:77], v[6:7] op_sel_hi:[1,0]
	v_pk_mul_f32 v[16:17], v[74:75], v[6:7] op_sel_hi:[1,0]
	v_cvt_pk_bf16_f32 v6, v12, v13
	v_cvt_pk_bf16_f32 v7, v8, v9
	v_cvt_pk_bf16_f32 v8, v16, v17
	v_cvt_pk_bf16_f32 v9, v14, v15
	global_store_dwordx4 v[10:11], v[6:9], off offset:256
	ds_read2_b32 v[10:11], v191 offset0:144 offset1:160
	s_nop 0
	v_add_u32_e32 v6, 0x90, v20
	v_mad_i64_i32 v[6:7], s[4:5], v6, s89, v[2:3]
	v_lshl_add_u64 v[12:13], v[6:7], 0, v[4:5]
	s_waitcnt lgkmcnt(0)
	v_mul_f32_e32 v6, v21, v10
	v_pk_mul_f32 v[8:9], v[88:89], v[6:7] op_sel_hi:[1,0]
	v_pk_mul_f32 v[14:15], v[86:87], v[6:7] op_sel_hi:[1,0]
	v_pk_mul_f32 v[16:17], v[84:85], v[6:7] op_sel_hi:[1,0]
	v_pk_mul_f32 v[18:19], v[82:83], v[6:7] op_sel_hi:[1,0]
	v_cvt_pk_bf16_f32 v6, v14, v15
	v_cvt_pk_bf16_f32 v7, v8, v9
	v_cvt_pk_bf16_f32 v8, v18, v19
	v_cvt_pk_bf16_f32 v9, v16, v17
	global_store_dwordx4 v[12:13], v[6:9], off
	s_nop 1
	v_mul_f32_e32 v6, v22, v10
	v_pk_mul_f32 v[8:9], v[64:65], v[6:7] op_sel_hi:[1,0]
	v_pk_mul_f32 v[14:15], v[62:63], v[6:7] op_sel_hi:[1,0]
	v_pk_mul_f32 v[16:17], v[60:61], v[6:7] op_sel_hi:[1,0]
	v_pk_mul_f32 v[18:19], v[58:59], v[6:7] op_sel_hi:[1,0]
	v_cvt_pk_bf16_f32 v6, v14, v15
	v_cvt_pk_bf16_f32 v7, v8, v9
	v_cvt_pk_bf16_f32 v8, v18, v19
	v_cvt_pk_bf16_f32 v9, v16, v17
	global_store_dwordx4 v[12:13], v[6:9], off offset:256
	s_nop 1
	v_add_u32_e32 v6, 0xa0, v20
	v_mad_i64_i32 v[6:7], s[4:5], v6, s89, v[2:3]
	v_lshl_add_u64 v[12:13], v[6:7], 0, v[4:5]
	v_mul_f32_e32 v6, v21, v11
	v_pk_mul_f32 v[8:9], v[72:73], v[6:7] op_sel_hi:[1,0]
	v_pk_mul_f32 v[14:15], v[70:71], v[6:7] op_sel_hi:[1,0]
	v_pk_mul_f32 v[16:17], v[68:69], v[6:7] op_sel_hi:[1,0]
	v_pk_mul_f32 v[18:19], v[66:67], v[6:7] op_sel_hi:[1,0]
	v_cvt_pk_bf16_f32 v6, v14, v15
	v_cvt_pk_bf16_f32 v7, v8, v9
	v_cvt_pk_bf16_f32 v8, v18, v19
	v_cvt_pk_bf16_f32 v9, v16, v17
	global_store_dwordx4 v[12:13], v[6:9], off
	s_nop 1
	v_mul_f32_e32 v6, v22, v11
	v_pk_mul_f32 v[8:9], v[48:49], v[6:7] op_sel_hi:[1,0]
	v_pk_mul_f32 v[10:11], v[46:47], v[6:7] op_sel_hi:[1,0]
	v_pk_mul_f32 v[14:15], v[44:45], v[6:7] op_sel_hi:[1,0]
	v_pk_mul_f32 v[16:17], v[42:43], v[6:7] op_sel_hi:[1,0]
	v_cvt_pk_bf16_f32 v6, v10, v11
	v_cvt_pk_bf16_f32 v7, v8, v9
	v_cvt_pk_bf16_f32 v8, v16, v17
	v_cvt_pk_bf16_f32 v9, v14, v15
	global_store_dwordx4 v[12:13], v[6:9], off offset:256
	s_nop 1
	v_add_u32_e32 v6, 0xb0, v20
	v_mad_i64_i32 v[2:3], s[4:5], v6, s89, v[2:3]
	v_lshl_add_u64 v[6:7], v[2:3], 0, v[4:5]
	v_mul_f32_e32 v2, v21, v23
	v_pk_mul_f32 v[4:5], v[56:57], v[2:3] op_sel_hi:[1,0]
	v_pk_mul_f32 v[8:9], v[54:55], v[2:3] op_sel_hi:[1,0]
	v_pk_mul_f32 v[10:11], v[52:53], v[2:3] op_sel_hi:[1,0]
	v_pk_mul_f32 v[12:13], v[50:51], v[2:3] op_sel_hi:[1,0]
	v_cvt_pk_bf16_f32 v2, v8, v9
	v_cvt_pk_bf16_f32 v3, v4, v5
	v_cvt_pk_bf16_f32 v4, v12, v13
	v_cvt_pk_bf16_f32 v5, v10, v11
	global_store_dwordx4 v[6:7], v[2:5], off
	s_nop 1
	v_mul_f32_e32 v2, v22, v23
	v_pk_mul_f32 v[4:5], v[40:41], v[2:3] op_sel_hi:[1,0]
	v_pk_mul_f32 v[8:9], v[38:39], v[2:3] op_sel_hi:[1,0]
	v_pk_mul_f32 v[10:11], v[36:37], v[2:3] op_sel_hi:[1,0]
	v_pk_mul_f32 v[12:13], v[34:35], v[2:3] op_sel_hi:[1,0]
	v_cvt_pk_bf16_f32 v2, v8, v9
	v_cvt_pk_bf16_f32 v3, v4, v5
	v_cvt_pk_bf16_f32 v4, v12, v13
	v_cvt_pk_bf16_f32 v5, v10, v11
	global_store_dwordx4 v[6:7], v[2:5], off offset:256
	s_barrier
	s_cbranch_vccnz .LBB0_147
	s_andn2_b64 vcc, exec, s[14:15]
	s_cbranch_vccnz .LBB0_146
	s_barrier
	s_branch .LBB0_146

; #define PG8_STAGE(bufoff, gbase, voff) do { _Pragma("unroll") for (int _i = 0; _i < 2; ++_i) \
;         __builtin_amdgcn_global_load_lds((const unsigned*)((const char*)(gbase) + (voff)[_i]), (PG8_LAS unsigned*)(lds + (bufoff) + ldsw + _i * 8192), 16, 0, 0); } while (0)
; #define PG8_LDA(dst, b, h) do { _Pragma("unroll") for (int m = 0; m < 4; ++m) Frag<F8>::load(dst[m], lds + PG8_SA(b, h) + aoff + m * 2048); } while (0)
; #define PG8_LDB(dst, b, h) do { _Pragma("unroll") for (int n = 0; n < 2; ++n) Frag<F8>::load(dst[n], lds + PG8_SB(b, h) + boff + n * 2048); } while (0)
; #define PG8_MMA(ai, bj, At, Bt) do { __builtin_amdgcn_s_setprio(3); _Pragma("unroll") for (int m = 0; m < 4; ++m) _Pragma("unroll") for (int n = 0; n < 2; ++n) Frag<F8>::mma(acc[ai][bj][m][n], Bt[n], At[m]); \
;         __builtin_amdgcn_s_setprio(0); } while (0)
; #define PG8_WAIT_V(n) asm volatile("s_waitcnt vmcnt(" #n ")" ::: "memory")
; #define PG8_BAR __builtin_amdgcn_s_barrier()
; template <class Epi, class Sched, bool ALIGN_EPI = false, bool SP2 = false, bool F8 = false>
; __device__ __forceinline__ void gemm_phase(PG8_LAS unsigned char* lds, const Gemm g, const Sched& S, const Epi& E) {
;     ...
;         const bool has_next = S.next(ui + 1, nxt);
;         const char* nA = has_next ? (const char*)g.A + (size_t)nxt.pm * tstep + nxt.ko : cA; const char* nB = has_next ? (const char*)g.Bt + (size_t)nxt.pn * tstep + nxt.ko : cB;
;         for (int t = 0; t < nt; t += 2) {
;             const bool last = (t == nt - 2);
;             const char* a1 = cA + (size_t)(t + 1) * kstep;
;             const char* a2 = last ? nA : cA + (size_t)(t + 2) * kstep; const char* b2 = last ? nB : cB + (size_t)(t + 2) * kstep;
;             const char* a3 = a2 + kstep; const char* b3 = b2 + kstep;
;             if (last && has_next) S.a_ready(nxt);
;             if constexpr (SP2) {
;             PG8_LDB(B0, 0, 0); PG8_LDB(B1, 0, 1); PG8_SCHED; PG8_LDA(At, 0, 0); PG8_STAGE(PG8_SA(1, 1), a1 + hstep, voffA);
;             PG8_WAIT_V(8); PG8_WAIT_L(0); PG8_BAR; PG8_MMA(0, 0, At, B0); PG8_MMA(0, 1, At, B1); PG8_BAR; PG8_SCHED;
;             PG8_LDA(At, 0, 1); PG8_STAGE(PG8_SB(0, 0), b2, voffB); PG8_STAGE(PG8_SB(0, 1), b2 + hstep, voffB); PG8_STAGE(PG8_SA(0, 0), a2, voffA);
;             PG8_WAIT_V(8); PG8_WAIT_L(0); PG8_BAR; PG8_MMA(1, 0, At, B0); PG8_MMA(1, 1, At, B1); PG8_BAR; PG8_SCHED;
.LBB0_561:
	s_ashr_i32 s25, s24, 31
	s_lshl_b64 s[4:5], s[24:25], 19
	s_add_u32 s36, s50, s4
	s_addc_u32 s37, s51, s5
	s_and_b64 s[4:5], s[8:9], exec
	s_cselect_b32 s6, s37, s43
	s_cselect_b32 s7, s36, s42
	s_ashr_i32 s31, s30, 31
	s_lshl_b64 s[4:5], s[30:31], 19
	s_add_u32 s38, s52, s4
	s_addc_u32 s39, s53, s5
	s_and_b64 s[4:5], s[8:9], exec
	s_cselect_b32 s25, s39, s45
	s_cselect_b32 s31, s38, s44
	s_add_u32 s42, s42, 0x40080
	s_addc_u32 s43, s43, 0
	s_add_u32 s84, s44, 0x100
	s_addc_u32 s85, s45, 0
	s_mov_b32 s86, -2
	ds_read_b128 v[146:149], v155
	ds_read_b128 v[158:161], v155 offset:1024
	ds_read_b128 v[166:169], v155 offset:2048
	ds_read_b128 v[170:173], v155 offset:3072
	ds_read_b128 v[174:177], v156
	ds_read_b128 v[178:181], v156 offset:1024
	ds_read_b128 v[182:185], v156 offset:2048
	ds_read_b128 v[186:189], v156 offset:3072
	s_add_u32 s0, s42, 0xfffc0080
	s_addc_u32 s1, s43, -1
	s_cmp_eq_u32 s86, 12
	s_cselect_b32 s47, s6, s1
	s_cselect_b32 s46, s7, s0
	s_cselect_b32 s45, s25, s85
	s_cselect_b32 s44, s31, s84
	v_lshl_add_u64 v[222:223], s[42:43], 0, v[138:139]
	s_add_i32 m0, s41, 0xc000
	ds_read_b128 v[190:193], v157
	ds_read_b128 v[194:197], v157 offset:1024
	ds_read_b128 v[198:201], v157 offset:2048
	ds_read_b128 v[202:205], v157 offset:3072
	ds_read_b128 v[206:209], v157 offset:4096
	ds_read_b128 v[210:213], v157 offset:5120
	ds_read_b128 v[214:217], v157 offset:6144
	ds_read_b128 v[218:221], v157 offset:7168
	global_load_lds_dwordx4 v[222:223], off
	v_lshl_add_u64 v[222:223], s[42:43], 0, v[140:141]
	s_add_i32 m0, s41, 0xe000
	s_nop 0
	global_load_lds_dwordx4 v[222:223], off
	s_waitcnt vmcnt(8)
	s_waitcnt lgkmcnt(0)
	s_barrier
	s_setprio 3
	s_waitcnt lgkmcnt(0)
	v_mfma_f32_16x16x32_bf16 v[126:129], v[146:149], v[190:193], 0
	v_mfma_f32_16x16x32_bf16 v[118:121], v[166:169], v[190:193], 0
	v_mfma_f32_16x16x32_bf16 v[110:113], v[146:149], v[198:201], 0
	v_mfma_f32_16x16x32_bf16 v[102:105], v[166:169], v[198:201], 0
	v_mfma_f32_16x16x32_bf16 v[94:97], v[146:149], v[206:209], 0
	v_mfma_f32_16x16x32_bf16 v[86:89], v[166:169], v[206:209], 0
	v_mfma_f32_16x16x32_bf16 v[78:81], v[146:149], v[214:217], 0
	v_mfma_f32_16x16x32_bf16 v[70:73], v[166:169], v[214:217], 0
	v_mfma_f32_16x16x32_bf16 v[126:129], v[158:161], v[194:197], v[126:129]
	v_mfma_f32_16x16x32_bf16 v[118:121], v[170:173], v[194:197], v[118:121]
	v_mfma_f32_16x16x32_bf16 v[110:113], v[158:161], v[202:205], v[110:113]
	v_mfma_f32_16x16x32_bf16 v[102:105], v[170:173], v[202:205], v[102:105]
	v_mfma_f32_16x16x32_bf16 v[94:97], v[158:161], v[210:213], v[94:97]
	v_mfma_f32_16x16x32_bf16 v[86:89], v[170:173], v[210:213], v[86:89]
	v_mfma_f32_16x16x32_bf16 v[78:81], v[158:161], v[218:221], v[78:81]
	v_mfma_f32_16x16x32_bf16 v[70:73], v[170:173], v[218:221], v[70:73]
	s_setprio 0
	s_setprio 3
	v_mfma_f32_16x16x32_bf16 v[122:125], v[174:177], v[190:193], 0
	v_mfma_f32_16x16x32_bf16 v[114:117], v[182:185], v[190:193], 0
	v_mfma_f32_16x16x32_bf16 v[106:109], v[174:177], v[198:201], 0
	v_mfma_f32_16x16x32_bf16 v[98:101], v[182:185], v[198:201], 0
	v_mfma_f32_16x16x32_bf16 v[90:93], v[174:177], v[206:209], 0
	v_mfma_f32_16x16x32_bf16 v[82:85], v[182:185], v[206:209], 0
	v_mfma_f32_16x16x32_bf16 v[74:77], v[174:177], v[214:217], 0
	v_mfma_f32_16x16x32_bf16 v[66:69], v[182:185], v[214:217], 0
	v_mfma_f32_16x16x32_bf16 v[122:125], v[178:181], v[194:197], v[122:125]
	v_mfma_f32_16x16x32_bf16 v[114:117], v[186:189], v[194:197], v[114:117]
	v_mfma_f32_16x16x32_bf16 v[106:109], v[178:181], v[202:205], v[106:109]
	v_mfma_f32_16x16x32_bf16 v[98:101], v[186:189], v[202:205], v[98:101]
	v_mfma_f32_16x16x32_bf16 v[90:93], v[178:181], v[210:213], v[90:93]
	v_mfma_f32_16x16x32_bf16 v[82:85], v[186:189], v[210:213], v[82:85]
	v_mfma_f32_16x16x32_bf16 v[74:77], v[178:181], v[218:221], v[74:77]
	v_mfma_f32_16x16x32_bf16 v[66:69], v[186:189], v[218:221], v[66:69]
	s_setprio 0
	s_barrier
	s_add_i32 s0, s80, s49
	v_lshl_add_u64 v[222:223], s[44:45], 0, v[134:135]
	s_mov_b32 m0, s0
	ds_read_b128 v[190:193], v157 offset:16384
	ds_read_b128 v[194:197], v157 offset:17408
	ds_read_b128 v[198:201], v157 offset:18432
	ds_read_b128 v[202:205], v157 offset:19456
	ds_read_b128 v[206:209], v157 offset:20480
	ds_read_b128 v[210:213], v157 offset:21504
	ds_read_b128 v[214:217], v157 offset:22528
	ds_read_b128 v[218:221], v157 offset:23552
	global_load_lds_dwordx4 v[222:223], off
	s_add_i32 m0, s0, 0x2000
	s_add_u32 s4, s44, 0x40000
	v_lshl_add_u64 v[224:225], s[44:45], 0, v[130:131]
	s_addc_u32 s5, s45, 0
	s_add_i32 s0, s81, s49
	global_load_lds_dwordx4 v[224:225], off
	v_lshl_add_u64 v[226:227], s[4:5], 0, v[134:135]
	s_mov_b32 m0, s0
	v_lshl_add_u64 v[228:229], s[46:47], 0, v[132:133]
	global_load_lds_dwordx4 v[226:227], off
	v_lshl_add_u64 v[226:227], s[4:5], 0, v[130:131]
	s_add_i32 m0, s0, 0x2000
	s_nop 0
	global_load_lds_dwordx4 v[226:227], off
	v_lshl_add_u64 v[226:227], s[46:47], 0, v[136:137]
	s_mov_b32 m0, s41
	s_nop 0
	global_load_lds_dwordx4 v[226:227], off
	s_mov_b32 m0, s72
	s_nop 0
	global_load_lds_dwordx4 v[228:229], off
	s_waitcnt vmcnt(8)
	s_waitcnt lgkmcnt(0)
	s_barrier
; #define PG8_STAGE(bufoff, gbase, voff) do { _Pragma("unroll") for (int _i = 0; _i < 2; ++_i) \
;         __builtin_amdgcn_global_load_lds((const unsigned*)((const char*)(gbase) + (voff)[_i]), (PG8_LAS unsigned*)(lds + (bufoff) + ldsw + _i * 8192), 16, 0, 0); } while (0)
; #define PG8_LDA(dst, b, h) do { _Pragma("unroll") for (int m = 0; m < 4; ++m) Frag<F8>::load(dst[m], lds + PG8_SA(b, h) + aoff + m * 2048); } while (0)
; #define PG8_LDB(dst, b, h) do { _Pragma("unroll") for (int n = 0; n < 2; ++n) Frag<F8>::load(dst[n], lds + PG8_SB(b, h) + boff + n * 2048); } while (0)
; #define PG8_MMA(ai, bj, At, Bt) do { __builtin_amdgcn_s_setprio(3); _Pragma("unroll") for (int m = 0; m < 4; ++m) _Pragma("unroll") for (int n = 0; n < 2; ++n) Frag<F8>::mma(acc[ai][bj][m][n], Bt[n], At[m]); \
;         __builtin_amdgcn_s_setprio(0); } while (0)
; #define PG8_WAIT_V(n) asm volatile("s_waitcnt vmcnt(" #n ")" ::: "memory")
; #define PG8_WAIT_L(n) asm volatile("s_waitcnt lgkmcnt(" #n ")" ::: "memory")
; #define PG8_BAR __builtin_amdgcn_s_barrier()
; #define PG8_SCHED __builtin_amdgcn_sched_barrier(0)
; template <class Epi, class Sched, bool ALIGN_EPI = false, bool SP2 = false, bool F8 = false>
; __device__ __forceinline__ void gemm_phase(PG8_LAS unsigned char* lds, const Gemm g, const Sched& S, const Epi& E) {
;     ...
;             PG8_WAIT_V(8); PG8_WAIT_L(0); PG8_BAR; PG8_MMA(1, 0, At, B0); PG8_MMA(1, 1, At, B1); PG8_BAR; PG8_SCHED;
;             PG8_LDB(B0, 1, 0); PG8_LDB(B1, 1, 1); PG8_SCHED; PG8_LDA(At, 1, 0); PG8_STAGE(PG8_SA(0, 1), a2 + hstep, voffA);
;             PG8_WAIT_V(8); PG8_WAIT_L(0); PG8_BAR; PG8_MMA(0, 0, At, B0); PG8_MMA(0, 1, At, B1); PG8_BAR; PG8_SCHED;
	s_setprio 3
	s_waitcnt lgkmcnt(0)
	v_mfma_f32_16x16x32_bf16 v[62:65], v[146:149], v[190:193], 0
	v_mfma_f32_16x16x32_bf16 v[58:61], v[166:169], v[190:193], 0
	v_mfma_f32_16x16x32_bf16 v[50:53], v[146:149], v[198:201], 0
	v_mfma_f32_16x16x32_bf16 v[42:45], v[166:169], v[198:201], 0
	v_mfma_f32_16x16x32_bf16 v[34:37], v[146:149], v[206:209], 0
	v_mfma_f32_16x16x32_bf16 v[26:29], v[166:169], v[206:209], 0
	v_mfma_f32_16x16x32_bf16 v[14:17], v[146:149], v[214:217], 0
	v_mfma_f32_16x16x32_bf16 v[6:9], v[166:169], v[214:217], 0
	v_mfma_f32_16x16x32_bf16 v[62:65], v[158:161], v[194:197], v[62:65]
	v_mfma_f32_16x16x32_bf16 v[58:61], v[170:173], v[194:197], v[58:61]
	v_mfma_f32_16x16x32_bf16 v[50:53], v[158:161], v[202:205], v[50:53]
	v_mfma_f32_16x16x32_bf16 v[42:45], v[170:173], v[202:205], v[42:45]
	v_mfma_f32_16x16x32_bf16 v[34:37], v[158:161], v[210:213], v[34:37]
	v_mfma_f32_16x16x32_bf16 v[26:29], v[170:173], v[210:213], v[26:29]
	v_mfma_f32_16x16x32_bf16 v[14:17], v[158:161], v[218:221], v[14:17]
	v_mfma_f32_16x16x32_bf16 v[6:9], v[170:173], v[218:221], v[6:9]
	s_setprio 0
	s_setprio 3
	v_mfma_f32_16x16x32_bf16 v[54:57], v[174:177], v[190:193], 0
	v_mfma_f32_16x16x32_bf16 v[46:49], v[182:185], v[190:193], 0
	v_mfma_f32_16x16x32_bf16 v[38:41], v[174:177], v[198:201], 0
	v_mfma_f32_16x16x32_bf16 v[30:33], v[182:185], v[198:201], 0
	v_mfma_f32_16x16x32_bf16 v[22:25], v[174:177], v[206:209], 0
	v_mfma_f32_16x16x32_bf16 v[18:21], v[182:185], v[206:209], 0
	v_mfma_f32_16x16x32_bf16 v[10:13], v[174:177], v[214:217], 0
	v_mfma_f32_16x16x32_bf16 v[2:5], v[182:185], v[214:217], 0
	v_mfma_f32_16x16x32_bf16 v[54:57], v[178:181], v[194:197], v[54:57]
	v_mfma_f32_16x16x32_bf16 v[46:49], v[186:189], v[194:197], v[46:49]
	v_mfma_f32_16x16x32_bf16 v[38:41], v[178:181], v[202:205], v[38:41]
	v_mfma_f32_16x16x32_bf16 v[30:33], v[186:189], v[202:205], v[30:33]
	v_mfma_f32_16x16x32_bf16 v[22:25], v[178:181], v[210:213], v[22:25]
	v_mfma_f32_16x16x32_bf16 v[18:21], v[186:189], v[210:213], v[18:21]
	v_mfma_f32_16x16x32_bf16 v[10:13], v[178:181], v[218:221], v[10:13]
	v_mfma_f32_16x16x32_bf16 v[2:5], v[186:189], v[218:221], v[2:5]
	s_setprio 0
	s_barrier
	s_add_i32 s0, 0, 0x18000
	v_add_u32_e32 v165, s0, v151
	s_add_i32 s1, 0, 0x1c000
	ds_read_b128 v[146:149], v165
	ds_read_b128 v[158:161], v165 offset:1024
	ds_read_b128 v[166:169], v165 offset:2048
	ds_read_b128 v[170:173], v165 offset:3072
	v_add_u32_e32 v165, s1, v151
	ds_read_b128 v[174:177], v165
	ds_read_b128 v[178:181], v165 offset:1024
	ds_read_b128 v[182:185], v165 offset:2048
	ds_read_b128 v[186:189], v165 offset:3072
	s_add_u32 s4, s46, 0x40000
	s_addc_u32 s5, s47, 0
	s_mov_b32 m0, s73
	v_lshl_add_u64 v[230:231], s[4:5], 0, v[136:137]
	ds_read_b128 v[190:193], v157 offset:32768
	ds_read_b128 v[194:197], v157 offset:33792
	ds_read_b128 v[198:201], v157 offset:34816
	ds_read_b128 v[202:205], v157 offset:35840
	ds_read_b128 v[206:209], v157 offset:36864
	ds_read_b128 v[210:213], v157 offset:37888
	ds_read_b128 v[214:217], v157 offset:38912
	ds_read_b128 v[218:221], v157 offset:39936
	global_load_lds_dwordx4 v[230:231], off
	v_lshl_add_u64 v[230:231], s[4:5], 0, v[132:133]
	s_mov_b32 m0, s74
	s_nop 0
	global_load_lds_dwordx4 v[230:231], off
	s_waitcnt vmcnt(8)
	s_waitcnt lgkmcnt(0)
	s_barrier
	s_setprio 3
	s_waitcnt lgkmcnt(0)
	v_mfma_f32_16x16x32_bf16 v[126:129], v[146:149], v[190:193], v[126:129]
	v_mfma_f32_16x16x32_bf16 v[118:121], v[166:169], v[190:193], v[118:121]
	v_mfma_f32_16x16x32_bf16 v[110:113], v[146:149], v[198:201], v[110:113]
	v_mfma_f32_16x16x32_bf16 v[102:105], v[166:169], v[198:201], v[102:105]
	v_mfma_f32_16x16x32_bf16 v[94:97], v[146:149], v[206:209], v[94:97]
	v_mfma_f32_16x16x32_bf16 v[86:89], v[166:169], v[206:209], v[86:89]
	v_mfma_f32_16x16x32_bf16 v[78:81], v[146:149], v[214:217], v[78:81]
	v_mfma_f32_16x16x32_bf16 v[70:73], v[166:169], v[214:217], v[70:73]
	v_mfma_f32_16x16x32_bf16 v[126:129], v[158:161], v[194:197], v[126:129]
	v_mfma_f32_16x16x32_bf16 v[118:121], v[170:173], v[194:197], v[118:121]
	v_mfma_f32_16x16x32_bf16 v[110:113], v[158:161], v[202:205], v[110:113]
	v_mfma_f32_16x16x32_bf16 v[102:105], v[170:173], v[202:205], v[102:105]
	v_mfma_f32_16x16x32_bf16 v[94:97], v[158:161], v[210:213], v[94:97]
	v_mfma_f32_16x16x32_bf16 v[86:89], v[170:173], v[210:213], v[86:89]
	v_mfma_f32_16x16x32_bf16 v[78:81], v[158:161], v[218:221], v[78:81]
	v_mfma_f32_16x16x32_bf16 v[70:73], v[170:173], v[218:221], v[70:73]
	s_setprio 0
	s_setprio 3
	v_mfma_f32_16x16x32_bf16 v[122:125], v[174:177], v[190:193], v[122:125]
	v_mfma_f32_16x16x32_bf16 v[114:117], v[182:185], v[190:193], v[114:117]
	v_mfma_f32_16x16x32_bf16 v[106:109], v[174:177], v[198:201], v[106:109]
	v_mfma_f32_16x16x32_bf16 v[98:101], v[182:185], v[198:201], v[98:101]
	v_mfma_f32_16x16x32_bf16 v[90:93], v[174:177], v[206:209], v[90:93]
	v_mfma_f32_16x16x32_bf16 v[82:85], v[182:185], v[206:209], v[82:85]
	v_mfma_f32_16x16x32_bf16 v[74:77], v[174:177], v[214:217], v[74:77]
	v_mfma_f32_16x16x32_bf16 v[66:69], v[182:185], v[214:217], v[66:69]
	v_mfma_f32_16x16x32_bf16 v[122:125], v[178:181], v[194:197], v[122:125]
	v_mfma_f32_16x16x32_bf16 v[114:117], v[186:189], v[194:197], v[114:117]
	v_mfma_f32_16x16x32_bf16 v[106:109], v[178:181], v[202:205], v[106:109]
	v_mfma_f32_16x16x32_bf16 v[98:101], v[186:189], v[202:205], v[98:101]
	v_mfma_f32_16x16x32_bf16 v[90:93], v[178:181], v[210:213], v[90:93]
	v_mfma_f32_16x16x32_bf16 v[82:85], v[186:189], v[210:213], v[82:85]
	v_mfma_f32_16x16x32_bf16 v[74:77], v[178:181], v[218:221], v[74:77]
	v_mfma_f32_16x16x32_bf16 v[66:69], v[186:189], v[218:221], v[66:69]
	s_setprio 0
	s_barrier
; #define PG8_STAGE(bufoff, gbase, voff) do { _Pragma("unroll") for (int _i = 0; _i < 2; ++_i) \
;         __builtin_amdgcn_global_load_lds((const unsigned*)((const char*)(gbase) + (voff)[_i]), (PG8_LAS unsigned*)(lds + (bufoff) + ldsw + _i * 8192), 16, 0, 0); } while (0)
; #define PG8_LDA(dst, b, h) do { _Pragma("unroll") for (int m = 0; m < 4; ++m) Frag<F8>::load(dst[m], lds + PG8_SA(b, h) + aoff + m * 2048); } while (0)
; #define PG8_LDB(dst, b, h) do { _Pragma("unroll") for (int n = 0; n < 2; ++n) Frag<F8>::load(dst[n], lds + PG8_SB(b, h) + boff + n * 2048); } while (0)
; #define PG8_MMA(ai, bj, At, Bt) do { __builtin_amdgcn_s_setprio(3); _Pragma("unroll") for (int m = 0; m < 4; ++m) _Pragma("unroll") for (int n = 0; n < 2; ++n) Frag<F8>::mma(acc[ai][bj][m][n], Bt[n], At[m]); \
;         __builtin_amdgcn_s_setprio(0); } while (0)
; #define PG8_WAIT_V(n) asm volatile("s_waitcnt vmcnt(" #n ")" ::: "memory")
; #define PG8_WAIT_L(n) asm volatile("s_waitcnt lgkmcnt(" #n ")" ::: "memory")
; #define PG8_BAR __builtin_amdgcn_s_barrier()
; #define PG8_SCHED __builtin_amdgcn_sched_barrier(0)
; template <class Epi, class Sched, bool ALIGN_EPI = false, bool SP2 = false, bool F8 = false>
; __device__ __forceinline__ void gemm_phase(PG8_LAS unsigned char* lds, const Gemm g, const Sched& S, const Epi& E) {
;     ...
;             PG8_LDB(B0, 0, 0); PG8_LDB(B1, 0, 1); PG8_SCHED; PG8_LDA(At, 0, 0); PG8_STAGE(PG8_SA(1, 1), a1 + hstep, voffA);
;             PG8_WAIT_V(8); PG8_WAIT_L(0); PG8_BAR; PG8_MMA(0, 0, At, B0); PG8_MMA(0, 1, At, B1); PG8_BAR; PG8_SCHED;
;     ...
;             PG8_LDA(At, 1, 1); PG8_STAGE(PG8_SB(1, 0), b3, voffB); PG8_STAGE(PG8_SB(1, 1), b3 + hstep, voffB); PG8_STAGE(PG8_SA(1, 0), a3, voffA);
;             PG8_WAIT_V(8); PG8_WAIT_L(0); PG8_BAR; PG8_MMA(1, 0, At, B0); PG8_MMA(1, 1, At, B1); PG8_BAR; PG8_SCHED;
	s_add_i32 s0, s0, s49
	v_lshl_add_u64 v[222:223], v[222:223], 0, s[18:19]
	s_mov_b32 m0, s0
	ds_read_b128 v[190:193], v157 offset:49152
	ds_read_b128 v[194:197], v157 offset:50176
	ds_read_b128 v[198:201], v157 offset:51200
	ds_read_b128 v[202:205], v157 offset:52224
	ds_read_b128 v[206:209], v157 offset:53248
	ds_read_b128 v[210:213], v157 offset:54272
	ds_read_b128 v[214:217], v157 offset:55296
	ds_read_b128 v[218:221], v157 offset:56320
	global_load_lds_dwordx4 v[222:223], off
	s_add_i32 m0, s0, 0x2000
	s_add_u32 s4, s44, 0x40080
	v_lshl_add_u64 v[222:223], v[224:225], 0, s[18:19]
	s_addc_u32 s5, s45, 0
	s_add_i32 s0, s1, s49
	global_load_lds_dwordx4 v[222:223], off
	v_lshl_add_u64 v[222:223], s[4:5], 0, v[134:135]
	s_mov_b32 m0, s0
	s_nop 0
	global_load_lds_dwordx4 v[222:223], off
	v_lshl_add_u64 v[222:223], s[4:5], 0, v[130:131]
	s_add_i32 m0, s0, 0x2000
	s_nop 0
	global_load_lds_dwordx4 v[222:223], off
	v_lshl_add_u64 v[222:223], v[226:227], 0, s[18:19]
	s_mov_b32 m0, s75
	s_nop 0
	global_load_lds_dwordx4 v[222:223], off
	v_lshl_add_u64 v[222:223], v[228:229], 0, s[18:19]
	s_mov_b32 m0, s79
	s_nop 0
	global_load_lds_dwordx4 v[222:223], off
	s_waitcnt vmcnt(8)
	s_waitcnt lgkmcnt(0)
	s_barrier
	s_setprio 3
	s_waitcnt lgkmcnt(0)
	v_mfma_f32_16x16x32_bf16 v[62:65], v[146:149], v[190:193], v[62:65]
	v_mfma_f32_16x16x32_bf16 v[58:61], v[166:169], v[190:193], v[58:61]
	v_mfma_f32_16x16x32_bf16 v[50:53], v[146:149], v[198:201], v[50:53]
	v_mfma_f32_16x16x32_bf16 v[42:45], v[166:169], v[198:201], v[42:45]
	v_mfma_f32_16x16x32_bf16 v[34:37], v[146:149], v[206:209], v[34:37]
	v_mfma_f32_16x16x32_bf16 v[26:29], v[166:169], v[206:209], v[26:29]
	v_mfma_f32_16x16x32_bf16 v[14:17], v[146:149], v[214:217], v[14:17]
	v_mfma_f32_16x16x32_bf16 v[6:9], v[166:169], v[214:217], v[6:9]
	v_mfma_f32_16x16x32_bf16 v[62:65], v[158:161], v[194:197], v[62:65]
	v_mfma_f32_16x16x32_bf16 v[58:61], v[170:173], v[194:197], v[58:61]
	v_mfma_f32_16x16x32_bf16 v[50:53], v[158:161], v[202:205], v[50:53]
	v_mfma_f32_16x16x32_bf16 v[42:45], v[170:173], v[202:205], v[42:45]
	v_mfma_f32_16x16x32_bf16 v[34:37], v[158:161], v[210:213], v[34:37]
	v_mfma_f32_16x16x32_bf16 v[26:29], v[170:173], v[210:213], v[26:29]
	v_mfma_f32_16x16x32_bf16 v[14:17], v[158:161], v[218:221], v[14:17]
	v_mfma_f32_16x16x32_bf16 v[6:9], v[170:173], v[218:221], v[6:9]
	s_setprio 0
	s_setprio 3
	v_mfma_f32_16x16x32_bf16 v[54:57], v[174:177], v[190:193], v[54:57]
	v_mfma_f32_16x16x32_bf16 v[46:49], v[182:185], v[190:193], v[46:49]
	v_mfma_f32_16x16x32_bf16 v[38:41], v[174:177], v[198:201], v[38:41]
	v_mfma_f32_16x16x32_bf16 v[30:33], v[182:185], v[198:201], v[30:33]
	v_mfma_f32_16x16x32_bf16 v[22:25], v[174:177], v[206:209], v[22:25]
	v_mfma_f32_16x16x32_bf16 v[18:21], v[182:185], v[206:209], v[18:21]
	v_mfma_f32_16x16x32_bf16 v[10:13], v[174:177], v[214:217], v[10:13]
	v_mfma_f32_16x16x32_bf16 v[2:5], v[182:185], v[214:217], v[2:5]
	v_mfma_f32_16x16x32_bf16 v[54:57], v[178:181], v[194:197], v[54:57]
	v_mfma_f32_16x16x32_bf16 v[46:49], v[186:189], v[194:197], v[46:49]
	v_mfma_f32_16x16x32_bf16 v[38:41], v[178:181], v[202:205], v[38:41]
	v_mfma_f32_16x16x32_bf16 v[30:33], v[186:189], v[202:205], v[30:33]
	v_mfma_f32_16x16x32_bf16 v[22:25], v[178:181], v[210:213], v[22:25]
	v_mfma_f32_16x16x32_bf16 v[18:21], v[186:189], v[210:213], v[18:21]
	v_mfma_f32_16x16x32_bf16 v[10:13], v[178:181], v[218:221], v[10:13]
	v_mfma_f32_16x16x32_bf16 v[2:5], v[186:189], v[218:221], v[2:5]
	s_setprio 0
	s_add_i32 s86, s86, 2
	s_add_u32 s42, s42, 0x100
	s_addc_u32 s43, s43, 0
	s_add_u32 s84, s84, 0x100
	s_addc_u32 s85, s85, 0
	s_cmp_gt_u32 s86, 13
	s_cbranch_scc1 .Lpeel_exit_1
.LBB0_562:
	s_barrier
	ds_read_b128 v[146:149], v155
	ds_read_b128 v[158:161], v155 offset:1024
	ds_read_b128 v[166:169], v155 offset:2048
	ds_read_b128 v[170:173], v155 offset:3072
	ds_read_b128 v[174:177], v156
	ds_read_b128 v[178:181], v156 offset:1024
	ds_read_b128 v[182:185], v156 offset:2048
	ds_read_b128 v[186:189], v156 offset:3072
	s_add_u32 s0, s42, 0xfffc0080
	s_addc_u32 s1, s43, -1
	s_cmp_eq_u32 s86, 12
	s_cselect_b32 s47, s6, s1
	s_cselect_b32 s46, s7, s0
	s_cselect_b32 s45, s25, s85
	s_cselect_b32 s44, s31, s84
	v_lshl_add_u64 v[222:223], s[42:43], 0, v[138:139]
	s_add_i32 m0, s41, 0xc000
	ds_read_b128 v[190:193], v157
	ds_read_b128 v[194:197], v157 offset:1024
	ds_read_b128 v[198:201], v157 offset:2048
	ds_read_b128 v[202:205], v157 offset:3072
	ds_read_b128 v[206:209], v157 offset:4096
	ds_read_b128 v[210:213], v157 offset:5120
	ds_read_b128 v[214:217], v157 offset:6144
	ds_read_b128 v[218:221], v157 offset:7168
	global_load_lds_dwordx4 v[222:223], off
	v_lshl_add_u64 v[222:223], s[42:43], 0, v[140:141]
	s_add_i32 m0, s41, 0xe000
	s_nop 0
	global_load_lds_dwordx4 v[222:223], off
	s_waitcnt vmcnt(8)
	s_waitcnt lgkmcnt(0)
	s_barrier
; #define PG8_STAGE(bufoff, gbase, voff) do { _Pragma("unroll") for (int _i = 0; _i < 2; ++_i) \
;         __builtin_amdgcn_global_load_lds((const unsigned*)((const char*)(gbase) + (voff)[_i]), (PG8_LAS unsigned*)(lds + (bufoff) + ldsw + _i * 8192), 16, 0, 0); } while (0)
; #define PG8_LDA(dst, b, h) do { _Pragma("unroll") for (int m = 0; m < 4; ++m) Frag<F8>::load(dst[m], lds + PG8_SA(b, h) + aoff + m * 2048); } while (0)
; #define PG8_MMA(ai, bj, At, Bt) do { __builtin_amdgcn_s_setprio(3); _Pragma("unroll") for (int m = 0; m < 4; ++m) _Pragma("unroll") for (int n = 0; n < 2; ++n) Frag<F8>::mma(acc[ai][bj][m][n], Bt[n], At[m]); \
;         __builtin_amdgcn_s_setprio(0); } while (0)
; #define PG8_WAIT_V(n) asm volatile("s_waitcnt vmcnt(" #n ")" ::: "memory")
; #define PG8_WAIT_L(n) asm volatile("s_waitcnt lgkmcnt(" #n ")" ::: "memory")
; #define PG8_BAR __builtin_amdgcn_s_barrier()
; #define PG8_SCHED __builtin_amdgcn_sched_barrier(0)
; template <class Epi, class Sched, bool ALIGN_EPI = false, bool SP2 = false, bool F8 = false>
; __device__ __forceinline__ void gemm_phase(PG8_LAS unsigned char* lds, const Gemm g, const Sched& S, const Epi& E) {
;     ...
;             PG8_WAIT_V(8); PG8_WAIT_L(0); PG8_BAR; PG8_MMA(0, 0, At, B0); PG8_MMA(0, 1, At, B1); PG8_BAR; PG8_SCHED;
;             PG8_LDA(At, 0, 1); PG8_STAGE(PG8_SB(0, 0), b2, voffB); PG8_STAGE(PG8_SB(0, 1), b2 + hstep, voffB); PG8_STAGE(PG8_SA(0, 0), a2, voffA);
;             PG8_WAIT_V(8); PG8_WAIT_L(0); PG8_BAR; PG8_MMA(1, 0, At, B0); PG8_MMA(1, 1, At, B1); PG8_BAR; PG8_SCHED;
	s_setprio 3
	s_waitcnt lgkmcnt(0)
	v_mfma_f32_16x16x32_bf16 v[126:129], v[146:149], v[190:193], v[126:129]
	v_mfma_f32_16x16x32_bf16 v[118:121], v[166:169], v[190:193], v[118:121]
	v_mfma_f32_16x16x32_bf16 v[110:113], v[146:149], v[198:201], v[110:113]
	v_mfma_f32_16x16x32_bf16 v[102:105], v[166:169], v[198:201], v[102:105]
	v_mfma_f32_16x16x32_bf16 v[94:97], v[146:149], v[206:209], v[94:97]
	v_mfma_f32_16x16x32_bf16 v[86:89], v[166:169], v[206:209], v[86:89]
	v_mfma_f32_16x16x32_bf16 v[78:81], v[146:149], v[214:217], v[78:81]
	v_mfma_f32_16x16x32_bf16 v[70:73], v[166:169], v[214:217], v[70:73]
	v_mfma_f32_16x16x32_bf16 v[126:129], v[158:161], v[194:197], v[126:129]
	v_mfma_f32_16x16x32_bf16 v[118:121], v[170:173], v[194:197], v[118:121]
	v_mfma_f32_16x16x32_bf16 v[110:113], v[158:161], v[202:205], v[110:113]
	v_mfma_f32_16x16x32_bf16 v[102:105], v[170:173], v[202:205], v[102:105]
	v_mfma_f32_16x16x32_bf16 v[94:97], v[158:161], v[210:213], v[94:97]
	v_mfma_f32_16x16x32_bf16 v[86:89], v[170:173], v[210:213], v[86:89]
	v_mfma_f32_16x16x32_bf16 v[78:81], v[158:161], v[218:221], v[78:81]
	v_mfma_f32_16x16x32_bf16 v[70:73], v[170:173], v[218:221], v[70:73]
	s_setprio 0
	s_setprio 3
	v_mfma_f32_16x16x32_bf16 v[122:125], v[174:177], v[190:193], v[122:125]
	v_mfma_f32_16x16x32_bf16 v[114:117], v[182:185], v[190:193], v[114:117]
	v_mfma_f32_16x16x32_bf16 v[106:109], v[174:177], v[198:201], v[106:109]
	v_mfma_f32_16x16x32_bf16 v[98:101], v[182:185], v[198:201], v[98:101]
	v_mfma_f32_16x16x32_bf16 v[90:93], v[174:177], v[206:209], v[90:93]
	v_mfma_f32_16x16x32_bf16 v[82:85], v[182:185], v[206:209], v[82:85]
	v_mfma_f32_16x16x32_bf16 v[74:77], v[174:177], v[214:217], v[74:77]
	v_mfma_f32_16x16x32_bf16 v[66:69], v[182:185], v[214:217], v[66:69]
	v_mfma_f32_16x16x32_bf16 v[122:125], v[178:181], v[194:197], v[122:125]
	v_mfma_f32_16x16x32_bf16 v[114:117], v[186:189], v[194:197], v[114:117]
	v_mfma_f32_16x16x32_bf16 v[106:109], v[178:181], v[202:205], v[106:109]
	v_mfma_f32_16x16x32_bf16 v[98:101], v[186:189], v[202:205], v[98:101]
	v_mfma_f32_16x16x32_bf16 v[90:93], v[178:181], v[210:213], v[90:93]
	v_mfma_f32_16x16x32_bf16 v[82:85], v[186:189], v[210:213], v[82:85]
	v_mfma_f32_16x16x32_bf16 v[74:77], v[178:181], v[218:221], v[74:77]
	v_mfma_f32_16x16x32_bf16 v[66:69], v[186:189], v[218:221], v[66:69]
	s_setprio 0
	s_barrier
	s_add_i32 s0, s80, s49
	v_lshl_add_u64 v[222:223], s[44:45], 0, v[134:135]
	s_mov_b32 m0, s0
	ds_read_b128 v[190:193], v157 offset:16384
	ds_read_b128 v[194:197], v157 offset:17408
	ds_read_b128 v[198:201], v157 offset:18432
	ds_read_b128 v[202:205], v157 offset:19456
	ds_read_b128 v[206:209], v157 offset:20480
	ds_read_b128 v[210:213], v157 offset:21504
	ds_read_b128 v[214:217], v157 offset:22528
	ds_read_b128 v[218:221], v157 offset:23552
	global_load_lds_dwordx4 v[222:223], off
	s_add_i32 m0, s0, 0x2000
	s_add_u32 s4, s44, 0x40000
	v_lshl_add_u64 v[224:225], s[44:45], 0, v[130:131]
	s_addc_u32 s5, s45, 0
	s_add_i32 s0, s81, s49
	global_load_lds_dwordx4 v[224:225], off
	v_lshl_add_u64 v[226:227], s[4:5], 0, v[134:135]
	s_mov_b32 m0, s0
	v_lshl_add_u64 v[228:229], s[46:47], 0, v[132:133]
	global_load_lds_dwordx4 v[226:227], off
	v_lshl_add_u64 v[226:227], s[4:5], 0, v[130:131]
	s_add_i32 m0, s0, 0x2000
	s_nop 0
	global_load_lds_dwordx4 v[226:227], off
	v_lshl_add_u64 v[226:227], s[46:47], 0, v[136:137]
	s_mov_b32 m0, s41
	s_nop 0
	global_load_lds_dwordx4 v[226:227], off
	s_mov_b32 m0, s72
	s_nop 0
	global_load_lds_dwordx4 v[228:229], off
	s_waitcnt vmcnt(8)
	s_waitcnt lgkmcnt(0)
	s_barrier
	s_setprio 3
	s_waitcnt lgkmcnt(0)
	v_mfma_f32_16x16x32_bf16 v[62:65], v[146:149], v[190:193], v[62:65]
	v_mfma_f32_16x16x32_bf16 v[58:61], v[166:169], v[190:193], v[58:61]
	v_mfma_f32_16x16x32_bf16 v[50:53], v[146:149], v[198:201], v[50:53]
	v_mfma_f32_16x16x32_bf16 v[42:45], v[166:169], v[198:201], v[42:45]
	v_mfma_f32_16x16x32_bf16 v[34:37], v[146:149], v[206:209], v[34:37]
	v_mfma_f32_16x16x32_bf16 v[26:29], v[166:169], v[206:209], v[26:29]
	v_mfma_f32_16x16x32_bf16 v[14:17], v[146:149], v[214:217], v[14:17]
	v_mfma_f32_16x16x32_bf16 v[6:9], v[166:169], v[214:217], v[6:9]
	v_mfma_f32_16x16x32_bf16 v[62:65], v[158:161], v[194:197], v[62:65]
	v_mfma_f32_16x16x32_bf16 v[58:61], v[170:173], v[194:197], v[58:61]
	v_mfma_f32_16x16x32_bf16 v[50:53], v[158:161], v[202:205], v[50:53]
	v_mfma_f32_16x16x32_bf16 v[42:45], v[170:173], v[202:205], v[42:45]
	v_mfma_f32_16x16x32_bf16 v[34:37], v[158:161], v[210:213], v[34:37]
	v_mfma_f32_16x16x32_bf16 v[26:29], v[170:173], v[210:213], v[26:29]
	v_mfma_f32_16x16x32_bf16 v[14:17], v[158:161], v[218:221], v[14:17]
	v_mfma_f32_16x16x32_bf16 v[6:9], v[170:173], v[218:221], v[6:9]
	s_setprio 0
	s_setprio 3
	v_mfma_f32_16x16x32_bf16 v[54:57], v[174:177], v[190:193], v[54:57]
	v_mfma_f32_16x16x32_bf16 v[46:49], v[182:185], v[190:193], v[46:49]
	v_mfma_f32_16x16x32_bf16 v[38:41], v[174:177], v[198:201], v[38:41]
	v_mfma_f32_16x16x32_bf16 v[30:33], v[182:185], v[198:201], v[30:33]
	v_mfma_f32_16x16x32_bf16 v[22:25], v[174:177], v[206:209], v[22:25]
	v_mfma_f32_16x16x32_bf16 v[18:21], v[182:185], v[206:209], v[18:21]
	v_mfma_f32_16x16x32_bf16 v[10:13], v[174:177], v[214:217], v[10:13]
	v_mfma_f32_16x16x32_bf16 v[2:5], v[182:185], v[214:217], v[2:5]
	v_mfma_f32_16x16x32_bf16 v[54:57], v[178:181], v[194:197], v[54:57]
	v_mfma_f32_16x16x32_bf16 v[46:49], v[186:189], v[194:197], v[46:49]
	v_mfma_f32_16x16x32_bf16 v[38:41], v[178:181], v[202:205], v[38:41]
	v_mfma_f32_16x16x32_bf16 v[30:33], v[186:189], v[202:205], v[30:33]
	v_mfma_f32_16x16x32_bf16 v[22:25], v[178:181], v[210:213], v[22:25]
	v_mfma_f32_16x16x32_bf16 v[18:21], v[186:189], v[210:213], v[18:21]
	v_mfma_f32_16x16x32_bf16 v[10:13], v[178:181], v[218:221], v[10:13]
	v_mfma_f32_16x16x32_bf16 v[2:5], v[186:189], v[218:221], v[2:5]
	s_setprio 0
	s_barrier
; #define PG8_STAGE(bufoff, gbase, voff) do { _Pragma("unroll") for (int _i = 0; _i < 2; ++_i) \
;         __builtin_amdgcn_global_load_lds((const unsigned*)((const char*)(gbase) + (voff)[_i]), (PG8_LAS unsigned*)(lds + (bufoff) + ldsw + _i * 8192), 16, 0, 0); } while (0)
; #define PG8_LDA(dst, b, h) do { _Pragma("unroll") for (int m = 0; m < 4; ++m) Frag<F8>::load(dst[m], lds + PG8_SA(b, h) + aoff + m * 2048); } while (0)
; #define PG8_LDB(dst, b, h) do { _Pragma("unroll") for (int n = 0; n < 2; ++n) Frag<F8>::load(dst[n], lds + PG8_SB(b, h) + boff + n * 2048); } while (0)
; #define PG8_MMA(ai, bj, At, Bt) do { __builtin_amdgcn_s_setprio(3); _Pragma("unroll") for (int m = 0; m < 4; ++m) _Pragma("unroll") for (int n = 0; n < 2; ++n) Frag<F8>::mma(acc[ai][bj][m][n], Bt[n], At[m]); \
;         __builtin_amdgcn_s_setprio(0); } while (0)
; #define PG8_WAIT_V(n) asm volatile("s_waitcnt vmcnt(" #n ")" ::: "memory")
; #define PG8_WAIT_L(n) asm volatile("s_waitcnt lgkmcnt(" #n ")" ::: "memory")
; #define PG8_BAR __builtin_amdgcn_s_barrier()
; #define PG8_SCHED __builtin_amdgcn_sched_barrier(0)
; template <class Epi, class Sched, bool ALIGN_EPI = false, bool SP2 = false, bool F8 = false>
; __device__ __forceinline__ void gemm_phase(PG8_LAS unsigned char* lds, const Gemm g, const Sched& S, const Epi& E) {
;     ...
;             PG8_LDB(B0, 1, 0); PG8_LDB(B1, 1, 1); PG8_SCHED; PG8_LDA(At, 1, 0); PG8_STAGE(PG8_SA(0, 1), a2 + hstep, voffA);
;             PG8_WAIT_V(8); PG8_WAIT_L(0); PG8_BAR; PG8_MMA(0, 0, At, B0); PG8_MMA(0, 1, At, B1); PG8_BAR; PG8_SCHED;
	s_add_i32 s0, 0, 0x18000
	v_add_u32_e32 v165, s0, v151
	s_add_i32 s1, 0, 0x1c000
	ds_read_b128 v[146:149], v165
	ds_read_b128 v[158:161], v165 offset:1024
	ds_read_b128 v[166:169], v165 offset:2048
	ds_read_b128 v[170:173], v165 offset:3072
	v_add_u32_e32 v165, s1, v151
	ds_read_b128 v[174:177], v165
	ds_read_b128 v[178:181], v165 offset:1024
	ds_read_b128 v[182:185], v165 offset:2048
	ds_read_b128 v[186:189], v165 offset:3072
	s_add_u32 s4, s46, 0x40000
	s_addc_u32 s5, s47, 0
	s_mov_b32 m0, s73
	v_lshl_add_u64 v[230:231], s[4:5], 0, v[136:137]
	ds_read_b128 v[190:193], v157 offset:32768
	ds_read_b128 v[194:197], v157 offset:33792
	ds_read_b128 v[198:201], v157 offset:34816
	ds_read_b128 v[202:205], v157 offset:35840
	ds_read_b128 v[206:209], v157 offset:36864
	ds_read_b128 v[210:213], v157 offset:37888
	ds_read_b128 v[214:217], v157 offset:38912
	ds_read_b128 v[218:221], v157 offset:39936
	global_load_lds_dwordx4 v[230:231], off
	v_lshl_add_u64 v[230:231], s[4:5], 0, v[132:133]
	s_mov_b32 m0, s74
	s_nop 0
	global_load_lds_dwordx4 v[230:231], off
	s_waitcnt vmcnt(8)
	s_waitcnt lgkmcnt(0)
	s_barrier
	s_setprio 3
	s_waitcnt lgkmcnt(0)
	v_mfma_f32_16x16x32_bf16 v[126:129], v[146:149], v[190:193], v[126:129]
	v_mfma_f32_16x16x32_bf16 v[118:121], v[166:169], v[190:193], v[118:121]
	v_mfma_f32_16x16x32_bf16 v[110:113], v[146:149], v[198:201], v[110:113]
	v_mfma_f32_16x16x32_bf16 v[102:105], v[166:169], v[198:201], v[102:105]
	v_mfma_f32_16x16x32_bf16 v[94:97], v[146:149], v[206:209], v[94:97]
	v_mfma_f32_16x16x32_bf16 v[86:89], v[166:169], v[206:209], v[86:89]
	v_mfma_f32_16x16x32_bf16 v[78:81], v[146:149], v[214:217], v[78:81]
	v_mfma_f32_16x16x32_bf16 v[70:73], v[166:169], v[214:217], v[70:73]
	v_mfma_f32_16x16x32_bf16 v[126:129], v[158:161], v[194:197], v[126:129]
	v_mfma_f32_16x16x32_bf16 v[118:121], v[170:173], v[194:197], v[118:121]
	v_mfma_f32_16x16x32_bf16 v[110:113], v[158:161], v[202:205], v[110:113]
	v_mfma_f32_16x16x32_bf16 v[102:105], v[170:173], v[202:205], v[102:105]
	v_mfma_f32_16x16x32_bf16 v[94:97], v[158:161], v[210:213], v[94:97]
	v_mfma_f32_16x16x32_bf16 v[86:89], v[170:173], v[210:213], v[86:89]
	v_mfma_f32_16x16x32_bf16 v[78:81], v[158:161], v[218:221], v[78:81]
	v_mfma_f32_16x16x32_bf16 v[70:73], v[170:173], v[218:221], v[70:73]
	s_setprio 0
	s_setprio 3
	v_mfma_f32_16x16x32_bf16 v[122:125], v[174:177], v[190:193], v[122:125]
	v_mfma_f32_16x16x32_bf16 v[114:117], v[182:185], v[190:193], v[114:117]
	v_mfma_f32_16x16x32_bf16 v[106:109], v[174:177], v[198:201], v[106:109]
	v_mfma_f32_16x16x32_bf16 v[98:101], v[182:185], v[198:201], v[98:101]
	v_mfma_f32_16x16x32_bf16 v[90:93], v[174:177], v[206:209], v[90:93]
	v_mfma_f32_16x16x32_bf16 v[82:85], v[182:185], v[206:209], v[82:85]
	v_mfma_f32_16x16x32_bf16 v[74:77], v[174:177], v[214:217], v[74:77]
	v_mfma_f32_16x16x32_bf16 v[66:69], v[182:185], v[214:217], v[66:69]
	v_mfma_f32_16x16x32_bf16 v[122:125], v[178:181], v[194:197], v[122:125]
	v_mfma_f32_16x16x32_bf16 v[114:117], v[186:189], v[194:197], v[114:117]
	v_mfma_f32_16x16x32_bf16 v[106:109], v[178:181], v[202:205], v[106:109]
	v_mfma_f32_16x16x32_bf16 v[98:101], v[186:189], v[202:205], v[98:101]
	v_mfma_f32_16x16x32_bf16 v[90:93], v[178:181], v[210:213], v[90:93]
	v_mfma_f32_16x16x32_bf16 v[82:85], v[186:189], v[210:213], v[82:85]
	v_mfma_f32_16x16x32_bf16 v[74:77], v[178:181], v[218:221], v[74:77]
	v_mfma_f32_16x16x32_bf16 v[66:69], v[186:189], v[218:221], v[66:69]
	s_setprio 0
	s_barrier
; #define PG8_STAGE(bufoff, gbase, voff) do { _Pragma("unroll") for (int _i = 0; _i < 2; ++_i) \
;         __builtin_amdgcn_global_load_lds((const unsigned*)((const char*)(gbase) + (voff)[_i]), (PG8_LAS unsigned*)(lds + (bufoff) + ldsw + _i * 8192), 16, 0, 0); } while (0)
; #define PG8_LDA(dst, b, h) do { _Pragma("unroll") for (int m = 0; m < 4; ++m) Frag<F8>::load(dst[m], lds + PG8_SA(b, h) + aoff + m * 2048); } while (0)
; #define PG8_MMA(ai, bj, At, Bt) do { __builtin_amdgcn_s_setprio(3); _Pragma("unroll") for (int m = 0; m < 4; ++m) _Pragma("unroll") for (int n = 0; n < 2; ++n) Frag<F8>::mma(acc[ai][bj][m][n], Bt[n], At[m]); \
;         __builtin_amdgcn_s_setprio(0); } while (0)
; #define PG8_WAIT_V(n) asm volatile("s_waitcnt vmcnt(" #n ")" ::: "memory")
; #define PG8_WAIT_L(n) asm volatile("s_waitcnt lgkmcnt(" #n ")" ::: "memory")
; #define PG8_BAR __builtin_amdgcn_s_barrier()
; #define PG8_SCHED __builtin_amdgcn_sched_barrier(0)
; template <class Epi, class Sched, bool ALIGN_EPI = false, bool SP2 = false, bool F8 = false>
; __device__ __forceinline__ void gemm_phase(PG8_LAS unsigned char* lds, const Gemm g, const Sched& S, const Epi& E) {
;     ...
;         for (int t = 0; t < nt; t += 2) {
;     ...
;             PG8_LDA(At, 1, 1); PG8_STAGE(PG8_SB(1, 0), b3, voffB); PG8_STAGE(PG8_SB(1, 1), b3 + hstep, voffB); PG8_STAGE(PG8_SA(1, 0), a3, voffA);
;             PG8_WAIT_V(8); PG8_WAIT_L(0); PG8_BAR; PG8_MMA(1, 0, At, B0); PG8_MMA(1, 1, At, B1); PG8_BAR; PG8_SCHED;
	s_add_i32 s0, s0, s49
	v_lshl_add_u64 v[222:223], v[222:223], 0, s[18:19]
	s_mov_b32 m0, s0
	ds_read_b128 v[190:193], v157 offset:49152
	ds_read_b128 v[194:197], v157 offset:50176
	ds_read_b128 v[198:201], v157 offset:51200
	ds_read_b128 v[202:205], v157 offset:52224
	ds_read_b128 v[206:209], v157 offset:53248
	ds_read_b128 v[210:213], v157 offset:54272
	ds_read_b128 v[214:217], v157 offset:55296
	ds_read_b128 v[218:221], v157 offset:56320
	global_load_lds_dwordx4 v[222:223], off
	s_add_i32 m0, s0, 0x2000
	s_add_u32 s4, s44, 0x40080
	v_lshl_add_u64 v[222:223], v[224:225], 0, s[18:19]
	s_addc_u32 s5, s45, 0
	s_add_i32 s0, s1, s49
	global_load_lds_dwordx4 v[222:223], off
	v_lshl_add_u64 v[222:223], s[4:5], 0, v[134:135]
	s_mov_b32 m0, s0
	s_nop 0
	global_load_lds_dwordx4 v[222:223], off
	v_lshl_add_u64 v[222:223], s[4:5], 0, v[130:131]
	s_add_i32 m0, s0, 0x2000
	s_nop 0
	global_load_lds_dwordx4 v[222:223], off
	v_lshl_add_u64 v[222:223], v[226:227], 0, s[18:19]
	s_mov_b32 m0, s75
	s_nop 0
	global_load_lds_dwordx4 v[222:223], off
	v_lshl_add_u64 v[222:223], v[228:229], 0, s[18:19]
	s_mov_b32 m0, s79
	s_nop 0
	global_load_lds_dwordx4 v[222:223], off
	s_waitcnt vmcnt(8)
	s_waitcnt lgkmcnt(0)
	s_barrier
	s_setprio 3
	s_waitcnt lgkmcnt(0)
	v_mfma_f32_16x16x32_bf16 v[62:65], v[146:149], v[190:193], v[62:65]
	v_mfma_f32_16x16x32_bf16 v[58:61], v[166:169], v[190:193], v[58:61]
	v_mfma_f32_16x16x32_bf16 v[50:53], v[146:149], v[198:201], v[50:53]
	v_mfma_f32_16x16x32_bf16 v[42:45], v[166:169], v[198:201], v[42:45]
	v_mfma_f32_16x16x32_bf16 v[34:37], v[146:149], v[206:209], v[34:37]
	v_mfma_f32_16x16x32_bf16 v[26:29], v[166:169], v[206:209], v[26:29]
	v_mfma_f32_16x16x32_bf16 v[14:17], v[146:149], v[214:217], v[14:17]
	v_mfma_f32_16x16x32_bf16 v[6:9], v[166:169], v[214:217], v[6:9]
	v_mfma_f32_16x16x32_bf16 v[62:65], v[158:161], v[194:197], v[62:65]
	v_mfma_f32_16x16x32_bf16 v[58:61], v[170:173], v[194:197], v[58:61]
	v_mfma_f32_16x16x32_bf16 v[50:53], v[158:161], v[202:205], v[50:53]
	v_mfma_f32_16x16x32_bf16 v[42:45], v[170:173], v[202:205], v[42:45]
	v_mfma_f32_16x16x32_bf16 v[34:37], v[158:161], v[210:213], v[34:37]
	v_mfma_f32_16x16x32_bf16 v[26:29], v[170:173], v[210:213], v[26:29]
	v_mfma_f32_16x16x32_bf16 v[14:17], v[158:161], v[218:221], v[14:17]
	v_mfma_f32_16x16x32_bf16 v[6:9], v[170:173], v[218:221], v[6:9]
	s_setprio 0
	s_setprio 3
	v_mfma_f32_16x16x32_bf16 v[54:57], v[174:177], v[190:193], v[54:57]
	v_mfma_f32_16x16x32_bf16 v[46:49], v[182:185], v[190:193], v[46:49]
	v_mfma_f32_16x16x32_bf16 v[38:41], v[174:177], v[198:201], v[38:41]
	v_mfma_f32_16x16x32_bf16 v[30:33], v[182:185], v[198:201], v[30:33]
	v_mfma_f32_16x16x32_bf16 v[22:25], v[174:177], v[206:209], v[22:25]
	v_mfma_f32_16x16x32_bf16 v[18:21], v[182:185], v[206:209], v[18:21]
	v_mfma_f32_16x16x32_bf16 v[10:13], v[174:177], v[214:217], v[10:13]
	v_mfma_f32_16x16x32_bf16 v[2:5], v[182:185], v[214:217], v[2:5]
	v_mfma_f32_16x16x32_bf16 v[54:57], v[178:181], v[194:197], v[54:57]
	v_mfma_f32_16x16x32_bf16 v[46:49], v[186:189], v[194:197], v[46:49]
	v_mfma_f32_16x16x32_bf16 v[38:41], v[178:181], v[202:205], v[38:41]
	v_mfma_f32_16x16x32_bf16 v[30:33], v[186:189], v[202:205], v[30:33]
	v_mfma_f32_16x16x32_bf16 v[22:25], v[178:181], v[210:213], v[22:25]
	v_mfma_f32_16x16x32_bf16 v[18:21], v[186:189], v[210:213], v[18:21]
	v_mfma_f32_16x16x32_bf16 v[10:13], v[178:181], v[218:221], v[10:13]
	v_mfma_f32_16x16x32_bf16 v[2:5], v[186:189], v[218:221], v[2:5]
	s_setprio 0
	s_add_i32 s86, s86, 2
	s_add_u32 s42, s42, 0x100
	s_addc_u32 s43, s43, 0
	s_add_u32 s84, s84, 0x100
	s_addc_u32 s85, s85, 0
	s_cmp_gt_u32 s86, 13
	s_cbranch_scc0 .LBB0_562

; __device__ __forceinline__ unsigned cvt_pk_bf16(float lo, float hi) { const f32x2 v = {lo, hi}; const bf16x2_t b = __builtin_convertvector(v, bf16x2_t); return __builtin_bit_cast(unsigned, b); }
; __device__ __forceinline__ unsigned long long rt() { return __builtin_amdgcn_s_memrealtime(); }
; __device__ __forceinline__ f32x2 silu_mul2(f32x2 g, f32x2 u, float c1, float k) {
;     const f32x2 a = g * c1; f32x2 e; e[0] = __builtin_amdgcn_exp2f(a[0]); e[1] = __builtin_amdgcn_exp2f(a[1]);
;     const f32x2 kk = {k, k}; const f32x2 d = __builtin_elementwise_fma(e, kk, kk); f32x2 r; r[0] = __builtin_amdgcn_rcpf(d[0]); r[1] = __builtin_amdgcn_rcpf(d[1]);
;     return (g * u) * r;
; }
;     __device__ __forceinline__ void operator()(const f32x4 (&acc)[2][2][4][2], const Unit& u, int wr, int wc, int fr, int fq) const {
;         const int row0 = u.pm * BM + wr * 64 + fr, col0 = (u.pn % pn_mod) * HALF + wc * 32 + 8 * fq;
; #pragma unroll
;         for (int ai = 0; ai < 2; ++ai)
; #pragma unroll
;             for (int m = 0; m < 4; ++m) { bf16_t* rowp = O + (size_t)(row0 + ai * HALF + m * 16) * ldc + col0;
;                 const float rs = rt ? rt[ai * HALF + wr * 64 + m * 16 + fr] : 1.0f, c1 = rs * -1.4426950408889634f, k = __builtin_amdgcn_rcpf(rs * rs);
;                 const f32x4 g0 = acc[ai][0][m][0], g1 = acc[ai][0][m][1], u0 = acc[ai][1][m][0], u1 = acc[ai][1][m][1];
;                 const f32x2 o0 = silu_mul2(g0.xy, u0.xy, c1, k), o1 = silu_mul2(g0.zw, u0.zw, c1, k), o2 = silu_mul2(g1.xy, u1.xy, c1, k), o3 = silu_mul2(g1.zw, u1.zw, c1, k);
;                 u32x4 w; w.x = cvt_pk_bf16(o0[0], o0[1]); w.y = cvt_pk_bf16(o1[0], o1[1]); w.z = cvt_pk_bf16(o2[0], o2[1]); w.w = cvt_pk_bf16(o3[0], o3[1]);
;                 *(u32x4*)rowp = w; }
.LBB0_565:
	ds_read2_b32 v[160:161], v152 offset1:16
	v_pk_mul_f32 v[124:125], v[128:129], v[124:125]
	v_pk_mul_f32 v[122:123], v[126:127], v[122:123]
	s_ashr_i32 s0, s83, 31
	s_lshr_b32 s0, s0, 12
	s_waitcnt lgkmcnt(0)
	v_mul_f32_e32 v168, 0xbfb8aa3b, v160
	v_mul_f32_e32 v159, v160, v160
	v_pk_mul_f32 v[170:171], v[126:127], v[168:169] op_sel_hi:[1,0]
	v_pk_mul_f32 v[172:173], v[128:129], v[168:169] op_sel_hi:[1,0]
	v_pk_mul_f32 v[126:127], v[118:119], v[168:169] op_sel_hi:[1,0]
	v_pk_mul_f32 v[128:129], v[120:121], v[168:169] op_sel_hi:[1,0]
	v_rcp_f32_e32 v160, v159
	v_exp_f32_e32 v170, v170
	v_exp_f32_e32 v171, v171
	v_exp_f32_e32 v172, v172
	v_exp_f32_e32 v173, v173
	v_exp_f32_e32 v126, v126
	v_exp_f32_e32 v127, v127
	v_exp_f32_e32 v128, v128
	v_exp_f32_e32 v129, v129
	s_add_i32 s0, s83, s0
	v_pk_fma_f32 v[170:171], v[170:171], v[160:161], v[160:161] op_sel_hi:[1,0,0]
	v_pk_fma_f32 v[172:173], v[172:173], v[160:161], v[160:161] op_sel_hi:[1,0,0]
	v_pk_fma_f32 v[126:127], v[126:127], v[160:161], v[160:161] op_sel_hi:[1,0,0]
	v_pk_fma_f32 v[128:129], v[128:129], v[160:161], v[160:161] op_sel_hi:[1,0,0]
	s_and_b32 s0, s0, 0x1f00000
	v_rcp_f32_e32 v170, v170
	v_rcp_f32_e32 v171, v171
	v_rcp_f32_e32 v172, v172
	v_rcp_f32_e32 v173, v173
	v_rcp_f32_e32 v126, v126
	v_rcp_f32_e32 v127, v127
	v_rcp_f32_e32 v128, v128
	v_rcp_f32_e32 v129, v129
	s_sub_i32 s0, s83, s0
	v_lshl_or_b32 v148, s0, 7, v154
	v_lshl_add_u32 v158, s40, 8, v150
	v_ashrrev_i32_e32 v149, 31, v148
	v_mov_b64_e32 v[146:147], s[16:17]
	v_pk_mul_f32 v[116:117], v[120:121], v[116:117]
	v_pk_mul_f32 v[114:115], v[118:119], v[114:115]
	v_mad_i64_i32 v[166:167], s[4:5], v158, s82, v[146:147]
	v_lshlrev_b64 v[148:149], 1, v[148:149]
	v_pk_mul_f32 v[122:123], v[122:123], v[170:171]
	v_pk_mul_f32 v[124:125], v[124:125], v[172:173]
	v_pk_mul_f32 v[118:119], v[114:115], v[126:127]
	v_pk_mul_f32 v[120:121], v[116:117], v[128:129]
	v_lshl_add_u64 v[166:167], v[166:167], 0, v[148:149]
	v_cvt_pk_bf16_f32 v114, v122, v123
	v_cvt_pk_bf16_f32 v115, v124, v125
	v_cvt_pk_bf16_f32 v116, v118, v119
	v_cvt_pk_bf16_f32 v117, v120, v121
	global_store_dwordx4 v[166:167], v[114:117], off
	v_pk_mul_f32 v[108:109], v[112:113], v[108:109]
	v_pk_mul_f32 v[106:107], v[110:111], v[106:107]
	v_mul_f32_e32 v116, 0xbfb8aa3b, v161
	v_mul_f32_e32 v117, v161, v161
	v_pk_mul_f32 v[120:121], v[110:111], v[116:117] op_sel_hi:[1,0]
	v_pk_mul_f32 v[122:123], v[112:113], v[116:117] op_sel_hi:[1,0]
	v_pk_mul_f32 v[110:111], v[102:103], v[116:117] op_sel_hi:[1,0]
	v_pk_mul_f32 v[112:113], v[104:105], v[116:117] op_sel_hi:[1,0]
	v_rcp_f32_e32 v118, v117
	v_exp_f32_e32 v120, v120
	v_exp_f32_e32 v121, v121
	v_exp_f32_e32 v122, v122
	v_exp_f32_e32 v123, v123
	v_exp_f32_e32 v110, v110
	v_exp_f32_e32 v111, v111
	v_exp_f32_e32 v112, v112
	v_exp_f32_e32 v113, v113
	v_pk_fma_f32 v[120:121], v[120:121], v[118:119], v[118:119] op_sel_hi:[1,0,0]
	v_pk_fma_f32 v[122:123], v[122:123], v[118:119], v[118:119] op_sel_hi:[1,0,0]
	v_pk_fma_f32 v[110:111], v[110:111], v[118:119], v[118:119] op_sel_hi:[1,0,0]
	v_pk_fma_f32 v[112:113], v[112:113], v[118:119], v[118:119] op_sel_hi:[1,0,0]
	v_rcp_f32_e32 v120, v120
	v_rcp_f32_e32 v121, v121
	v_rcp_f32_e32 v122, v122
	v_rcp_f32_e32 v123, v123
	v_rcp_f32_e32 v110, v110
	v_rcp_f32_e32 v111, v111
	v_rcp_f32_e32 v112, v112
	v_rcp_f32_e32 v113, v113
	v_or_b32_e32 v114, 16, v158
	v_pk_mul_f32 v[100:101], v[104:105], v[100:101]
	v_pk_mul_f32 v[98:99], v[102:103], v[98:99]
	v_mad_i64_i32 v[114:115], s[4:5], v114, s82, v[146:147]
	v_pk_mul_f32 v[106:107], v[106:107], v[120:121]
	v_pk_mul_f32 v[108:109], v[108:109], v[122:123]
	v_pk_mul_f32 v[102:103], v[98:99], v[110:111]
	v_pk_mul_f32 v[104:105], v[100:101], v[112:113]
	v_lshl_add_u64 v[114:115], v[114:115], 0, v[148:149]
	v_cvt_pk_bf16_f32 v98, v106, v107
	v_cvt_pk_bf16_f32 v99, v108, v109
	v_cvt_pk_bf16_f32 v100, v102, v103
	v_cvt_pk_bf16_f32 v101, v104, v105
	global_store_dwordx4 v[114:115], v[98:101], off
	ds_read2_b32 v[98:99], v152 offset0:32 offset1:48
	v_pk_mul_f32 v[92:93], v[96:97], v[92:93]
	v_pk_mul_f32 v[90:91], v[94:95], v[90:91]
	v_or_b32_e32 v100, 32, v158
	v_pk_mul_f32 v[84:85], v[88:89], v[84:85]
	s_waitcnt lgkmcnt(0)
	v_mul_f32_e32 v102, 0xbfb8aa3b, v98
	v_mul_f32_e32 v98, v98, v98
	v_pk_mul_f32 v[104:105], v[94:95], v[102:103] op_sel_hi:[1,0]
	v_pk_mul_f32 v[106:107], v[96:97], v[102:103] op_sel_hi:[1,0]
	v_pk_mul_f32 v[94:95], v[86:87], v[102:103] op_sel_hi:[1,0]
	v_pk_mul_f32 v[96:97], v[88:89], v[102:103] op_sel_hi:[1,0]
	v_rcp_f32_e32 v98, v98
	v_exp_f32_e32 v104, v104
	v_exp_f32_e32 v105, v105
	v_exp_f32_e32 v106, v106
	v_exp_f32_e32 v107, v107
	v_exp_f32_e32 v94, v94
	v_exp_f32_e32 v95, v95
	v_exp_f32_e32 v96, v96
	v_exp_f32_e32 v97, v97
	v_pk_fma_f32 v[104:105], v[104:105], v[98:99], v[98:99] op_sel_hi:[1,0,0]
	v_pk_fma_f32 v[106:107], v[106:107], v[98:99], v[98:99] op_sel_hi:[1,0,0]
	v_pk_fma_f32 v[94:95], v[94:95], v[98:99], v[98:99] op_sel_hi:[1,0,0]
	v_pk_fma_f32 v[96:97], v[96:97], v[98:99], v[98:99] op_sel_hi:[1,0,0]
	v_rcp_f32_e32 v104, v104
	v_rcp_f32_e32 v105, v105
	v_rcp_f32_e32 v106, v106
	v_rcp_f32_e32 v107, v107
	v_rcp_f32_e32 v94, v94
	v_rcp_f32_e32 v95, v95
	v_rcp_f32_e32 v96, v96
	v_rcp_f32_e32 v97, v97
	v_pk_mul_f32 v[82:83], v[86:87], v[82:83]
	v_mad_i64_i32 v[100:101], s[4:5], v100, s82, v[146:147]
	v_pk_mul_f32 v[90:91], v[90:91], v[104:105]
	v_pk_mul_f32 v[92:93], v[92:93], v[106:107]
	v_pk_mul_f32 v[86:87], v[82:83], v[94:95]
	v_pk_mul_f32 v[88:89], v[84:85], v[96:97]
	v_lshl_add_u64 v[100:101], v[100:101], 0, v[148:149]
	v_cvt_pk_bf16_f32 v82, v90, v91
	v_cvt_pk_bf16_f32 v83, v92, v93
	v_cvt_pk_bf16_f32 v84, v86, v87
; __device__ __forceinline__ unsigned cvt_pk_bf16(float lo, float hi) { const f32x2 v = {lo, hi}; const bf16x2_t b = __builtin_convertvector(v, bf16x2_t); return __builtin_bit_cast(unsigned, b); }
; __device__ __forceinline__ unsigned long long rt() { return __builtin_amdgcn_s_memrealtime(); }
; __device__ __forceinline__ f32x2 silu_mul2(f32x2 g, f32x2 u, float c1, float k) {
;     const f32x2 a = g * c1; f32x2 e; e[0] = __builtin_amdgcn_exp2f(a[0]); e[1] = __builtin_amdgcn_exp2f(a[1]);
;     const f32x2 kk = {k, k}; const f32x2 d = __builtin_elementwise_fma(e, kk, kk); f32x2 r; r[0] = __builtin_amdgcn_rcpf(d[0]); r[1] = __builtin_amdgcn_rcpf(d[1]);
;     return (g * u) * r;
; }
;     __device__ __forceinline__ void operator()(const f32x4 (&acc)[2][2][4][2], const Unit& u, int wr, int wc, int fr, int fq) const {
;         const int row0 = u.pm * BM + wr * 64 + fr, col0 = (u.pn % pn_mod) * HALF + wc * 32 + 8 * fq;
; #pragma unroll
;         for (int ai = 0; ai < 2; ++ai)
; #pragma unroll
;             for (int m = 0; m < 4; ++m) { bf16_t* rowp = O + (size_t)(row0 + ai * HALF + m * 16) * ldc + col0;
;                 const float rs = rt ? rt[ai * HALF + wr * 64 + m * 16 + fr] : 1.0f, c1 = rs * -1.4426950408889634f, k = __builtin_amdgcn_rcpf(rs * rs);
;                 const f32x4 g0 = acc[ai][0][m][0], g1 = acc[ai][0][m][1], u0 = acc[ai][1][m][0], u1 = acc[ai][1][m][1];
;                 const f32x2 o0 = silu_mul2(g0.xy, u0.xy, c1, k), o1 = silu_mul2(g0.zw, u0.zw, c1, k), o2 = silu_mul2(g1.xy, u1.xy, c1, k), o3 = silu_mul2(g1.zw, u1.zw, c1, k);
;                 u32x4 w; w.x = cvt_pk_bf16(o0[0], o0[1]); w.y = cvt_pk_bf16(o1[0], o1[1]); w.z = cvt_pk_bf16(o2[0], o2[1]); w.w = cvt_pk_bf16(o3[0], o3[1]);
;                 *(u32x4*)rowp = w; }
	v_cvt_pk_bf16_f32 v85, v88, v89
	global_store_dwordx4 v[100:101], v[82:85], off
	v_pk_mul_f32 v[76:77], v[80:81], v[76:77]
	v_pk_mul_f32 v[74:75], v[78:79], v[74:75]
	v_mul_f32_e32 v84, 0xbfb8aa3b, v99
	v_mul_f32_e32 v85, v99, v99
	v_pk_mul_f32 v[88:89], v[78:79], v[84:85] op_sel_hi:[1,0]
	v_pk_mul_f32 v[90:91], v[80:81], v[84:85] op_sel_hi:[1,0]
	v_pk_mul_f32 v[78:79], v[70:71], v[84:85] op_sel_hi:[1,0]
	v_pk_mul_f32 v[80:81], v[72:73], v[84:85] op_sel_hi:[1,0]
	v_rcp_f32_e32 v86, v85
	v_exp_f32_e32 v88, v88
	v_exp_f32_e32 v89, v89
	v_exp_f32_e32 v90, v90
	v_exp_f32_e32 v91, v91
	v_exp_f32_e32 v78, v78
	v_exp_f32_e32 v79, v79
	v_exp_f32_e32 v80, v80
	v_exp_f32_e32 v81, v81
	v_pk_fma_f32 v[88:89], v[88:89], v[86:87], v[86:87] op_sel_hi:[1,0,0]
	v_pk_fma_f32 v[90:91], v[90:91], v[86:87], v[86:87] op_sel_hi:[1,0,0]
	v_pk_fma_f32 v[78:79], v[78:79], v[86:87], v[86:87] op_sel_hi:[1,0,0]
	v_pk_fma_f32 v[80:81], v[80:81], v[86:87], v[86:87] op_sel_hi:[1,0,0]
	v_rcp_f32_e32 v88, v88
	v_rcp_f32_e32 v89, v89
	v_rcp_f32_e32 v90, v90
	v_rcp_f32_e32 v91, v91
	v_rcp_f32_e32 v78, v78
	v_rcp_f32_e32 v79, v79
	v_rcp_f32_e32 v80, v80
	v_rcp_f32_e32 v81, v81
	v_or_b32_e32 v82, 48, v158
	v_pk_mul_f32 v[68:69], v[72:73], v[68:69]
	v_pk_mul_f32 v[66:67], v[70:71], v[66:67]
	v_mad_i64_i32 v[82:83], s[4:5], v82, s82, v[146:147]
	v_pk_mul_f32 v[74:75], v[74:75], v[88:89]
	v_pk_mul_f32 v[76:77], v[76:77], v[90:91]
	v_pk_mul_f32 v[70:71], v[66:67], v[78:79]
	v_pk_mul_f32 v[72:73], v[68:69], v[80:81]
	v_lshl_add_u64 v[82:83], v[82:83], 0, v[148:149]
	v_cvt_pk_bf16_f32 v66, v74, v75
	v_cvt_pk_bf16_f32 v67, v76, v77
	v_cvt_pk_bf16_f32 v68, v70, v71
	v_cvt_pk_bf16_f32 v69, v72, v73
	global_store_dwordx4 v[82:83], v[66:69], off
	ds_read_b32 v69, v153
	ds_read_b32 v71, v152 offset:704
	v_pk_mul_f32 v[56:57], v[64:65], v[56:57]
	v_pk_mul_f32 v[54:55], v[62:63], v[54:55]
	v_add_u32_e32 v66, 0x80, v158
	s_waitcnt lgkmcnt(0)
	v_mul_f32_e32 v68, 0xbfb8aa3b, v69
	v_mul_f32_e32 v69, v69, v69
	v_pk_mul_f32 v[72:73], v[62:63], v[68:69] op_sel_hi:[1,0]
	v_pk_mul_f32 v[74:75], v[64:65], v[68:69] op_sel_hi:[1,0]
	v_pk_mul_f32 v[62:63], v[58:59], v[68:69] op_sel_hi:[1,0]
	v_pk_mul_f32 v[64:65], v[60:61], v[68:69] op_sel_hi:[1,0]
	v_rcp_f32_e32 v70, v69
	v_exp_f32_e32 v72, v72
	v_exp_f32_e32 v73, v73
	v_exp_f32_e32 v74, v74
	v_exp_f32_e32 v75, v75
	v_exp_f32_e32 v62, v62
	v_exp_f32_e32 v63, v63
	v_exp_f32_e32 v64, v64
	v_exp_f32_e32 v65, v65
	v_pk_fma_f32 v[72:73], v[72:73], v[70:71], v[70:71] op_sel_hi:[1,0,0]
	v_pk_fma_f32 v[74:75], v[74:75], v[70:71], v[70:71] op_sel_hi:[1,0,0]
	v_pk_fma_f32 v[62:63], v[62:63], v[70:71], v[70:71] op_sel_hi:[1,0,0]
	v_pk_fma_f32 v[64:65], v[64:65], v[70:71], v[70:71] op_sel_hi:[1,0,0]
	v_rcp_f32_e32 v72, v72
	v_rcp_f32_e32 v73, v73
	v_rcp_f32_e32 v74, v74
	v_rcp_f32_e32 v75, v75
	v_rcp_f32_e32 v62, v62
	v_rcp_f32_e32 v63, v63
	v_rcp_f32_e32 v64, v64
	v_rcp_f32_e32 v65, v65
	v_pk_mul_f32 v[48:49], v[60:61], v[48:49]
	v_pk_mul_f32 v[46:47], v[58:59], v[46:47]
	v_mad_i64_i32 v[66:67], s[4:5], v66, s82, v[146:147]
	v_pk_mul_f32 v[54:55], v[54:55], v[72:73]
	v_pk_mul_f32 v[56:57], v[56:57], v[74:75]
	v_pk_mul_f32 v[58:59], v[46:47], v[62:63]
	v_pk_mul_f32 v[60:61], v[48:49], v[64:65]
	v_lshl_add_u64 v[66:67], v[66:67], 0, v[148:149]
	v_cvt_pk_bf16_f32 v46, v54, v55
	v_cvt_pk_bf16_f32 v47, v56, v57
	v_cvt_pk_bf16_f32 v48, v58, v59
	v_cvt_pk_bf16_f32 v49, v60, v61
	global_store_dwordx4 v[66:67], v[46:49], off
	ds_read2_b32 v[46:47], v152 offset0:144 offset1:160
	v_pk_mul_f32 v[40:41], v[52:53], v[40:41]
	v_pk_mul_f32 v[38:39], v[50:51], v[38:39]
	v_add_u32_e32 v48, 0x90, v158
	v_pk_mul_f32 v[32:33], v[44:45], v[32:33]
	s_waitcnt lgkmcnt(0)
; #define PG8_BAR __builtin_amdgcn_s_barrier()
; __device__ __forceinline__ unsigned long long rt() { return __builtin_amdgcn_s_memrealtime(); }
; __device__ __forceinline__ f32x2 silu_mul2(f32x2 g, f32x2 u, float c1, float k) {
;     const f32x2 a = g * c1; f32x2 e; e[0] = __builtin_amdgcn_exp2f(a[0]); e[1] = __builtin_amdgcn_exp2f(a[1]);
;     const f32x2 kk = {k, k}; const f32x2 d = __builtin_elementwise_fma(e, kk, kk); f32x2 r; r[0] = __builtin_amdgcn_rcpf(d[0]); r[1] = __builtin_amdgcn_rcpf(d[1]);
;     return (g * u) * r;
; }
;     __device__ __forceinline__ void operator()(const f32x4 (&acc)[2][2][4][2], const Unit& u, int wr, int wc, int fr, int fq) const {
;         const int row0 = u.pm * BM + wr * 64 + fr, col0 = (u.pn % pn_mod) * HALF + wc * 32 + 8 * fq;
; #pragma unroll
;         for (int ai = 0; ai < 2; ++ai)
; #pragma unroll
;             for (int m = 0; m < 4; ++m) { bf16_t* rowp = O + (size_t)(row0 + ai * HALF + m * 16) * ldc + col0;
;                 const float rs = rt ? rt[ai * HALF + wr * 64 + m * 16 + fr] : 1.0f, c1 = rs * -1.4426950408889634f, k = __builtin_amdgcn_rcpf(rs * rs);
;                 const f32x4 g0 = acc[ai][0][m][0], g1 = acc[ai][0][m][1], u0 = acc[ai][1][m][0], u1 = acc[ai][1][m][1];
;                 const f32x2 o0 = silu_mul2(g0.xy, u0.xy, c1, k), o1 = silu_mul2(g0.zw, u0.zw, c1, k), o2 = silu_mul2(g1.xy, u1.xy, c1, k), o3 = silu_mul2(g1.zw, u1.zw, c1, k);
;                 u32x4 w; w.x = cvt_pk_bf16(o0[0], o0[1]); w.y = cvt_pk_bf16(o1[0], o1[1]); w.z = cvt_pk_bf16(o2[0], o2[1]); w.w = cvt_pk_bf16(o3[0], o3[1]);
;                 *(u32x4*)rowp = w; }
; template <class Epi, class Sched, bool ALIGN_EPI = false, bool SP2 = false, bool F8 = false>
; __device__ __forceinline__ void gemm_phase(PG8_LAS unsigned char* lds, const Gemm g, const Sched& S, const Epi& E) {
;     ...
;         if constexpr (!Epi::AFTER_DRAIN) { E(acc, cur, wr, wc, fr, fq); S.done(cur); }
;         if (!has_next) break;
; #pragma unroll
;         for (int a = 0; a < 2; ++a)
; #pragma unroll
;             for (int b = 0; b < 2; ++b)
; #pragma unroll
;                 for (int m = 0; m < 4; ++m)
; #pragma unroll
;                     for (int n = 0; n < 2; ++n) acc[a][b][m][n] = (f32x4){0.f, 0.f, 0.f, 0.f};
;         cur = nxt; cA = nA; cB = nB; ++ui;
;         if constexpr (ALIGN_EPI) { if (wr == 1) PG8_BAR; }
	v_mul_f32_e32 v54, 0xbfb8aa3b, v46
	v_mul_f32_e32 v46, v46, v46
	v_pk_mul_f32 v[56:57], v[50:51], v[54:55] op_sel_hi:[1,0]
	v_pk_mul_f32 v[58:59], v[52:53], v[54:55] op_sel_hi:[1,0]
	v_pk_mul_f32 v[50:51], v[42:43], v[54:55] op_sel_hi:[1,0]
	v_pk_mul_f32 v[52:53], v[44:45], v[54:55] op_sel_hi:[1,0]
	v_rcp_f32_e32 v46, v46
	v_exp_f32_e32 v56, v56
	v_exp_f32_e32 v57, v57
	v_exp_f32_e32 v58, v58
	v_exp_f32_e32 v59, v59
	v_exp_f32_e32 v50, v50
	v_exp_f32_e32 v51, v51
	v_exp_f32_e32 v52, v52
	v_exp_f32_e32 v53, v53
	v_pk_fma_f32 v[56:57], v[56:57], v[46:47], v[46:47] op_sel_hi:[1,0,0]
	v_pk_fma_f32 v[58:59], v[58:59], v[46:47], v[46:47] op_sel_hi:[1,0,0]
	v_pk_fma_f32 v[50:51], v[50:51], v[46:47], v[46:47] op_sel_hi:[1,0,0]
	v_pk_fma_f32 v[52:53], v[52:53], v[46:47], v[46:47] op_sel_hi:[1,0,0]
	v_rcp_f32_e32 v56, v56
	v_rcp_f32_e32 v57, v57
	v_rcp_f32_e32 v58, v58
	v_rcp_f32_e32 v59, v59
	v_rcp_f32_e32 v50, v50
	v_rcp_f32_e32 v51, v51
	v_rcp_f32_e32 v52, v52
	v_rcp_f32_e32 v53, v53
	v_pk_mul_f32 v[30:31], v[42:43], v[30:31]
	v_mad_i64_i32 v[48:49], s[4:5], v48, s82, v[146:147]
	v_pk_mul_f32 v[38:39], v[38:39], v[56:57]
	v_pk_mul_f32 v[40:41], v[40:41], v[58:59]
	v_pk_mul_f32 v[42:43], v[30:31], v[50:51]
	v_pk_mul_f32 v[44:45], v[32:33], v[52:53]
	v_lshl_add_u64 v[48:49], v[48:49], 0, v[148:149]
	v_cvt_pk_bf16_f32 v30, v38, v39
	v_cvt_pk_bf16_f32 v31, v40, v41
	v_cvt_pk_bf16_f32 v32, v42, v43
	v_cvt_pk_bf16_f32 v33, v44, v45
	global_store_dwordx4 v[48:49], v[30:33], off
	v_pk_mul_f32 v[22:23], v[34:35], v[22:23]
	v_pk_mul_f32 v[24:25], v[36:37], v[24:25]
	v_mul_f32_e32 v32, 0xbfb8aa3b, v47
	v_mul_f32_e32 v33, v47, v47
	v_rcp_f32_e32 v38, v33
	v_pk_mul_f32 v[40:41], v[34:35], v[32:33] op_sel_hi:[1,0]
	v_pk_mul_f32 v[42:43], v[36:37], v[32:33] op_sel_hi:[1,0]
	v_pk_mul_f32 v[34:35], v[26:27], v[32:33] op_sel_hi:[1,0]
	v_pk_mul_f32 v[32:33], v[28:29], v[32:33] op_sel_hi:[1,0]
	v_exp_f32_e32 v40, v40
	v_exp_f32_e32 v41, v41
	v_exp_f32_e32 v42, v42
	v_exp_f32_e32 v43, v43
	v_exp_f32_e32 v34, v34
	v_exp_f32_e32 v35, v35
	v_exp_f32_e32 v32, v32
	v_exp_f32_e32 v33, v33
	v_pk_fma_f32 v[40:41], v[40:41], v[38:39], v[38:39] op_sel_hi:[1,0,0]
	v_pk_fma_f32 v[42:43], v[42:43], v[38:39], v[38:39] op_sel_hi:[1,0,0]
	v_pk_fma_f32 v[34:35], v[34:35], v[38:39], v[38:39] op_sel_hi:[1,0,0]
	v_pk_fma_f32 v[32:33], v[32:33], v[38:39], v[38:39] op_sel_hi:[1,0,0]
	v_rcp_f32_e32 v40, v40
	v_rcp_f32_e32 v41, v41
	v_rcp_f32_e32 v42, v42
	v_rcp_f32_e32 v43, v43
	v_rcp_f32_e32 v34, v34
	v_rcp_f32_e32 v35, v35
	v_rcp_f32_e32 v32, v32
	v_rcp_f32_e32 v33, v33
	v_add_u32_e32 v30, 0xa0, v158
	v_pk_mul_f32 v[20:21], v[28:29], v[20:21]
	v_pk_mul_f32 v[18:19], v[26:27], v[18:19]
	v_mad_i64_i32 v[30:31], s[4:5], v30, s82, v[146:147]
	v_pk_mul_f32 v[22:23], v[22:23], v[40:41]
	v_pk_mul_f32 v[24:25], v[24:25], v[42:43]
	v_pk_mul_f32 v[26:27], v[18:19], v[34:35]
	v_pk_mul_f32 v[28:29], v[20:21], v[32:33]
	v_lshl_add_u64 v[30:31], v[30:31], 0, v[148:149]
	v_cvt_pk_bf16_f32 v18, v22, v23
	v_cvt_pk_bf16_f32 v19, v24, v25
	v_cvt_pk_bf16_f32 v20, v26, v27
	v_cvt_pk_bf16_f32 v21, v28, v29
	global_store_dwordx4 v[30:31], v[18:21], off
	v_pk_mul_f32 v[12:13], v[16:17], v[12:13]
	v_pk_mul_f32 v[10:11], v[14:15], v[10:11]
	v_mul_f32_e32 v20, 0xbfb8aa3b, v71
	v_mul_f32_e32 v21, v71, v71
	v_pk_mul_f32 v[24:25], v[14:15], v[20:21] op_sel_hi:[1,0]
	v_pk_mul_f32 v[26:27], v[16:17], v[20:21] op_sel_hi:[1,0]
	v_pk_mul_f32 v[14:15], v[6:7], v[20:21] op_sel_hi:[1,0]
	v_pk_mul_f32 v[16:17], v[8:9], v[20:21] op_sel_hi:[1,0]
	v_rcp_f32_e32 v22, v21
	v_exp_f32_e32 v24, v24
	v_exp_f32_e32 v25, v25
	v_exp_f32_e32 v26, v26
	v_exp_f32_e32 v27, v27
	v_exp_f32_e32 v14, v14
	v_exp_f32_e32 v15, v15
	v_exp_f32_e32 v16, v16
	v_exp_f32_e32 v17, v17
	v_pk_fma_f32 v[24:25], v[24:25], v[22:23], v[22:23] op_sel_hi:[1,0,0]
	v_pk_fma_f32 v[26:27], v[26:27], v[22:23], v[22:23] op_sel_hi:[1,0,0]
	v_pk_fma_f32 v[14:15], v[14:15], v[22:23], v[22:23] op_sel_hi:[1,0,0]
	v_pk_fma_f32 v[16:17], v[16:17], v[22:23], v[22:23] op_sel_hi:[1,0,0]
	v_rcp_f32_e32 v24, v24
	v_rcp_f32_e32 v25, v25
	v_rcp_f32_e32 v26, v26
	v_rcp_f32_e32 v27, v27
	v_rcp_f32_e32 v14, v14
	v_rcp_f32_e32 v15, v15
	v_rcp_f32_e32 v16, v16
	v_rcp_f32_e32 v17, v17
	v_add_u32_e32 v18, 0xb0, v158
	v_pk_mul_f32 v[4:5], v[8:9], v[4:5]
	v_pk_mul_f32 v[2:3], v[6:7], v[2:3]
	v_mad_i64_i32 v[18:19], s[4:5], v18, s82, v[146:147]
	v_pk_mul_f32 v[10:11], v[10:11], v[24:25]
	v_pk_mul_f32 v[12:13], v[12:13], v[26:27]
	v_pk_mul_f32 v[6:7], v[2:3], v[14:15]
	v_pk_mul_f32 v[8:9], v[4:5], v[16:17]
	v_lshl_add_u64 v[18:19], v[18:19], 0, v[148:149]
	v_cvt_pk_bf16_f32 v2, v10, v11
	v_cvt_pk_bf16_f32 v3, v12, v13
	v_cvt_pk_bf16_f32 v4, v6, v7
	v_cvt_pk_bf16_f32 v5, v8, v9
	s_andn2_b64 vcc, exec, s[8:9]
	s_mov_b64 s[8:9], -1
	global_store_dwordx4 v[18:19], v[2:5], off
	s_barrier
	s_cbranch_vccnz .LBB0_558
	s_andn2_b64 vcc, exec, s[14:15]
	s_cbranch_vccnz .LBB0_557
	s_barrier
	s_branch .LBB0_557

; #define PG8_STAGE(bufoff, gbase, voff) do { _Pragma("unroll") for (int _i = 0; _i < 2; ++_i) \
;         __builtin_amdgcn_global_load_lds((const unsigned*)((const char*)(gbase) + (voff)[_i]), (PG8_LAS unsigned*)(lds + (bufoff) + ldsw + _i * 8192), 16, 0, 0); } while (0)
; #define PG8_LDA(dst, b, h) do { _Pragma("unroll") for (int m = 0; m < 4; ++m) Frag<F8>::load(dst[m], lds + PG8_SA(b, h) + aoff + m * 2048); } while (0)
; #define PG8_LDB(dst, b, h) do { _Pragma("unroll") for (int n = 0; n < 2; ++n) Frag<F8>::load(dst[n], lds + PG8_SB(b, h) + boff + n * 2048); } while (0)
; #define PG8_MMA(ai, bj, At, Bt) do { __builtin_amdgcn_s_setprio(3); _Pragma("unroll") for (int m = 0; m < 4; ++m) _Pragma("unroll") for (int n = 0; n < 2; ++n) Frag<F8>::mma(acc[ai][bj][m][n], Bt[n], At[m]); \
;         __builtin_amdgcn_s_setprio(0); } while (0)
; #define PG8_WAIT_V(n) asm volatile("s_waitcnt vmcnt(" #n ")" ::: "memory")
; #define PG8_BAR __builtin_amdgcn_s_barrier()
; template <class Epi, class Sched, bool ALIGN_EPI = false, bool SP2 = false, bool F8 = false>
; __device__ __forceinline__ void gemm_phase(PG8_LAS unsigned char* lds, const Gemm g, const Sched& S, const Epi& E) {
;     ...
;         const bool has_next = S.next(ui + 1, nxt);
;         const char* nA = has_next ? (const char*)g.A + (size_t)nxt.pm * tstep + nxt.ko : cA; const char* nB = has_next ? (const char*)g.Bt + (size_t)nxt.pn * tstep + nxt.ko : cB;
;         for (int t = 0; t < nt; t += 2) {
;             const bool last = (t == nt - 2);
;             const char* a1 = cA + (size_t)(t + 1) * kstep;
;             const char* a2 = last ? nA : cA + (size_t)(t + 2) * kstep; const char* b2 = last ? nB : cB + (size_t)(t + 2) * kstep;
;             const char* a3 = a2 + kstep; const char* b3 = b2 + kstep;
;             if (last && has_next) S.a_ready(nxt);
;             if constexpr (SP2) {
;             PG8_LDB(B0, 0, 0); PG8_LDB(B1, 0, 1); PG8_SCHED; PG8_LDA(At, 0, 0); PG8_STAGE(PG8_SA(1, 1), a1 + hstep, voffA);
;             PG8_WAIT_V(8); PG8_WAIT_L(0); PG8_BAR; PG8_MMA(0, 0, At, B0); PG8_MMA(0, 1, At, B1); PG8_BAR; PG8_SCHED;
;             PG8_LDA(At, 0, 1); PG8_STAGE(PG8_SB(0, 0), b2, voffB); PG8_STAGE(PG8_SB(0, 1), b2 + hstep, voffB); PG8_STAGE(PG8_SA(0, 0), a2, voffA);
;             PG8_WAIT_V(8); PG8_WAIT_L(0); PG8_BAR; PG8_MMA(1, 0, At, B0); PG8_MMA(1, 1, At, B1); PG8_BAR; PG8_SCHED;
.LBB0_801:
	s_ashr_i32 s25, s24, 31
	s_lshl_b64 s[4:5], s[24:25], 18
	s_add_u32 s36, s49, s4
	s_addc_u32 s37, s50, s5
	s_and_b64 s[4:5], s[8:9], exec
	s_cselect_b32 s25, s37, s43
	s_cselect_b32 s83, s36, s42
	s_ashr_i32 s31, s30, 31
	s_lshl_b64 s[4:5], s[30:31], 18
	s_add_u32 s38, s51, s4
	s_addc_u32 s39, s52, s5
	s_and_b64 s[4:5], s[8:9], exec
	s_cselect_b32 s31, s39, s45
	s_cselect_b32 s84, s38, s44
	s_add_u32 s42, s42, 0x20080
	s_addc_u32 s43, s43, 0
	s_add_u32 s85, s44, 0x100
	s_addc_u32 s86, s45, 0
	s_mov_b32 s87, -2
	ds_read_b128 v[18:21], v194
	ds_read_b128 v[22:25], v194 offset:1024
	ds_read_b128 v[26:29], v194 offset:2048
	ds_read_b128 v[30:33], v194 offset:3072
	ds_read_b128 v[2:5], v195
	ds_read_b128 v[6:9], v195 offset:1024
	ds_read_b128 v[10:13], v195 offset:2048
	ds_read_b128 v[14:17], v195 offset:3072
	s_add_u32 s0, s42, 0xfffe0080
	s_addc_u32 s1, s43, -1
	s_cmp_eq_u32 s87, 4
	s_cselect_b32 s47, s25, s1
	s_cselect_b32 s46, s83, s0
	s_cselect_b32 s45, s31, s86
	s_cselect_b32 s44, s84, s85
	v_lshl_add_u64 v[224:225], s[42:43], 0, v[174:175]
	s_add_i32 m0, s41, 0xc000
	ds_read_b128 v[182:185], v196
	ds_read_b128 v[186:189], v196 offset:1024
	ds_read_b128 v[200:203], v196 offset:2048
	ds_read_b128 v[204:207], v196 offset:3072
	ds_read_b128 v[208:211], v196 offset:4096
	ds_read_b128 v[212:215], v196 offset:5120
	ds_read_b128 v[216:219], v196 offset:6144
	ds_read_b128 v[220:223], v196 offset:7168
	global_load_lds_dwordx4 v[224:225], off
	v_lshl_add_u64 v[224:225], s[42:43], 0, v[176:177]
	s_add_i32 m0, s41, 0xe000
	s_nop 0
	global_load_lds_dwordx4 v[224:225], off
	s_waitcnt vmcnt(8)
	s_waitcnt lgkmcnt(0)
	s_barrier
	s_setprio 3
	s_waitcnt lgkmcnt(0)
	v_mfma_scale_f32_16x16x128_f8f6f4 v[158:161], v[18:25], v[182:189], 0, v197, v197 op_sel_hi:[0, 0, 0]
	v_mfma_scale_f32_16x16x128_f8f6f4 v[154:157], v[26:33], v[182:189], 0, v197, v197 op_sel_hi:[0, 0, 0]
	v_mfma_scale_f32_16x16x128_f8f6f4 v[150:153], v[18:25], v[200:207], 0, v197, v197 op_sel_hi:[0, 0, 0]
	v_mfma_scale_f32_16x16x128_f8f6f4 v[142:145], v[26:33], v[200:207], 0, v197, v197 op_sel_hi:[0, 0, 0]
	v_mfma_scale_f32_16x16x128_f8f6f4 v[130:133], v[18:25], v[208:215], 0, v197, v197 op_sel_hi:[0, 0, 0]
	v_mfma_scale_f32_16x16x128_f8f6f4 v[122:125], v[26:33], v[208:215], 0, v197, v197 op_sel_hi:[0, 0, 0]
	v_mfma_scale_f32_16x16x128_f8f6f4 v[118:121], v[18:25], v[216:223], 0, v197, v197 op_sel_hi:[0, 0, 0]
	v_mfma_scale_f32_16x16x128_f8f6f4 v[110:113], v[26:33], v[216:223], 0, v197, v197 op_sel_hi:[0, 0, 0]
	s_setprio 0
	s_setprio 3
	v_mfma_scale_f32_16x16x128_f8f6f4 v[146:149], v[2:9], v[182:189], 0, v197, v197 op_sel_hi:[0, 0, 0]
	v_mfma_scale_f32_16x16x128_f8f6f4 v[138:141], v[10:17], v[182:189], 0, v197, v197 op_sel_hi:[0, 0, 0]
	v_mfma_scale_f32_16x16x128_f8f6f4 v[134:137], v[2:9], v[200:207], 0, v197, v197 op_sel_hi:[0, 0, 0]
	v_mfma_scale_f32_16x16x128_f8f6f4 v[126:129], v[10:17], v[200:207], 0, v197, v197 op_sel_hi:[0, 0, 0]
	v_mfma_scale_f32_16x16x128_f8f6f4 v[114:117], v[2:9], v[208:215], 0, v197, v197 op_sel_hi:[0, 0, 0]
	v_mfma_scale_f32_16x16x128_f8f6f4 v[106:109], v[10:17], v[208:215], 0, v197, v197 op_sel_hi:[0, 0, 0]
	v_mfma_scale_f32_16x16x128_f8f6f4 v[102:105], v[2:9], v[216:223], 0, v197, v197 op_sel_hi:[0, 0, 0]
	v_mfma_scale_f32_16x16x128_f8f6f4 v[98:101], v[10:17], v[216:223], 0, v197, v197 op_sel_hi:[0, 0, 0]
	s_setprio 0
	s_barrier
	s_add_i32 s0, s79, s48
	v_lshl_add_u64 v[182:183], s[44:45], 0, v[170:171]
	s_mov_b32 m0, s0
	ds_read_b128 v[200:203], v196 offset:16384
	ds_read_b128 v[204:207], v196 offset:17408
	ds_read_b128 v[208:211], v196 offset:18432
	ds_read_b128 v[212:215], v196 offset:19456
	ds_read_b128 v[216:219], v196 offset:20480
	ds_read_b128 v[220:223], v196 offset:21504
	ds_read_b128 v[224:227], v196 offset:22528
	ds_read_b128 v[228:231], v196 offset:23552
	global_load_lds_dwordx4 v[182:183], off
	s_add_i32 m0, s0, 0x2000
	s_add_u32 s4, s44, 0x20000
	v_lshl_add_u64 v[184:185], s[44:45], 0, v[166:167]
	s_addc_u32 s5, s45, 0
	s_add_i32 s0, s80, s48
	global_load_lds_dwordx4 v[184:185], off
	v_lshl_add_u64 v[186:187], s[4:5], 0, v[170:171]
	s_mov_b32 m0, s0
	v_lshl_add_u64 v[188:189], s[46:47], 0, v[168:169]
	global_load_lds_dwordx4 v[186:187], off
	v_lshl_add_u64 v[186:187], s[4:5], 0, v[166:167]
	s_add_i32 m0, s0, 0x2000
	s_nop 0
	global_load_lds_dwordx4 v[186:187], off
	v_lshl_add_u64 v[186:187], s[46:47], 0, v[172:173]
	s_mov_b32 m0, s41
	s_nop 0
	global_load_lds_dwordx4 v[186:187], off
	s_mov_b32 m0, s71
	s_nop 0
	global_load_lds_dwordx4 v[188:189], off
	s_waitcnt vmcnt(8)
	s_waitcnt lgkmcnt(0)
	s_barrier
	s_setprio 3
	s_waitcnt lgkmcnt(0)
	v_mfma_scale_f32_16x16x128_f8f6f4 v[94:97], v[18:25], v[200:207], 0, v197, v197 op_sel_hi:[0, 0, 0]
	v_mfma_scale_f32_16x16x128_f8f6f4 v[90:93], v[26:33], v[200:207], 0, v197, v197 op_sel_hi:[0, 0, 0]
	v_mfma_scale_f32_16x16x128_f8f6f4 v[86:89], v[18:25], v[208:215], 0, v197, v197 op_sel_hi:[0, 0, 0]
	v_mfma_scale_f32_16x16x128_f8f6f4 v[82:85], v[26:33], v[208:215], 0, v197, v197 op_sel_hi:[0, 0, 0]
	v_mfma_scale_f32_16x16x128_f8f6f4 v[70:73], v[18:25], v[216:223], 0, v197, v197 op_sel_hi:[0, 0, 0]
	v_mfma_scale_f32_16x16x128_f8f6f4 v[66:69], v[26:33], v[216:223], 0, v197, v197 op_sel_hi:[0, 0, 0]
	v_mfma_scale_f32_16x16x128_f8f6f4 v[54:57], v[18:25], v[224:231], 0, v197, v197 op_sel_hi:[0, 0, 0]
	v_mfma_scale_f32_16x16x128_f8f6f4 v[50:53], v[26:33], v[224:231], 0, v197, v197 op_sel_hi:[0, 0, 0]
	s_setprio 0
	s_setprio 3
	v_mfma_scale_f32_16x16x128_f8f6f4 v[78:81], v[2:9], v[200:207], 0, v197, v197 op_sel_hi:[0, 0, 0]
	v_mfma_scale_f32_16x16x128_f8f6f4 v[74:77], v[10:17], v[200:207], 0, v197, v197 op_sel_hi:[0, 0, 0]
	v_mfma_scale_f32_16x16x128_f8f6f4 v[62:65], v[2:9], v[208:215], 0, v197, v197 op_sel_hi:[0, 0, 0]
	v_mfma_scale_f32_16x16x128_f8f6f4 v[58:61], v[10:17], v[208:215], 0, v197, v197 op_sel_hi:[0, 0, 0]
	v_mfma_scale_f32_16x16x128_f8f6f4 v[46:49], v[2:9], v[216:223], 0, v197, v197 op_sel_hi:[0, 0, 0]
	v_mfma_scale_f32_16x16x128_f8f6f4 v[42:45], v[10:17], v[216:223], 0, v197, v197 op_sel_hi:[0, 0, 0]
	v_mfma_scale_f32_16x16x128_f8f6f4 v[38:41], v[2:9], v[224:231], 0, v197, v197 op_sel_hi:[0, 0, 0]
	v_mfma_scale_f32_16x16x128_f8f6f4 v[34:37], v[10:17], v[224:231], 0, v197, v197 op_sel_hi:[0, 0, 0]
	s_setprio 0
	s_barrier
; #define PG8_STAGE(bufoff, gbase, voff) do { _Pragma("unroll") for (int _i = 0; _i < 2; ++_i) \
;         __builtin_amdgcn_global_load_lds((const unsigned*)((const char*)(gbase) + (voff)[_i]), (PG8_LAS unsigned*)(lds + (bufoff) + ldsw + _i * 8192), 16, 0, 0); } while (0)
; #define PG8_LDA(dst, b, h) do { _Pragma("unroll") for (int m = 0; m < 4; ++m) Frag<F8>::load(dst[m], lds + PG8_SA(b, h) + aoff + m * 2048); } while (0)
; #define PG8_LDB(dst, b, h) do { _Pragma("unroll") for (int n = 0; n < 2; ++n) Frag<F8>::load(dst[n], lds + PG8_SB(b, h) + boff + n * 2048); } while (0)
; #define PG8_MMA(ai, bj, At, Bt) do { __builtin_amdgcn_s_setprio(3); _Pragma("unroll") for (int m = 0; m < 4; ++m) _Pragma("unroll") for (int n = 0; n < 2; ++n) Frag<F8>::mma(acc[ai][bj][m][n], Bt[n], At[m]); \
;         __builtin_amdgcn_s_setprio(0); } while (0)
; #define PG8_WAIT_V(n) asm volatile("s_waitcnt vmcnt(" #n ")" ::: "memory")
; #define PG8_WAIT_L(n) asm volatile("s_waitcnt lgkmcnt(" #n ")" ::: "memory")
; #define PG8_BAR __builtin_amdgcn_s_barrier()
; #define PG8_SCHED __builtin_amdgcn_sched_barrier(0)
; template <class Epi, class Sched, bool ALIGN_EPI = false, bool SP2 = false, bool F8 = false>
; __device__ __forceinline__ void gemm_phase(PG8_LAS unsigned char* lds, const Gemm g, const Sched& S, const Epi& E) {
;     ...
;             PG8_LDB(B0, 1, 0); PG8_LDB(B1, 1, 1); PG8_SCHED; PG8_LDA(At, 1, 0); PG8_STAGE(PG8_SA(0, 1), a2 + hstep, voffA);
;             PG8_WAIT_V(8); PG8_WAIT_L(0); PG8_BAR; PG8_MMA(0, 0, At, B0); PG8_MMA(0, 1, At, B1); PG8_BAR; PG8_SCHED;
;             PG8_LDA(At, 1, 1); PG8_STAGE(PG8_SB(1, 0), b3, voffB); PG8_STAGE(PG8_SB(1, 1), b3 + hstep, voffB); PG8_STAGE(PG8_SA(1, 0), a3, voffA);
;             PG8_WAIT_V(8); PG8_WAIT_L(0); PG8_BAR; PG8_MMA(1, 0, At, B0); PG8_MMA(1, 1, At, B1); PG8_BAR; PG8_SCHED;
	s_add_i32 s0, 0, 0x18000
	s_add_i32 s1, 0, 0x1c000
	v_add_u32_e32 v14, s0, v190
	v_add_u32_e32 v30, s1, v190
	ds_read_b128 v[2:5], v14
	ds_read_b128 v[6:9], v14 offset:1024
	ds_read_b128 v[10:13], v14 offset:2048
	ds_read_b128 v[14:17], v14 offset:3072
	ds_read_b128 v[18:21], v30
	ds_read_b128 v[22:25], v30 offset:1024
	ds_read_b128 v[26:29], v30 offset:2048
	ds_read_b128 v[30:33], v30 offset:3072
	s_add_u32 s4, s46, 0x20000
	s_addc_u32 s5, s47, 0
	s_mov_b32 m0, s72
	v_lshl_add_u64 v[232:233], s[4:5], 0, v[172:173]
	ds_read_b128 v[200:203], v196 offset:32768
	ds_read_b128 v[204:207], v196 offset:33792
	ds_read_b128 v[208:211], v196 offset:34816
	ds_read_b128 v[212:215], v196 offset:35840
	ds_read_b128 v[216:219], v196 offset:36864
	ds_read_b128 v[220:223], v196 offset:37888
	ds_read_b128 v[224:227], v196 offset:38912
	ds_read_b128 v[228:231], v196 offset:39936
	global_load_lds_dwordx4 v[232:233], off
	v_lshl_add_u64 v[232:233], s[4:5], 0, v[168:169]
	s_mov_b32 m0, s73
	s_nop 0
	global_load_lds_dwordx4 v[232:233], off
	s_waitcnt vmcnt(8)
	s_waitcnt lgkmcnt(0)
	s_barrier
	s_setprio 3
	s_waitcnt lgkmcnt(0)
	v_mfma_scale_f32_16x16x128_f8f6f4 v[158:161], v[2:9], v[200:207], v[158:161], v197, v197 op_sel_hi:[0,0,0]
	v_mfma_scale_f32_16x16x128_f8f6f4 v[154:157], v[10:17], v[200:207], v[154:157], v197, v197 op_sel_hi:[0,0,0]
	v_mfma_scale_f32_16x16x128_f8f6f4 v[150:153], v[2:9], v[208:215], v[150:153], v197, v197 op_sel_hi:[0,0,0]
	v_mfma_scale_f32_16x16x128_f8f6f4 v[142:145], v[10:17], v[208:215], v[142:145], v197, v197 op_sel_hi:[0,0,0]
	v_mfma_scale_f32_16x16x128_f8f6f4 v[130:133], v[2:9], v[216:223], v[130:133], v197, v197 op_sel_hi:[0,0,0]
	v_mfma_scale_f32_16x16x128_f8f6f4 v[122:125], v[10:17], v[216:223], v[122:125], v197, v197 op_sel_hi:[0,0,0]
	v_mfma_scale_f32_16x16x128_f8f6f4 v[118:121], v[2:9], v[224:231], v[118:121], v197, v197 op_sel_hi:[0,0,0]
	v_mfma_scale_f32_16x16x128_f8f6f4 v[110:113], v[10:17], v[224:231], v[110:113], v197, v197 op_sel_hi:[0,0,0]
	s_setprio 0
	s_setprio 3
	v_mfma_scale_f32_16x16x128_f8f6f4 v[146:149], v[18:25], v[200:207], v[146:149], v197, v197 op_sel_hi:[0,0,0]
	v_mfma_scale_f32_16x16x128_f8f6f4 v[138:141], v[26:33], v[200:207], v[138:141], v197, v197 op_sel_hi:[0,0,0]
	v_mfma_scale_f32_16x16x128_f8f6f4 v[134:137], v[18:25], v[208:215], v[134:137], v197, v197 op_sel_hi:[0,0,0]
	v_mfma_scale_f32_16x16x128_f8f6f4 v[126:129], v[26:33], v[208:215], v[126:129], v197, v197 op_sel_hi:[0,0,0]
	v_mfma_scale_f32_16x16x128_f8f6f4 v[114:117], v[18:25], v[216:223], v[114:117], v197, v197 op_sel_hi:[0,0,0]
	v_mfma_scale_f32_16x16x128_f8f6f4 v[106:109], v[26:33], v[216:223], v[106:109], v197, v197 op_sel_hi:[0,0,0]
	v_mfma_scale_f32_16x16x128_f8f6f4 v[102:105], v[18:25], v[224:231], v[102:105], v197, v197 op_sel_hi:[0,0,0]
	v_mfma_scale_f32_16x16x128_f8f6f4 v[98:101], v[26:33], v[224:231], v[98:101], v197, v197 op_sel_hi:[0,0,0]
	s_setprio 0
	s_barrier
	s_add_i32 s0, s0, s48
	v_lshl_add_u64 v[182:183], v[182:183], 0, s[18:19]
	s_mov_b32 m0, s0
	ds_read_b128 v[200:203], v196 offset:49152
	ds_read_b128 v[204:207], v196 offset:50176
	ds_read_b128 v[208:211], v196 offset:51200
	ds_read_b128 v[212:215], v196 offset:52224
	ds_read_b128 v[216:219], v196 offset:53248
	ds_read_b128 v[220:223], v196 offset:54272
	ds_read_b128 v[224:227], v196 offset:55296
	ds_read_b128 v[228:231], v196 offset:56320
	global_load_lds_dwordx4 v[182:183], off
	s_add_i32 m0, s0, 0x2000
	s_add_u32 s4, s44, 0x20080
	v_lshl_add_u64 v[182:183], v[184:185], 0, s[18:19]
	s_addc_u32 s5, s45, 0
	s_add_i32 s0, s1, s48
	global_load_lds_dwordx4 v[182:183], off
	v_lshl_add_u64 v[182:183], s[4:5], 0, v[170:171]
	s_mov_b32 m0, s0
	s_nop 0
	global_load_lds_dwordx4 v[182:183], off
	v_lshl_add_u64 v[182:183], s[4:5], 0, v[166:167]
	s_add_i32 m0, s0, 0x2000
	s_nop 0
	global_load_lds_dwordx4 v[182:183], off
	v_lshl_add_u64 v[182:183], v[186:187], 0, s[18:19]
	s_mov_b32 m0, s74
	s_nop 0
	global_load_lds_dwordx4 v[182:183], off
	v_lshl_add_u64 v[182:183], v[188:189], 0, s[18:19]
	s_mov_b32 m0, s75
	s_nop 0
	global_load_lds_dwordx4 v[182:183], off
	s_waitcnt vmcnt(8)
	s_waitcnt lgkmcnt(0)
	s_barrier
	s_setprio 3
	s_waitcnt lgkmcnt(0)
	v_mfma_scale_f32_16x16x128_f8f6f4 v[94:97], v[2:9], v[200:207], v[94:97], v197, v197 op_sel_hi:[0,0,0]
	v_mfma_scale_f32_16x16x128_f8f6f4 v[90:93], v[10:17], v[200:207], v[90:93], v197, v197 op_sel_hi:[0,0,0]
	v_mfma_scale_f32_16x16x128_f8f6f4 v[86:89], v[2:9], v[208:215], v[86:89], v197, v197 op_sel_hi:[0,0,0]
	v_mfma_scale_f32_16x16x128_f8f6f4 v[82:85], v[10:17], v[208:215], v[82:85], v197, v197 op_sel_hi:[0,0,0]
	v_mfma_scale_f32_16x16x128_f8f6f4 v[70:73], v[2:9], v[216:223], v[70:73], v197, v197 op_sel_hi:[0,0,0]
	v_mfma_scale_f32_16x16x128_f8f6f4 v[66:69], v[10:17], v[216:223], v[66:69], v197, v197 op_sel_hi:[0,0,0]
	v_mfma_scale_f32_16x16x128_f8f6f4 v[54:57], v[2:9], v[224:231], v[54:57], v197, v197 op_sel_hi:[0,0,0]
	v_mfma_scale_f32_16x16x128_f8f6f4 v[50:53], v[10:17], v[224:231], v[50:53], v197, v197 op_sel_hi:[0,0,0]
	s_setprio 0
	s_setprio 3
	v_mfma_scale_f32_16x16x128_f8f6f4 v[78:81], v[18:25], v[200:207], v[78:81], v197, v197 op_sel_hi:[0,0,0]
	v_mfma_scale_f32_16x16x128_f8f6f4 v[74:77], v[26:33], v[200:207], v[74:77], v197, v197 op_sel_hi:[0,0,0]
	v_mfma_scale_f32_16x16x128_f8f6f4 v[62:65], v[18:25], v[208:215], v[62:65], v197, v197 op_sel_hi:[0,0,0]
	v_mfma_scale_f32_16x16x128_f8f6f4 v[58:61], v[26:33], v[208:215], v[58:61], v197, v197 op_sel_hi:[0,0,0]
	v_mfma_scale_f32_16x16x128_f8f6f4 v[46:49], v[18:25], v[216:223], v[46:49], v197, v197 op_sel_hi:[0,0,0]
	v_mfma_scale_f32_16x16x128_f8f6f4 v[42:45], v[26:33], v[216:223], v[42:45], v197, v197 op_sel_hi:[0,0,0]
	v_mfma_scale_f32_16x16x128_f8f6f4 v[38:41], v[18:25], v[224:231], v[38:41], v197, v197 op_sel_hi:[0,0,0]
	v_mfma_scale_f32_16x16x128_f8f6f4 v[34:37], v[26:33], v[224:231], v[34:37], v197, v197 op_sel_hi:[0,0,0]
	s_setprio 0
	s_add_i32 s87, s87, 2
	s_add_u32 s42, s42, 0x100
	s_addc_u32 s43, s43, 0
	s_add_u32 s85, s85, 0x100
	s_addc_u32 s86, s86, 0
	s_cmp_gt_u32 s87, 5
	s_cbranch_scc1 .Lpeel_exit_2
; #define PG8_STAGE(bufoff, gbase, voff) do { _Pragma("unroll") for (int _i = 0; _i < 2; ++_i) \
;         __builtin_amdgcn_global_load_lds((const unsigned*)((const char*)(gbase) + (voff)[_i]), (PG8_LAS unsigned*)(lds + (bufoff) + ldsw + _i * 8192), 16, 0, 0); } while (0)
; #define PG8_LDA(dst, b, h) do { _Pragma("unroll") for (int m = 0; m < 4; ++m) Frag<F8>::load(dst[m], lds + PG8_SA(b, h) + aoff + m * 2048); } while (0)
; #define PG8_LDB(dst, b, h) do { _Pragma("unroll") for (int n = 0; n < 2; ++n) Frag<F8>::load(dst[n], lds + PG8_SB(b, h) + boff + n * 2048); } while (0)
; #define PG8_MMA(ai, bj, At, Bt) do { __builtin_amdgcn_s_setprio(3); _Pragma("unroll") for (int m = 0; m < 4; ++m) _Pragma("unroll") for (int n = 0; n < 2; ++n) Frag<F8>::mma(acc[ai][bj][m][n], Bt[n], At[m]); \
;         __builtin_amdgcn_s_setprio(0); } while (0)
; #define PG8_WAIT_V(n) asm volatile("s_waitcnt vmcnt(" #n ")" ::: "memory")
; #define PG8_WAIT_L(n) asm volatile("s_waitcnt lgkmcnt(" #n ")" ::: "memory")
; #define PG8_BAR __builtin_amdgcn_s_barrier()
; #define PG8_SCHED __builtin_amdgcn_sched_barrier(0)
; template <class Epi, class Sched, bool ALIGN_EPI = false, bool SP2 = false, bool F8 = false>
; __device__ __forceinline__ void gemm_phase(PG8_LAS unsigned char* lds, const Gemm g, const Sched& S, const Epi& E) {
;     ...
;             PG8_LDB(B0, 0, 0); PG8_LDB(B1, 0, 1); PG8_SCHED; PG8_LDA(At, 0, 0); PG8_STAGE(PG8_SA(1, 1), a1 + hstep, voffA);
;             PG8_WAIT_V(8); PG8_WAIT_L(0); PG8_BAR; PG8_MMA(0, 0, At, B0); PG8_MMA(0, 1, At, B1); PG8_BAR; PG8_SCHED;
;             PG8_LDA(At, 0, 1); PG8_STAGE(PG8_SB(0, 0), b2, voffB); PG8_STAGE(PG8_SB(0, 1), b2 + hstep, voffB); PG8_STAGE(PG8_SA(0, 0), a2, voffA);
;             PG8_WAIT_V(8); PG8_WAIT_L(0); PG8_BAR; PG8_MMA(1, 0, At, B0); PG8_MMA(1, 1, At, B1); PG8_BAR; PG8_SCHED;
.LBB0_802:
	s_barrier
	ds_read_b128 v[18:21], v194
	ds_read_b128 v[22:25], v194 offset:1024
	ds_read_b128 v[26:29], v194 offset:2048
	ds_read_b128 v[30:33], v194 offset:3072
	ds_read_b128 v[2:5], v195
	ds_read_b128 v[6:9], v195 offset:1024
	ds_read_b128 v[10:13], v195 offset:2048
	ds_read_b128 v[14:17], v195 offset:3072
	s_add_u32 s0, s42, 0xfffe0080
	s_addc_u32 s1, s43, -1
	s_cmp_eq_u32 s87, 4
	s_cselect_b32 s47, s25, s1
	s_cselect_b32 s46, s83, s0
	s_cselect_b32 s45, s31, s86
	s_cselect_b32 s44, s84, s85
	v_lshl_add_u64 v[224:225], s[42:43], 0, v[174:175]
	s_add_i32 m0, s41, 0xc000
	ds_read_b128 v[182:185], v196
	ds_read_b128 v[186:189], v196 offset:1024
	ds_read_b128 v[200:203], v196 offset:2048
	ds_read_b128 v[204:207], v196 offset:3072
	ds_read_b128 v[208:211], v196 offset:4096
	ds_read_b128 v[212:215], v196 offset:5120
	ds_read_b128 v[216:219], v196 offset:6144
	ds_read_b128 v[220:223], v196 offset:7168
	global_load_lds_dwordx4 v[224:225], off
	v_lshl_add_u64 v[224:225], s[42:43], 0, v[176:177]
	s_add_i32 m0, s41, 0xe000
	s_nop 0
	global_load_lds_dwordx4 v[224:225], off
	s_waitcnt vmcnt(8)
	s_waitcnt lgkmcnt(0)
	s_barrier
	s_setprio 3
	s_waitcnt lgkmcnt(0)
	v_mfma_scale_f32_16x16x128_f8f6f4 v[158:161], v[18:25], v[182:189], v[158:161], v197, v197 op_sel_hi:[0,0,0]
	v_mfma_scale_f32_16x16x128_f8f6f4 v[154:157], v[26:33], v[182:189], v[154:157], v197, v197 op_sel_hi:[0,0,0]
	v_mfma_scale_f32_16x16x128_f8f6f4 v[150:153], v[18:25], v[200:207], v[150:153], v197, v197 op_sel_hi:[0,0,0]
	v_mfma_scale_f32_16x16x128_f8f6f4 v[142:145], v[26:33], v[200:207], v[142:145], v197, v197 op_sel_hi:[0,0,0]
	v_mfma_scale_f32_16x16x128_f8f6f4 v[130:133], v[18:25], v[208:215], v[130:133], v197, v197 op_sel_hi:[0,0,0]
	v_mfma_scale_f32_16x16x128_f8f6f4 v[122:125], v[26:33], v[208:215], v[122:125], v197, v197 op_sel_hi:[0,0,0]
	v_mfma_scale_f32_16x16x128_f8f6f4 v[118:121], v[18:25], v[216:223], v[118:121], v197, v197 op_sel_hi:[0,0,0]
	v_mfma_scale_f32_16x16x128_f8f6f4 v[110:113], v[26:33], v[216:223], v[110:113], v197, v197 op_sel_hi:[0,0,0]
	s_setprio 0
	s_setprio 3
	v_mfma_scale_f32_16x16x128_f8f6f4 v[146:149], v[2:9], v[182:189], v[146:149], v197, v197 op_sel_hi:[0,0,0]
	v_mfma_scale_f32_16x16x128_f8f6f4 v[138:141], v[10:17], v[182:189], v[138:141], v197, v197 op_sel_hi:[0,0,0]
	v_mfma_scale_f32_16x16x128_f8f6f4 v[134:137], v[2:9], v[200:207], v[134:137], v197, v197 op_sel_hi:[0,0,0]
	v_mfma_scale_f32_16x16x128_f8f6f4 v[126:129], v[10:17], v[200:207], v[126:129], v197, v197 op_sel_hi:[0,0,0]
	v_mfma_scale_f32_16x16x128_f8f6f4 v[114:117], v[2:9], v[208:215], v[114:117], v197, v197 op_sel_hi:[0,0,0]
	v_mfma_scale_f32_16x16x128_f8f6f4 v[106:109], v[10:17], v[208:215], v[106:109], v197, v197 op_sel_hi:[0,0,0]
	v_mfma_scale_f32_16x16x128_f8f6f4 v[102:105], v[2:9], v[216:223], v[102:105], v197, v197 op_sel_hi:[0,0,0]
	v_mfma_scale_f32_16x16x128_f8f6f4 v[98:101], v[10:17], v[216:223], v[98:101], v197, v197 op_sel_hi:[0,0,0]
	s_setprio 0
	s_barrier
	s_add_i32 s0, s79, s48
	v_lshl_add_u64 v[182:183], s[44:45], 0, v[170:171]
	s_mov_b32 m0, s0
	ds_read_b128 v[200:203], v196 offset:16384
	ds_read_b128 v[204:207], v196 offset:17408
	ds_read_b128 v[208:211], v196 offset:18432
	ds_read_b128 v[212:215], v196 offset:19456
	ds_read_b128 v[216:219], v196 offset:20480
	ds_read_b128 v[220:223], v196 offset:21504
	ds_read_b128 v[224:227], v196 offset:22528
	ds_read_b128 v[228:231], v196 offset:23552
	global_load_lds_dwordx4 v[182:183], off
	s_add_i32 m0, s0, 0x2000
	s_add_u32 s4, s44, 0x20000
	v_lshl_add_u64 v[184:185], s[44:45], 0, v[166:167]
	s_addc_u32 s5, s45, 0
	s_add_i32 s0, s80, s48
	global_load_lds_dwordx4 v[184:185], off
	v_lshl_add_u64 v[186:187], s[4:5], 0, v[170:171]
	s_mov_b32 m0, s0
	v_lshl_add_u64 v[188:189], s[46:47], 0, v[168:169]
	global_load_lds_dwordx4 v[186:187], off
	v_lshl_add_u64 v[186:187], s[4:5], 0, v[166:167]
	s_add_i32 m0, s0, 0x2000
	s_nop 0
	global_load_lds_dwordx4 v[186:187], off
	v_lshl_add_u64 v[186:187], s[46:47], 0, v[172:173]
	s_mov_b32 m0, s41
	s_nop 0
	global_load_lds_dwordx4 v[186:187], off
	s_mov_b32 m0, s71
	s_nop 0
	global_load_lds_dwordx4 v[188:189], off
	s_waitcnt vmcnt(8)
	s_waitcnt lgkmcnt(0)
	s_barrier
	s_setprio 3
	s_waitcnt lgkmcnt(0)
	v_mfma_scale_f32_16x16x128_f8f6f4 v[94:97], v[18:25], v[200:207], v[94:97], v197, v197 op_sel_hi:[0,0,0]
	v_mfma_scale_f32_16x16x128_f8f6f4 v[90:93], v[26:33], v[200:207], v[90:93], v197, v197 op_sel_hi:[0,0,0]
	v_mfma_scale_f32_16x16x128_f8f6f4 v[86:89], v[18:25], v[208:215], v[86:89], v197, v197 op_sel_hi:[0,0,0]
	v_mfma_scale_f32_16x16x128_f8f6f4 v[82:85], v[26:33], v[208:215], v[82:85], v197, v197 op_sel_hi:[0,0,0]
	v_mfma_scale_f32_16x16x128_f8f6f4 v[70:73], v[18:25], v[216:223], v[70:73], v197, v197 op_sel_hi:[0,0,0]
	v_mfma_scale_f32_16x16x128_f8f6f4 v[66:69], v[26:33], v[216:223], v[66:69], v197, v197 op_sel_hi:[0,0,0]
	v_mfma_scale_f32_16x16x128_f8f6f4 v[54:57], v[18:25], v[224:231], v[54:57], v197, v197 op_sel_hi:[0,0,0]
	v_mfma_scale_f32_16x16x128_f8f6f4 v[50:53], v[26:33], v[224:231], v[50:53], v197, v197 op_sel_hi:[0,0,0]
	s_setprio 0
	s_setprio 3
	v_mfma_scale_f32_16x16x128_f8f6f4 v[78:81], v[2:9], v[200:207], v[78:81], v197, v197 op_sel_hi:[0,0,0]
	v_mfma_scale_f32_16x16x128_f8f6f4 v[74:77], v[10:17], v[200:207], v[74:77], v197, v197 op_sel_hi:[0,0,0]
	v_mfma_scale_f32_16x16x128_f8f6f4 v[62:65], v[2:9], v[208:215], v[62:65], v197, v197 op_sel_hi:[0,0,0]
	v_mfma_scale_f32_16x16x128_f8f6f4 v[58:61], v[10:17], v[208:215], v[58:61], v197, v197 op_sel_hi:[0,0,0]
	v_mfma_scale_f32_16x16x128_f8f6f4 v[46:49], v[2:9], v[216:223], v[46:49], v197, v197 op_sel_hi:[0,0,0]
	v_mfma_scale_f32_16x16x128_f8f6f4 v[42:45], v[10:17], v[216:223], v[42:45], v197, v197 op_sel_hi:[0,0,0]
	v_mfma_scale_f32_16x16x128_f8f6f4 v[38:41], v[2:9], v[224:231], v[38:41], v197, v197 op_sel_hi:[0,0,0]
	v_mfma_scale_f32_16x16x128_f8f6f4 v[34:37], v[10:17], v[224:231], v[34:37], v197, v197 op_sel_hi:[0,0,0]
	s_setprio 0
	s_barrier
; #define PG8_STAGE(bufoff, gbase, voff) do { _Pragma("unroll") for (int _i = 0; _i < 2; ++_i) \
;         __builtin_amdgcn_global_load_lds((const unsigned*)((const char*)(gbase) + (voff)[_i]), (PG8_LAS unsigned*)(lds + (bufoff) + ldsw + _i * 8192), 16, 0, 0); } while (0)
; #define PG8_LDA(dst, b, h) do { _Pragma("unroll") for (int m = 0; m < 4; ++m) Frag<F8>::load(dst[m], lds + PG8_SA(b, h) + aoff + m * 2048); } while (0)
; #define PG8_LDB(dst, b, h) do { _Pragma("unroll") for (int n = 0; n < 2; ++n) Frag<F8>::load(dst[n], lds + PG8_SB(b, h) + boff + n * 2048); } while (0)
; #define PG8_MMA(ai, bj, At, Bt) do { __builtin_amdgcn_s_setprio(3); _Pragma("unroll") for (int m = 0; m < 4; ++m) _Pragma("unroll") for (int n = 0; n < 2; ++n) Frag<F8>::mma(acc[ai][bj][m][n], Bt[n], At[m]); \
;         __builtin_amdgcn_s_setprio(0); } while (0)
; #define PG8_WAIT_V(n) asm volatile("s_waitcnt vmcnt(" #n ")" ::: "memory")
; #define PG8_WAIT_L(n) asm volatile("s_waitcnt lgkmcnt(" #n ")" ::: "memory")
; #define PG8_BAR __builtin_amdgcn_s_barrier()
; #define PG8_SCHED __builtin_amdgcn_sched_barrier(0)
; template <class Epi, class Sched, bool ALIGN_EPI = false, bool SP2 = false, bool F8 = false>
; __device__ __forceinline__ void gemm_phase(PG8_LAS unsigned char* lds, const Gemm g, const Sched& S, const Epi& E) {
;     ...
;         for (int t = 0; t < nt; t += 2) {
;     ...
;             PG8_LDB(B0, 1, 0); PG8_LDB(B1, 1, 1); PG8_SCHED; PG8_LDA(At, 1, 0); PG8_STAGE(PG8_SA(0, 1), a2 + hstep, voffA);
;             PG8_WAIT_V(8); PG8_WAIT_L(0); PG8_BAR; PG8_MMA(0, 0, At, B0); PG8_MMA(0, 1, At, B1); PG8_BAR; PG8_SCHED;
;             PG8_LDA(At, 1, 1); PG8_STAGE(PG8_SB(1, 0), b3, voffB); PG8_STAGE(PG8_SB(1, 1), b3 + hstep, voffB); PG8_STAGE(PG8_SA(1, 0), a3, voffA);
;             PG8_WAIT_V(8); PG8_WAIT_L(0); PG8_BAR; PG8_MMA(1, 0, At, B0); PG8_MMA(1, 1, At, B1); PG8_BAR; PG8_SCHED;
	s_add_i32 s0, 0, 0x18000
	s_add_i32 s1, 0, 0x1c000
	v_add_u32_e32 v14, s0, v190
	v_add_u32_e32 v30, s1, v190
	ds_read_b128 v[2:5], v14
	ds_read_b128 v[6:9], v14 offset:1024
	ds_read_b128 v[10:13], v14 offset:2048
	ds_read_b128 v[14:17], v14 offset:3072
	ds_read_b128 v[18:21], v30
	ds_read_b128 v[22:25], v30 offset:1024
	ds_read_b128 v[26:29], v30 offset:2048
	ds_read_b128 v[30:33], v30 offset:3072
	s_add_u32 s4, s46, 0x20000
	s_addc_u32 s5, s47, 0
	s_mov_b32 m0, s72
	v_lshl_add_u64 v[232:233], s[4:5], 0, v[172:173]
	ds_read_b128 v[200:203], v196 offset:32768
	ds_read_b128 v[204:207], v196 offset:33792
	ds_read_b128 v[208:211], v196 offset:34816
	ds_read_b128 v[212:215], v196 offset:35840
	ds_read_b128 v[216:219], v196 offset:36864
	ds_read_b128 v[220:223], v196 offset:37888
	ds_read_b128 v[224:227], v196 offset:38912
	ds_read_b128 v[228:231], v196 offset:39936
	global_load_lds_dwordx4 v[232:233], off
	v_lshl_add_u64 v[232:233], s[4:5], 0, v[168:169]
	s_mov_b32 m0, s73
	s_nop 0
	global_load_lds_dwordx4 v[232:233], off
	s_waitcnt vmcnt(8)
	s_waitcnt lgkmcnt(0)
	s_barrier
	s_setprio 3
	s_waitcnt lgkmcnt(0)
	v_mfma_scale_f32_16x16x128_f8f6f4 v[158:161], v[2:9], v[200:207], v[158:161], v197, v197 op_sel_hi:[0,0,0]
	v_mfma_scale_f32_16x16x128_f8f6f4 v[154:157], v[10:17], v[200:207], v[154:157], v197, v197 op_sel_hi:[0,0,0]
	v_mfma_scale_f32_16x16x128_f8f6f4 v[150:153], v[2:9], v[208:215], v[150:153], v197, v197 op_sel_hi:[0,0,0]
	v_mfma_scale_f32_16x16x128_f8f6f4 v[142:145], v[10:17], v[208:215], v[142:145], v197, v197 op_sel_hi:[0,0,0]
	v_mfma_scale_f32_16x16x128_f8f6f4 v[130:133], v[2:9], v[216:223], v[130:133], v197, v197 op_sel_hi:[0,0,0]
	v_mfma_scale_f32_16x16x128_f8f6f4 v[122:125], v[10:17], v[216:223], v[122:125], v197, v197 op_sel_hi:[0,0,0]
	v_mfma_scale_f32_16x16x128_f8f6f4 v[118:121], v[2:9], v[224:231], v[118:121], v197, v197 op_sel_hi:[0,0,0]
	v_mfma_scale_f32_16x16x128_f8f6f4 v[110:113], v[10:17], v[224:231], v[110:113], v197, v197 op_sel_hi:[0,0,0]
	s_setprio 0
	s_setprio 3
	v_mfma_scale_f32_16x16x128_f8f6f4 v[146:149], v[18:25], v[200:207], v[146:149], v197, v197 op_sel_hi:[0,0,0]
	v_mfma_scale_f32_16x16x128_f8f6f4 v[138:141], v[26:33], v[200:207], v[138:141], v197, v197 op_sel_hi:[0,0,0]
	v_mfma_scale_f32_16x16x128_f8f6f4 v[134:137], v[18:25], v[208:215], v[134:137], v197, v197 op_sel_hi:[0,0,0]
	v_mfma_scale_f32_16x16x128_f8f6f4 v[126:129], v[26:33], v[208:215], v[126:129], v197, v197 op_sel_hi:[0,0,0]
	v_mfma_scale_f32_16x16x128_f8f6f4 v[114:117], v[18:25], v[216:223], v[114:117], v197, v197 op_sel_hi:[0,0,0]
	v_mfma_scale_f32_16x16x128_f8f6f4 v[106:109], v[26:33], v[216:223], v[106:109], v197, v197 op_sel_hi:[0,0,0]
	v_mfma_scale_f32_16x16x128_f8f6f4 v[102:105], v[18:25], v[224:231], v[102:105], v197, v197 op_sel_hi:[0,0,0]
	v_mfma_scale_f32_16x16x128_f8f6f4 v[98:101], v[26:33], v[224:231], v[98:101], v197, v197 op_sel_hi:[0,0,0]
	s_setprio 0
	s_barrier
	s_add_i32 s0, s0, s48
	v_lshl_add_u64 v[182:183], v[182:183], 0, s[18:19]
	s_mov_b32 m0, s0
	ds_read_b128 v[200:203], v196 offset:49152
	ds_read_b128 v[204:207], v196 offset:50176
	ds_read_b128 v[208:211], v196 offset:51200
	ds_read_b128 v[212:215], v196 offset:52224
	ds_read_b128 v[216:219], v196 offset:53248
	ds_read_b128 v[220:223], v196 offset:54272
	ds_read_b128 v[224:227], v196 offset:55296
	ds_read_b128 v[228:231], v196 offset:56320
	global_load_lds_dwordx4 v[182:183], off
	s_add_i32 m0, s0, 0x2000
	s_add_u32 s4, s44, 0x20080
	v_lshl_add_u64 v[182:183], v[184:185], 0, s[18:19]
	s_addc_u32 s5, s45, 0
	s_add_i32 s0, s1, s48
	global_load_lds_dwordx4 v[182:183], off
	v_lshl_add_u64 v[182:183], s[4:5], 0, v[170:171]
	s_mov_b32 m0, s0
	s_nop 0
	global_load_lds_dwordx4 v[182:183], off
	v_lshl_add_u64 v[182:183], s[4:5], 0, v[166:167]
	s_add_i32 m0, s0, 0x2000
	s_nop 0
	global_load_lds_dwordx4 v[182:183], off
	v_lshl_add_u64 v[182:183], v[186:187], 0, s[18:19]
	s_mov_b32 m0, s74
	s_nop 0
	global_load_lds_dwordx4 v[182:183], off
	v_lshl_add_u64 v[182:183], v[188:189], 0, s[18:19]
	s_mov_b32 m0, s75
	s_nop 0
	global_load_lds_dwordx4 v[182:183], off
	s_waitcnt vmcnt(8)
	s_waitcnt lgkmcnt(0)
	s_barrier
	s_setprio 3
	s_waitcnt lgkmcnt(0)
	v_mfma_scale_f32_16x16x128_f8f6f4 v[94:97], v[2:9], v[200:207], v[94:97], v197, v197 op_sel_hi:[0,0,0]
	v_mfma_scale_f32_16x16x128_f8f6f4 v[90:93], v[10:17], v[200:207], v[90:93], v197, v197 op_sel_hi:[0,0,0]
	v_mfma_scale_f32_16x16x128_f8f6f4 v[86:89], v[2:9], v[208:215], v[86:89], v197, v197 op_sel_hi:[0,0,0]
	v_mfma_scale_f32_16x16x128_f8f6f4 v[82:85], v[10:17], v[208:215], v[82:85], v197, v197 op_sel_hi:[0,0,0]
	v_mfma_scale_f32_16x16x128_f8f6f4 v[70:73], v[2:9], v[216:223], v[70:73], v197, v197 op_sel_hi:[0,0,0]
	v_mfma_scale_f32_16x16x128_f8f6f4 v[66:69], v[10:17], v[216:223], v[66:69], v197, v197 op_sel_hi:[0,0,0]
	v_mfma_scale_f32_16x16x128_f8f6f4 v[54:57], v[2:9], v[224:231], v[54:57], v197, v197 op_sel_hi:[0,0,0]
	v_mfma_scale_f32_16x16x128_f8f6f4 v[50:53], v[10:17], v[224:231], v[50:53], v197, v197 op_sel_hi:[0,0,0]
	s_setprio 0
	s_setprio 3
	v_mfma_scale_f32_16x16x128_f8f6f4 v[78:81], v[18:25], v[200:207], v[78:81], v197, v197 op_sel_hi:[0,0,0]
	v_mfma_scale_f32_16x16x128_f8f6f4 v[74:77], v[26:33], v[200:207], v[74:77], v197, v197 op_sel_hi:[0,0,0]
	v_mfma_scale_f32_16x16x128_f8f6f4 v[62:65], v[18:25], v[208:215], v[62:65], v197, v197 op_sel_hi:[0,0,0]
	v_mfma_scale_f32_16x16x128_f8f6f4 v[58:61], v[26:33], v[208:215], v[58:61], v197, v197 op_sel_hi:[0,0,0]
	v_mfma_scale_f32_16x16x128_f8f6f4 v[46:49], v[18:25], v[216:223], v[46:49], v197, v197 op_sel_hi:[0,0,0]
	v_mfma_scale_f32_16x16x128_f8f6f4 v[42:45], v[26:33], v[216:223], v[42:45], v197, v197 op_sel_hi:[0,0,0]
	v_mfma_scale_f32_16x16x128_f8f6f4 v[38:41], v[18:25], v[224:231], v[38:41], v197, v197 op_sel_hi:[0,0,0]
	v_mfma_scale_f32_16x16x128_f8f6f4 v[34:37], v[26:33], v[224:231], v[34:37], v197, v197 op_sel_hi:[0,0,0]
	s_setprio 0
	s_add_i32 s87, s87, 2
	s_add_u32 s42, s42, 0x100
	s_addc_u32 s43, s43, 0
	s_add_u32 s85, s85, 0x100
	s_addc_u32 s86, s86, 0
	s_cmp_gt_u32 s87, 5
	s_cbranch_scc0 .LBB0_802

; __device__ __forceinline__ unsigned cvt_pk_bf16(float lo, float hi) { const f32x2 v = {lo, hi}; const bf16x2_t b = __builtin_convertvector(v, bf16x2_t); return __builtin_bit_cast(unsigned, b); }
; __device__ __forceinline__ unsigned long long rt() { return __builtin_amdgcn_s_memrealtime(); }
;     __device__ __forceinline__ void operator()(const f32x4 (&acc)[2][2][4][2], const Unit& u, int wr, int wc, int fr, int fq) const {
;         const int row0 = u.pm * BM + wr * 64 + fr, col0 = u.pn * BM + wc * 32 + 8 * fq;
;         const float sc0 = ((smask >> (2 * u.pn)) & 1u) ? sval : 1.0f, sc1 = ((smask >> (2 * u.pn + 1)) & 1u) ? sval : 1.0f;
; #pragma unroll
;         for (int ai = 0; ai < 2; ++ai)
; #pragma unroll
;             for (int m = 0; m < 4; ++m) { bf16_t* rowp = O + (size_t)(row0 + ai * HALF + m * 16) * ldc + col0;
;                 const float rs = rt ? rt[ai * HALF + wr * 64 + m * 16 + fr] : 1.0f;
; #pragma unroll
;                 for (int bj = 0; bj < 2; ++bj) { const float sc = (bj ? sc1 : sc0) * rs; const f32x4 v0 = acc[ai][bj][m][0] * sc, v1 = acc[ai][bj][m][1] * sc;
;                     u32x4 w; w.x = cvt_pk_bf16(v0[0], v0[1]); w.y = cvt_pk_bf16(v0[2], v0[3]); w.z = cvt_pk_bf16(v1[0], v1[1]); w.w = cvt_pk_bf16(v1[2], v1[3]);
;                     *(u32x4*)(rowp + bj * HALF) = w; } }
.LBB0_805:
	s_nop 15
	s_nop 15
	s_lshl_b32 s0, s82, 1
	s_lshl_b32 s1, 1, s0
	s_and_b32 s1, s1, 0x41041
	s_cmp_eq_u32 s1, 0
	s_cselect_b64 s[4:5], -1, 0
	s_lshl_b32 s0, 2, s0
	ds_read2_b32 v[10:11], v191 offset1:16
	s_and_b32 s0, s0, 0x82082
	v_lshl_or_b32 v4, s82, 8, v193
	s_cmp_eq_u32 s0, 0
	v_lshl_add_u32 v20, s40, 8, v165
	v_cndmask_b32_e64 v21, v198, 1.0, s[4:5]
	s_cselect_b64 s[4:5], -1, 0
	v_ashrrev_i32_e32 v5, 31, v4
	v_mov_b64_e32 v[2:3], s[16:17]
	v_cndmask_b32_e64 v22, v198, 1.0, s[4:5]
	v_mad_i64_i32 v[6:7], s[4:5], v20, s81, v[2:3]
	v_lshlrev_b64 v[4:5], 1, v[4:5]
	v_lshl_add_u64 v[12:13], v[6:7], 0, v[4:5]
	s_waitcnt lgkmcnt(0)
	v_mul_f32_e32 v6, v21, v10
	v_pk_mul_f32 v[8:9], v[160:161], v[6:7] op_sel_hi:[1,0]
	v_pk_mul_f32 v[14:15], v[158:159], v[6:7] op_sel_hi:[1,0]
	v_pk_mul_f32 v[16:17], v[156:157], v[6:7] op_sel_hi:[1,0]
	v_pk_mul_f32 v[18:19], v[154:155], v[6:7] op_sel_hi:[1,0]
	v_cvt_pk_bf16_f32 v6, v14, v15
	v_cvt_pk_bf16_f32 v7, v8, v9
	v_cvt_pk_bf16_f32 v8, v18, v19
	v_cvt_pk_bf16_f32 v9, v16, v17
	global_store_dwordx4 v[12:13], v[6:9], off
	s_andn2_b64 vcc, exec, s[8:9]
	s_mov_b64 s[8:9], -1
	v_mul_f32_e32 v6, v22, v10
	v_pk_mul_f32 v[8:9], v[148:149], v[6:7] op_sel_hi:[1,0]
	v_pk_mul_f32 v[14:15], v[146:147], v[6:7] op_sel_hi:[1,0]
	v_pk_mul_f32 v[16:17], v[140:141], v[6:7] op_sel_hi:[1,0]
	v_pk_mul_f32 v[18:19], v[138:139], v[6:7] op_sel_hi:[1,0]
	v_cvt_pk_bf16_f32 v6, v14, v15
	v_cvt_pk_bf16_f32 v7, v8, v9
	v_cvt_pk_bf16_f32 v8, v18, v19
	v_cvt_pk_bf16_f32 v9, v16, v17
	global_store_dwordx4 v[12:13], v[6:9], off offset:256
	ds_read_b32 v23, v191 offset:704
	s_nop 0
	v_or_b32_e32 v6, 16, v20
	v_mad_i64_i32 v[6:7], s[4:5], v6, s81, v[2:3]
	v_lshl_add_u64 v[12:13], v[6:7], 0, v[4:5]
	v_mul_f32_e32 v6, v21, v11
	v_pk_mul_f32 v[8:9], v[152:153], v[6:7] op_sel_hi:[1,0]
	v_pk_mul_f32 v[14:15], v[150:151], v[6:7] op_sel_hi:[1,0]
	v_pk_mul_f32 v[16:17], v[144:145], v[6:7] op_sel_hi:[1,0]
	v_pk_mul_f32 v[18:19], v[142:143], v[6:7] op_sel_hi:[1,0]
	v_cvt_pk_bf16_f32 v6, v14, v15
	v_cvt_pk_bf16_f32 v7, v8, v9
	v_cvt_pk_bf16_f32 v8, v18, v19
	v_cvt_pk_bf16_f32 v9, v16, v17
	global_store_dwordx4 v[12:13], v[6:9], off
	s_nop 1
	v_mul_f32_e32 v6, v22, v11
	v_pk_mul_f32 v[10:11], v[134:135], v[6:7] op_sel_hi:[1,0]
	v_pk_mul_f32 v[8:9], v[136:137], v[6:7] op_sel_hi:[1,0]
	v_pk_mul_f32 v[14:15], v[128:129], v[6:7] op_sel_hi:[1,0]
	v_pk_mul_f32 v[16:17], v[126:127], v[6:7] op_sel_hi:[1,0]
	v_cvt_pk_bf16_f32 v6, v10, v11
	ds_read2_b32 v[10:11], v191 offset0:32 offset1:48
	v_cvt_pk_bf16_f32 v7, v8, v9
	v_cvt_pk_bf16_f32 v8, v16, v17
	v_cvt_pk_bf16_f32 v9, v14, v15
	global_store_dwordx4 v[12:13], v[6:9], off offset:256
	s_nop 1
	v_or_b32_e32 v6, 32, v20
	v_mad_i64_i32 v[6:7], s[4:5], v6, s81, v[2:3]
	v_lshl_add_u64 v[12:13], v[6:7], 0, v[4:5]
	s_waitcnt lgkmcnt(0)
	v_mul_f32_e32 v6, v21, v10
	v_pk_mul_f32 v[8:9], v[132:133], v[6:7] op_sel_hi:[1,0]
	v_pk_mul_f32 v[14:15], v[130:131], v[6:7] op_sel_hi:[1,0]
	v_pk_mul_f32 v[16:17], v[124:125], v[6:7] op_sel_hi:[1,0]
	v_pk_mul_f32 v[18:19], v[122:123], v[6:7] op_sel_hi:[1,0]
	v_cvt_pk_bf16_f32 v6, v14, v15
	v_cvt_pk_bf16_f32 v7, v8, v9
	v_cvt_pk_bf16_f32 v8, v18, v19
	v_cvt_pk_bf16_f32 v9, v16, v17
	global_store_dwordx4 v[12:13], v[6:9], off
	s_nop 1
	v_mul_f32_e32 v6, v22, v10
	v_pk_mul_f32 v[8:9], v[116:117], v[6:7] op_sel_hi:[1,0]
	v_pk_mul_f32 v[14:15], v[114:115], v[6:7] op_sel_hi:[1,0]
	v_pk_mul_f32 v[16:17], v[108:109], v[6:7] op_sel_hi:[1,0]
	v_pk_mul_f32 v[18:19], v[106:107], v[6:7] op_sel_hi:[1,0]
	v_cvt_pk_bf16_f32 v6, v14, v15
	v_cvt_pk_bf16_f32 v7, v8, v9
	v_cvt_pk_bf16_f32 v8, v18, v19
	v_cvt_pk_bf16_f32 v9, v16, v17
	global_store_dwordx4 v[12:13], v[6:9], off offset:256
	s_nop 1
	v_or_b32_e32 v6, 48, v20
	v_mad_i64_i32 v[6:7], s[4:5], v6, s81, v[2:3]
	v_lshl_add_u64 v[12:13], v[6:7], 0, v[4:5]
	v_mul_f32_e32 v6, v21, v11
	v_pk_mul_f32 v[8:9], v[120:121], v[6:7] op_sel_hi:[1,0]
	v_pk_mul_f32 v[14:15], v[118:119], v[6:7] op_sel_hi:[1,0]
	v_pk_mul_f32 v[16:17], v[112:113], v[6:7] op_sel_hi:[1,0]
	v_pk_mul_f32 v[18:19], v[110:111], v[6:7] op_sel_hi:[1,0]
	v_cvt_pk_bf16_f32 v6, v14, v15
	v_cvt_pk_bf16_f32 v7, v8, v9
	v_cvt_pk_bf16_f32 v8, v18, v19
	v_cvt_pk_bf16_f32 v9, v16, v17
	global_store_dwordx4 v[12:13], v[6:9], off
	ds_read_b32 v18, v192
	s_nop 0
	v_mul_f32_e32 v6, v22, v11
	v_pk_mul_f32 v[8:9], v[104:105], v[6:7] op_sel_hi:[1,0]
	v_pk_mul_f32 v[10:11], v[102:103], v[6:7] op_sel_hi:[1,0]
	v_pk_mul_f32 v[14:15], v[100:101], v[6:7] op_sel_hi:[1,0]
	v_pk_mul_f32 v[16:17], v[98:99], v[6:7] op_sel_hi:[1,0]
	v_cvt_pk_bf16_f32 v6, v10, v11
	v_cvt_pk_bf16_f32 v7, v8, v9
	v_cvt_pk_bf16_f32 v8, v16, v17
	v_cvt_pk_bf16_f32 v9, v14, v15
	global_store_dwordx4 v[12:13], v[6:9], off offset:256
	s_nop 1
	v_add_u32_e32 v6, 0x80, v20
	v_mad_i64_i32 v[6:7], s[4:5], v6, s81, v[2:3]
	v_lshl_add_u64 v[10:11], v[6:7], 0, v[4:5]
	s_waitcnt lgkmcnt(0)
; __device__ __forceinline__ unsigned cvt_pk_bf16(float lo, float hi) { const f32x2 v = {lo, hi}; const bf16x2_t b = __builtin_convertvector(v, bf16x2_t); return __builtin_bit_cast(unsigned, b); }
; #define PG8_BAR __builtin_amdgcn_s_barrier()
; __device__ __forceinline__ unsigned long long rt() { return __builtin_amdgcn_s_memrealtime(); }
;     __device__ __forceinline__ void operator()(const f32x4 (&acc)[2][2][4][2], const Unit& u, int wr, int wc, int fr, int fq) const {
;     ...
;         for (int ai = 0; ai < 2; ++ai)
; #pragma unroll
;             for (int m = 0; m < 4; ++m) { bf16_t* rowp = O + (size_t)(row0 + ai * HALF + m * 16) * ldc + col0;
;                 const float rs = rt ? rt[ai * HALF + wr * 64 + m * 16 + fr] : 1.0f;
; #pragma unroll
;                 for (int bj = 0; bj < 2; ++bj) { const float sc = (bj ? sc1 : sc0) * rs; const f32x4 v0 = acc[ai][bj][m][0] * sc, v1 = acc[ai][bj][m][1] * sc;
;                     u32x4 w; w.x = cvt_pk_bf16(v0[0], v0[1]); w.y = cvt_pk_bf16(v0[2], v0[3]); w.z = cvt_pk_bf16(v1[0], v1[1]); w.w = cvt_pk_bf16(v1[2], v1[3]);
;                     *(u32x4*)(rowp + bj * HALF) = w; } }
; template <class Epi, class Sched, bool ALIGN_EPI = false, bool SP2 = false, bool F8 = false>
; __device__ __forceinline__ void gemm_phase(PG8_LAS unsigned char* lds, const Gemm g, const Sched& S, const Epi& E) {
;     ...
;         if (!has_next) break;
; #pragma unroll
;         for (int a = 0; a < 2; ++a)
; #pragma unroll
;             for (int b = 0; b < 2; ++b)
; #pragma unroll
;                 for (int m = 0; m < 4; ++m)
; #pragma unroll
;                     for (int n = 0; n < 2; ++n) acc[a][b][m][n] = (f32x4){0.f, 0.f, 0.f, 0.f};
;         cur = nxt; cA = nA; cB = nB; ++ui;
;         if constexpr (ALIGN_EPI) { if (wr == 1) PG8_BAR; }
	v_mul_f32_e32 v6, v21, v18
	v_pk_mul_f32 v[8:9], v[96:97], v[6:7] op_sel_hi:[1,0]
	v_pk_mul_f32 v[12:13], v[94:95], v[6:7] op_sel_hi:[1,0]
	v_pk_mul_f32 v[14:15], v[92:93], v[6:7] op_sel_hi:[1,0]
	v_pk_mul_f32 v[16:17], v[90:91], v[6:7] op_sel_hi:[1,0]
	v_cvt_pk_bf16_f32 v6, v12, v13
	v_cvt_pk_bf16_f32 v7, v8, v9
	v_cvt_pk_bf16_f32 v8, v16, v17
	v_cvt_pk_bf16_f32 v9, v14, v15
	global_store_dwordx4 v[10:11], v[6:9], off
	s_nop 1
	v_mul_f32_e32 v6, v22, v18
	v_pk_mul_f32 v[8:9], v[80:81], v[6:7] op_sel_hi:[1,0]
	v_pk_mul_f32 v[12:13], v[78:79], v[6:7] op_sel_hi:[1,0]
	v_pk_mul_f32 v[14:15], v[76:77], v[6:7] op_sel_hi:[1,0]
	v_pk_mul_f32 v[16:17], v[74:75], v[6:7] op_sel_hi:[1,0]
	v_cvt_pk_bf16_f32 v6, v12, v13
	v_cvt_pk_bf16_f32 v7, v8, v9
	v_cvt_pk_bf16_f32 v8, v16, v17
	v_cvt_pk_bf16_f32 v9, v14, v15
	global_store_dwordx4 v[10:11], v[6:9], off offset:256
	ds_read2_b32 v[10:11], v191 offset0:144 offset1:160
	s_nop 0
	v_add_u32_e32 v6, 0x90, v20
	v_mad_i64_i32 v[6:7], s[4:5], v6, s81, v[2:3]
	v_lshl_add_u64 v[12:13], v[6:7], 0, v[4:5]
	s_waitcnt lgkmcnt(0)
	v_mul_f32_e32 v6, v21, v10
	v_pk_mul_f32 v[8:9], v[88:89], v[6:7] op_sel_hi:[1,0]
	v_pk_mul_f32 v[14:15], v[86:87], v[6:7] op_sel_hi:[1,0]
	v_pk_mul_f32 v[16:17], v[84:85], v[6:7] op_sel_hi:[1,0]
	v_pk_mul_f32 v[18:19], v[82:83], v[6:7] op_sel_hi:[1,0]
	v_cvt_pk_bf16_f32 v6, v14, v15
	v_cvt_pk_bf16_f32 v7, v8, v9
	v_cvt_pk_bf16_f32 v8, v18, v19
	v_cvt_pk_bf16_f32 v9, v16, v17
	global_store_dwordx4 v[12:13], v[6:9], off
	s_nop 1
	v_mul_f32_e32 v6, v22, v10
	v_pk_mul_f32 v[8:9], v[64:65], v[6:7] op_sel_hi:[1,0]
	v_pk_mul_f32 v[14:15], v[62:63], v[6:7] op_sel_hi:[1,0]
	v_pk_mul_f32 v[16:17], v[60:61], v[6:7] op_sel_hi:[1,0]
	v_pk_mul_f32 v[18:19], v[58:59], v[6:7] op_sel_hi:[1,0]
	v_cvt_pk_bf16_f32 v6, v14, v15
	v_cvt_pk_bf16_f32 v7, v8, v9
	v_cvt_pk_bf16_f32 v8, v18, v19
	v_cvt_pk_bf16_f32 v9, v16, v17
	global_store_dwordx4 v[12:13], v[6:9], off offset:256
	s_nop 1
	v_add_u32_e32 v6, 0xa0, v20
	v_mad_i64_i32 v[6:7], s[4:5], v6, s81, v[2:3]
	v_lshl_add_u64 v[12:13], v[6:7], 0, v[4:5]
	v_mul_f32_e32 v6, v21, v11
	v_pk_mul_f32 v[8:9], v[72:73], v[6:7] op_sel_hi:[1,0]
	v_pk_mul_f32 v[14:15], v[70:71], v[6:7] op_sel_hi:[1,0]
	v_pk_mul_f32 v[16:17], v[68:69], v[6:7] op_sel_hi:[1,0]
	v_pk_mul_f32 v[18:19], v[66:67], v[6:7] op_sel_hi:[1,0]
	v_cvt_pk_bf16_f32 v6, v14, v15
	v_cvt_pk_bf16_f32 v7, v8, v9
	v_cvt_pk_bf16_f32 v8, v18, v19
	v_cvt_pk_bf16_f32 v9, v16, v17
	global_store_dwordx4 v[12:13], v[6:9], off
	s_nop 1
	v_mul_f32_e32 v6, v22, v11
	v_pk_mul_f32 v[8:9], v[48:49], v[6:7] op_sel_hi:[1,0]
	v_pk_mul_f32 v[10:11], v[46:47], v[6:7] op_sel_hi:[1,0]
	v_pk_mul_f32 v[14:15], v[44:45], v[6:7] op_sel_hi:[1,0]
	v_pk_mul_f32 v[16:17], v[42:43], v[6:7] op_sel_hi:[1,0]
	v_cvt_pk_bf16_f32 v6, v10, v11
	v_cvt_pk_bf16_f32 v7, v8, v9
	v_cvt_pk_bf16_f32 v8, v16, v17
	v_cvt_pk_bf16_f32 v9, v14, v15
	global_store_dwordx4 v[12:13], v[6:9], off offset:256
	s_nop 1
	v_add_u32_e32 v6, 0xb0, v20
	v_mad_i64_i32 v[2:3], s[4:5], v6, s81, v[2:3]
	v_lshl_add_u64 v[6:7], v[2:3], 0, v[4:5]
	v_mul_f32_e32 v2, v21, v23
	v_pk_mul_f32 v[4:5], v[56:57], v[2:3] op_sel_hi:[1,0]
	v_pk_mul_f32 v[8:9], v[54:55], v[2:3] op_sel_hi:[1,0]
	v_pk_mul_f32 v[10:11], v[52:53], v[2:3] op_sel_hi:[1,0]
	v_pk_mul_f32 v[12:13], v[50:51], v[2:3] op_sel_hi:[1,0]
	v_cvt_pk_bf16_f32 v2, v8, v9
	v_cvt_pk_bf16_f32 v3, v4, v5
	v_cvt_pk_bf16_f32 v4, v12, v13
	v_cvt_pk_bf16_f32 v5, v10, v11
	global_store_dwordx4 v[6:7], v[2:5], off
	s_nop 1
	v_mul_f32_e32 v2, v22, v23
	v_pk_mul_f32 v[4:5], v[40:41], v[2:3] op_sel_hi:[1,0]
	v_pk_mul_f32 v[8:9], v[38:39], v[2:3] op_sel_hi:[1,0]
	v_pk_mul_f32 v[10:11], v[36:37], v[2:3] op_sel_hi:[1,0]
	v_pk_mul_f32 v[12:13], v[34:35], v[2:3] op_sel_hi:[1,0]
	v_cvt_pk_bf16_f32 v2, v8, v9
	v_cvt_pk_bf16_f32 v3, v4, v5
	v_cvt_pk_bf16_f32 v4, v12, v13
	v_cvt_pk_bf16_f32 v5, v10, v11
	global_store_dwordx4 v[6:7], v[2:5], off offset:256
	s_barrier
	s_cbranch_vccnz .LBB0_798
	s_andn2_b64 vcc, exec, s[14:15]
	s_cbranch_vccnz .LBB0_797
	s_barrier
	s_branch .LBB0_797

; #define PG8_STAGE(bufoff, gbase, voff) do { _Pragma("unroll") for (int _i = 0; _i < 2; ++_i) \
;         __builtin_amdgcn_global_load_lds((const unsigned*)((const char*)(gbase) + (voff)[_i]), (PG8_LAS unsigned*)(lds + (bufoff) + ldsw + _i * 8192), 16, 0, 0); } while (0)
; #define PG8_LDA(dst, b, h) do { _Pragma("unroll") for (int m = 0; m < 4; ++m) Frag<F8>::load(dst[m], lds + PG8_SA(b, h) + aoff + m * 2048); } while (0)
; #define PG8_LDB(dst, b, h) do { _Pragma("unroll") for (int n = 0; n < 2; ++n) Frag<F8>::load(dst[n], lds + PG8_SB(b, h) + boff + n * 2048); } while (0)
; #define PG8_MMA(ai, bj, At, Bt) do { __builtin_amdgcn_s_setprio(3); _Pragma("unroll") for (int m = 0; m < 4; ++m) _Pragma("unroll") for (int n = 0; n < 2; ++n) Frag<F8>::mma(acc[ai][bj][m][n], Bt[n], At[m]); \
;         __builtin_amdgcn_s_setprio(0); } while (0)
; #define PG8_WAIT_V(n) asm volatile("s_waitcnt vmcnt(" #n ")" ::: "memory")
; #define PG8_BAR __builtin_amdgcn_s_barrier()
; template <class Epi, class Sched, bool ALIGN_EPI = false, bool SP2 = false, bool F8 = false>
; __device__ __forceinline__ void gemm_phase(PG8_LAS unsigned char* lds, const Gemm g, const Sched& S, const Epi& E) {
;     ...
;         const bool has_next = S.next(ui + 1, nxt);
;         const char* nA = has_next ? (const char*)g.A + (size_t)nxt.pm * tstep + nxt.ko : cA; const char* nB = has_next ? (const char*)g.Bt + (size_t)nxt.pn * tstep + nxt.ko : cB;
;         for (int t = 0; t < nt; t += 2) {
;             const bool last = (t == nt - 2);
;             const char* a1 = cA + (size_t)(t + 1) * kstep;
;             const char* a2 = last ? nA : cA + (size_t)(t + 2) * kstep; const char* b2 = last ? nB : cB + (size_t)(t + 2) * kstep;
;             const char* a3 = a2 + kstep; const char* b3 = b2 + kstep;
;             if (last && has_next) S.a_ready(nxt);
;             if constexpr (SP2) {
;             PG8_LDB(B0, 0, 0); PG8_LDB(B1, 0, 1); PG8_SCHED; PG8_LDA(At, 0, 0); PG8_STAGE(PG8_SA(1, 1), a1 + hstep, voffA);
;             PG8_WAIT_V(8); PG8_WAIT_L(0); PG8_BAR; PG8_MMA(0, 0, At, B0); PG8_MMA(0, 1, At, B1); PG8_BAR; PG8_SCHED;
;             PG8_LDA(At, 0, 1); PG8_STAGE(PG8_SB(0, 0), b2, voffB); PG8_STAGE(PG8_SB(0, 1), b2 + hstep, voffB); PG8_STAGE(PG8_SA(0, 0), a2, voffA);
;             PG8_WAIT_V(8); PG8_WAIT_L(0); PG8_BAR; PG8_MMA(1, 0, At, B0); PG8_MMA(1, 1, At, B1); PG8_BAR; PG8_SCHED;
.LBB0_1309:
	s_ashr_i32 s25, s24, 31
	s_lshl_b64 s[4:5], s[24:25], 18
	s_add_u32 s30, s48, s4
	s_addc_u32 s31, s49, s5
	s_and_b64 s[4:5], s[22:23], exec
	s_cselect_b32 s25, s31, s43
	s_cselect_b32 s77, s30, s42
	s_ashr_i32 s27, s26, 31
	s_lshl_b64 s[4:5], s[26:27], 18
	s_add_u32 s36, s50, s4
	s_addc_u32 s37, s51, s5
	s_and_b64 s[4:5], s[22:23], exec
	s_cselect_b32 s27, s37, s45
	s_cselect_b32 s78, s36, s44
	s_add_u32 s42, s42, 0x20080
	s_addc_u32 s43, s43, 0
	s_add_u32 s79, s44, 0x100
	s_addc_u32 s80, s45, 0
	s_mov_b32 s81, -2
	ds_read_b128 v[18:21], v186
	ds_read_b128 v[22:25], v186 offset:1024
	ds_read_b128 v[26:29], v186 offset:2048
	ds_read_b128 v[30:33], v186 offset:3072
	ds_read_b128 v[2:5], v187
	ds_read_b128 v[6:9], v187 offset:1024
	ds_read_b128 v[10:13], v187 offset:2048
	ds_read_b128 v[14:17], v187 offset:3072
	s_add_u32 s0, s42, 0xfffe0080
	s_addc_u32 s1, s43, -1
	s_cmp_eq_u32 s81, 4
	s_cselect_b32 s47, s25, s1
	s_cselect_b32 s46, s77, s0
	s_cselect_b32 s45, s27, s80
	s_cselect_b32 s44, s78, s79
	v_lshl_add_u64 v[214:215], s[42:43], 0, v[172:173]
	s_add_i32 m0, s39, 0xc000
	ds_read_b128 v[176:179], v188
	ds_read_b128 v[180:183], v188 offset:1024
	ds_read_b128 v[190:193], v188 offset:2048
	ds_read_b128 v[194:197], v188 offset:3072
	ds_read_b128 v[198:201], v188 offset:4096
	ds_read_b128 v[202:205], v188 offset:5120
	ds_read_b128 v[206:209], v188 offset:6144
	ds_read_b128 v[210:213], v188 offset:7168
	global_load_lds_dwordx4 v[214:215], off
	v_lshl_add_u64 v[214:215], s[42:43], 0, v[174:175]
	s_add_i32 m0, s39, 0xe000
	s_nop 0
	global_load_lds_dwordx4 v[214:215], off
	s_waitcnt vmcnt(8)
	s_waitcnt lgkmcnt(0)
	s_barrier
	s_setprio 3
	s_waitcnt lgkmcnt(0)
	v_mfma_scale_f32_16x16x128_f8f6f4 v[158:161], v[18:25], v[176:183], 0, v189, v189 op_sel_hi:[0, 0, 0]
	v_mfma_scale_f32_16x16x128_f8f6f4 v[150:153], v[26:33], v[176:183], 0, v189, v189 op_sel_hi:[0, 0, 0]
	v_mfma_scale_f32_16x16x128_f8f6f4 v[142:145], v[18:25], v[190:197], 0, v189, v189 op_sel_hi:[0, 0, 0]
	v_mfma_scale_f32_16x16x128_f8f6f4 v[134:137], v[26:33], v[190:197], 0, v189, v189 op_sel_hi:[0, 0, 0]
	v_mfma_scale_f32_16x16x128_f8f6f4 v[126:129], v[18:25], v[198:205], 0, v189, v189 op_sel_hi:[0, 0, 0]
	v_mfma_scale_f32_16x16x128_f8f6f4 v[118:121], v[26:33], v[198:205], 0, v189, v189 op_sel_hi:[0, 0, 0]
	v_mfma_scale_f32_16x16x128_f8f6f4 v[110:113], v[18:25], v[206:213], 0, v189, v189 op_sel_hi:[0, 0, 0]
	v_mfma_scale_f32_16x16x128_f8f6f4 v[102:105], v[26:33], v[206:213], 0, v189, v189 op_sel_hi:[0, 0, 0]
	s_setprio 0
	s_setprio 3
	v_mfma_scale_f32_16x16x128_f8f6f4 v[154:157], v[2:9], v[176:183], 0, v189, v189 op_sel_hi:[0, 0, 0]
	v_mfma_scale_f32_16x16x128_f8f6f4 v[146:149], v[10:17], v[176:183], 0, v189, v189 op_sel_hi:[0, 0, 0]
	v_mfma_scale_f32_16x16x128_f8f6f4 v[138:141], v[2:9], v[190:197], 0, v189, v189 op_sel_hi:[0, 0, 0]
	v_mfma_scale_f32_16x16x128_f8f6f4 v[130:133], v[10:17], v[190:197], 0, v189, v189 op_sel_hi:[0, 0, 0]
	v_mfma_scale_f32_16x16x128_f8f6f4 v[122:125], v[2:9], v[198:205], 0, v189, v189 op_sel_hi:[0, 0, 0]
	v_mfma_scale_f32_16x16x128_f8f6f4 v[114:117], v[10:17], v[198:205], 0, v189, v189 op_sel_hi:[0, 0, 0]
	v_mfma_scale_f32_16x16x128_f8f6f4 v[106:109], v[2:9], v[206:213], 0, v189, v189 op_sel_hi:[0, 0, 0]
	v_mfma_scale_f32_16x16x128_f8f6f4 v[98:101], v[10:17], v[206:213], 0, v189, v189 op_sel_hi:[0, 0, 0]
	s_setprio 0
	s_barrier
	s_add_i32 s0, s74, s52
	v_lshl_add_u64 v[176:177], s[44:45], 0, v[168:169]
	s_mov_b32 m0, s0
	ds_read_b128 v[190:193], v188 offset:16384
	ds_read_b128 v[194:197], v188 offset:17408
	ds_read_b128 v[198:201], v188 offset:18432
	ds_read_b128 v[202:205], v188 offset:19456
	ds_read_b128 v[206:209], v188 offset:20480
	ds_read_b128 v[210:213], v188 offset:21504
	ds_read_b128 v[214:217], v188 offset:22528
	ds_read_b128 v[218:221], v188 offset:23552
	global_load_lds_dwordx4 v[176:177], off
	s_add_i32 m0, s0, 0x2000
	s_add_u32 s4, s44, 0x20000
	v_lshl_add_u64 v[178:179], s[44:45], 0, v[164:165]
	s_addc_u32 s5, s45, 0
	s_add_i32 s0, s75, s52
	global_load_lds_dwordx4 v[178:179], off
	v_lshl_add_u64 v[180:181], s[4:5], 0, v[168:169]
	s_mov_b32 m0, s0
	v_lshl_add_u64 v[182:183], s[46:47], 0, v[166:167]
	global_load_lds_dwordx4 v[180:181], off
	v_lshl_add_u64 v[180:181], s[4:5], 0, v[164:165]
	s_add_i32 m0, s0, 0x2000
	s_nop 0
	global_load_lds_dwordx4 v[180:181], off
	v_lshl_add_u64 v[180:181], s[46:47], 0, v[170:171]
	s_mov_b32 m0, s39
	s_nop 0
	global_load_lds_dwordx4 v[180:181], off
	s_mov_b32 m0, s41
	s_nop 0
	global_load_lds_dwordx4 v[182:183], off
	s_waitcnt vmcnt(8)
	s_waitcnt lgkmcnt(0)
	s_barrier
	s_setprio 3
	s_waitcnt lgkmcnt(0)
	v_mfma_scale_f32_16x16x128_f8f6f4 v[94:97], v[18:25], v[190:197], 0, v189, v189 op_sel_hi:[0, 0, 0]
	v_mfma_scale_f32_16x16x128_f8f6f4 v[86:89], v[26:33], v[190:197], 0, v189, v189 op_sel_hi:[0, 0, 0]
	v_mfma_scale_f32_16x16x128_f8f6f4 v[78:81], v[18:25], v[198:205], 0, v189, v189 op_sel_hi:[0, 0, 0]
	v_mfma_scale_f32_16x16x128_f8f6f4 v[70:73], v[26:33], v[198:205], 0, v189, v189 op_sel_hi:[0, 0, 0]
	v_mfma_scale_f32_16x16x128_f8f6f4 v[62:65], v[18:25], v[206:213], 0, v189, v189 op_sel_hi:[0, 0, 0]
	v_mfma_scale_f32_16x16x128_f8f6f4 v[54:57], v[26:33], v[206:213], 0, v189, v189 op_sel_hi:[0, 0, 0]
	v_mfma_scale_f32_16x16x128_f8f6f4 v[46:49], v[18:25], v[214:221], 0, v189, v189 op_sel_hi:[0, 0, 0]
	v_mfma_scale_f32_16x16x128_f8f6f4 v[38:41], v[26:33], v[214:221], 0, v189, v189 op_sel_hi:[0, 0, 0]
	s_setprio 0
	s_setprio 3
	v_mfma_scale_f32_16x16x128_f8f6f4 v[90:93], v[2:9], v[190:197], 0, v189, v189 op_sel_hi:[0, 0, 0]
	v_mfma_scale_f32_16x16x128_f8f6f4 v[82:85], v[10:17], v[190:197], 0, v189, v189 op_sel_hi:[0, 0, 0]
	v_mfma_scale_f32_16x16x128_f8f6f4 v[74:77], v[2:9], v[198:205], 0, v189, v189 op_sel_hi:[0, 0, 0]
	v_mfma_scale_f32_16x16x128_f8f6f4 v[66:69], v[10:17], v[198:205], 0, v189, v189 op_sel_hi:[0, 0, 0]
	v_mfma_scale_f32_16x16x128_f8f6f4 v[58:61], v[2:9], v[206:213], 0, v189, v189 op_sel_hi:[0, 0, 0]
	v_mfma_scale_f32_16x16x128_f8f6f4 v[50:53], v[10:17], v[206:213], 0, v189, v189 op_sel_hi:[0, 0, 0]
	v_mfma_scale_f32_16x16x128_f8f6f4 v[42:45], v[2:9], v[214:221], 0, v189, v189 op_sel_hi:[0, 0, 0]
	v_mfma_scale_f32_16x16x128_f8f6f4 v[34:37], v[10:17], v[214:221], 0, v189, v189 op_sel_hi:[0, 0, 0]
	s_setprio 0
	s_barrier
; #define PG8_STAGE(bufoff, gbase, voff) do { _Pragma("unroll") for (int _i = 0; _i < 2; ++_i) \
;         __builtin_amdgcn_global_load_lds((const unsigned*)((const char*)(gbase) + (voff)[_i]), (PG8_LAS unsigned*)(lds + (bufoff) + ldsw + _i * 8192), 16, 0, 0); } while (0)
; #define PG8_LDA(dst, b, h) do { _Pragma("unroll") for (int m = 0; m < 4; ++m) Frag<F8>::load(dst[m], lds + PG8_SA(b, h) + aoff + m * 2048); } while (0)
; #define PG8_LDB(dst, b, h) do { _Pragma("unroll") for (int n = 0; n < 2; ++n) Frag<F8>::load(dst[n], lds + PG8_SB(b, h) + boff + n * 2048); } while (0)
; #define PG8_MMA(ai, bj, At, Bt) do { __builtin_amdgcn_s_setprio(3); _Pragma("unroll") for (int m = 0; m < 4; ++m) _Pragma("unroll") for (int n = 0; n < 2; ++n) Frag<F8>::mma(acc[ai][bj][m][n], Bt[n], At[m]); \
;         __builtin_amdgcn_s_setprio(0); } while (0)
; #define PG8_WAIT_V(n) asm volatile("s_waitcnt vmcnt(" #n ")" ::: "memory")
; #define PG8_WAIT_L(n) asm volatile("s_waitcnt lgkmcnt(" #n ")" ::: "memory")
; #define PG8_BAR __builtin_amdgcn_s_barrier()
; #define PG8_SCHED __builtin_amdgcn_sched_barrier(0)
; template <class Epi, class Sched, bool ALIGN_EPI = false, bool SP2 = false, bool F8 = false>
; __device__ __forceinline__ void gemm_phase(PG8_LAS unsigned char* lds, const Gemm g, const Sched& S, const Epi& E) {
;     ...
;             PG8_LDB(B0, 1, 0); PG8_LDB(B1, 1, 1); PG8_SCHED; PG8_LDA(At, 1, 0); PG8_STAGE(PG8_SA(0, 1), a2 + hstep, voffA);
;             PG8_WAIT_V(8); PG8_WAIT_L(0); PG8_BAR; PG8_MMA(0, 0, At, B0); PG8_MMA(0, 1, At, B1); PG8_BAR; PG8_SCHED;
;             PG8_LDA(At, 1, 1); PG8_STAGE(PG8_SB(1, 0), b3, voffB); PG8_STAGE(PG8_SB(1, 1), b3 + hstep, voffB); PG8_STAGE(PG8_SA(1, 0), a3, voffA);
;             PG8_WAIT_V(8); PG8_WAIT_L(0); PG8_BAR; PG8_MMA(1, 0, At, B0); PG8_MMA(1, 1, At, B1); PG8_BAR; PG8_SCHED;
	s_add_i32 s0, 0, 0x18000
	s_add_i32 s1, 0, 0x1c000
	v_add_u32_e32 v14, s0, v184
	v_add_u32_e32 v30, s1, v184
	ds_read_b128 v[2:5], v14
	ds_read_b128 v[6:9], v14 offset:1024
	ds_read_b128 v[10:13], v14 offset:2048
	ds_read_b128 v[14:17], v14 offset:3072
	ds_read_b128 v[18:21], v30
	ds_read_b128 v[22:25], v30 offset:1024
	ds_read_b128 v[26:29], v30 offset:2048
	ds_read_b128 v[30:33], v30 offset:3072
	s_add_u32 s4, s46, 0x20000
	s_addc_u32 s5, s47, 0
	s_mov_b32 m0, s58
	v_lshl_add_u64 v[222:223], s[4:5], 0, v[170:171]
	ds_read_b128 v[190:193], v188 offset:32768
	ds_read_b128 v[194:197], v188 offset:33792
	ds_read_b128 v[198:201], v188 offset:34816
	ds_read_b128 v[202:205], v188 offset:35840
	ds_read_b128 v[206:209], v188 offset:36864
	ds_read_b128 v[210:213], v188 offset:37888
	ds_read_b128 v[214:217], v188 offset:38912
	ds_read_b128 v[218:221], v188 offset:39936
	global_load_lds_dwordx4 v[222:223], off
	v_lshl_add_u64 v[222:223], s[4:5], 0, v[166:167]
	s_mov_b32 m0, s59
	s_nop 0
	global_load_lds_dwordx4 v[222:223], off
	s_waitcnt vmcnt(8)
	s_waitcnt lgkmcnt(0)
	s_barrier
	s_setprio 3
	s_waitcnt lgkmcnt(0)
	v_mfma_scale_f32_16x16x128_f8f6f4 v[158:161], v[2:9], v[190:197], v[158:161], v189, v189 op_sel_hi:[0,0,0]
	v_mfma_scale_f32_16x16x128_f8f6f4 v[150:153], v[10:17], v[190:197], v[150:153], v189, v189 op_sel_hi:[0,0,0]
	v_mfma_scale_f32_16x16x128_f8f6f4 v[142:145], v[2:9], v[198:205], v[142:145], v189, v189 op_sel_hi:[0,0,0]
	v_mfma_scale_f32_16x16x128_f8f6f4 v[134:137], v[10:17], v[198:205], v[134:137], v189, v189 op_sel_hi:[0,0,0]
	v_mfma_scale_f32_16x16x128_f8f6f4 v[126:129], v[2:9], v[206:213], v[126:129], v189, v189 op_sel_hi:[0,0,0]
	v_mfma_scale_f32_16x16x128_f8f6f4 v[118:121], v[10:17], v[206:213], v[118:121], v189, v189 op_sel_hi:[0,0,0]
	v_mfma_scale_f32_16x16x128_f8f6f4 v[110:113], v[2:9], v[214:221], v[110:113], v189, v189 op_sel_hi:[0,0,0]
	v_mfma_scale_f32_16x16x128_f8f6f4 v[102:105], v[10:17], v[214:221], v[102:105], v189, v189 op_sel_hi:[0,0,0]
	s_setprio 0
	s_setprio 3
	v_mfma_scale_f32_16x16x128_f8f6f4 v[154:157], v[18:25], v[190:197], v[154:157], v189, v189 op_sel_hi:[0,0,0]
	v_mfma_scale_f32_16x16x128_f8f6f4 v[146:149], v[26:33], v[190:197], v[146:149], v189, v189 op_sel_hi:[0,0,0]
	v_mfma_scale_f32_16x16x128_f8f6f4 v[138:141], v[18:25], v[198:205], v[138:141], v189, v189 op_sel_hi:[0,0,0]
	v_mfma_scale_f32_16x16x128_f8f6f4 v[130:133], v[26:33], v[198:205], v[130:133], v189, v189 op_sel_hi:[0,0,0]
	v_mfma_scale_f32_16x16x128_f8f6f4 v[122:125], v[18:25], v[206:213], v[122:125], v189, v189 op_sel_hi:[0,0,0]
	v_mfma_scale_f32_16x16x128_f8f6f4 v[114:117], v[26:33], v[206:213], v[114:117], v189, v189 op_sel_hi:[0,0,0]
	v_mfma_scale_f32_16x16x128_f8f6f4 v[106:109], v[18:25], v[214:221], v[106:109], v189, v189 op_sel_hi:[0,0,0]
	v_mfma_scale_f32_16x16x128_f8f6f4 v[98:101], v[26:33], v[214:221], v[98:101], v189, v189 op_sel_hi:[0,0,0]
	s_setprio 0
	s_barrier
	s_add_i32 s0, s0, s52
	v_lshl_add_u64 v[176:177], v[176:177], 0, s[14:15]
	s_mov_b32 m0, s0
	ds_read_b128 v[190:193], v188 offset:49152
	ds_read_b128 v[194:197], v188 offset:50176
	ds_read_b128 v[198:201], v188 offset:51200
	ds_read_b128 v[202:205], v188 offset:52224
	ds_read_b128 v[206:209], v188 offset:53248
	ds_read_b128 v[210:213], v188 offset:54272
	ds_read_b128 v[214:217], v188 offset:55296
	ds_read_b128 v[218:221], v188 offset:56320
	global_load_lds_dwordx4 v[176:177], off
	s_add_i32 m0, s0, 0x2000
	s_add_u32 s4, s44, 0x20080
	v_lshl_add_u64 v[176:177], v[178:179], 0, s[14:15]
	s_addc_u32 s5, s45, 0
	s_add_i32 s0, s1, s52
	global_load_lds_dwordx4 v[176:177], off
	v_lshl_add_u64 v[176:177], s[4:5], 0, v[168:169]
	s_mov_b32 m0, s0
	s_nop 0
	global_load_lds_dwordx4 v[176:177], off
	v_lshl_add_u64 v[176:177], s[4:5], 0, v[164:165]
	s_add_i32 m0, s0, 0x2000
	s_nop 0
	global_load_lds_dwordx4 v[176:177], off
	v_lshl_add_u64 v[176:177], v[180:181], 0, s[14:15]
	s_mov_b32 m0, s60
	s_nop 0
	global_load_lds_dwordx4 v[176:177], off
	v_lshl_add_u64 v[176:177], v[182:183], 0, s[14:15]
	s_mov_b32 m0, s61
	s_nop 0
	global_load_lds_dwordx4 v[176:177], off
	s_waitcnt vmcnt(8)
	s_waitcnt lgkmcnt(0)
	s_barrier
	s_setprio 3
	s_waitcnt lgkmcnt(0)
	v_mfma_scale_f32_16x16x128_f8f6f4 v[94:97], v[2:9], v[190:197], v[94:97], v189, v189 op_sel_hi:[0,0,0]
	v_mfma_scale_f32_16x16x128_f8f6f4 v[86:89], v[10:17], v[190:197], v[86:89], v189, v189 op_sel_hi:[0,0,0]
	v_mfma_scale_f32_16x16x128_f8f6f4 v[78:81], v[2:9], v[198:205], v[78:81], v189, v189 op_sel_hi:[0,0,0]
	v_mfma_scale_f32_16x16x128_f8f6f4 v[70:73], v[10:17], v[198:205], v[70:73], v189, v189 op_sel_hi:[0,0,0]
	v_mfma_scale_f32_16x16x128_f8f6f4 v[62:65], v[2:9], v[206:213], v[62:65], v189, v189 op_sel_hi:[0,0,0]
	v_mfma_scale_f32_16x16x128_f8f6f4 v[54:57], v[10:17], v[206:213], v[54:57], v189, v189 op_sel_hi:[0,0,0]
	v_mfma_scale_f32_16x16x128_f8f6f4 v[46:49], v[2:9], v[214:221], v[46:49], v189, v189 op_sel_hi:[0,0,0]
	v_mfma_scale_f32_16x16x128_f8f6f4 v[38:41], v[10:17], v[214:221], v[38:41], v189, v189 op_sel_hi:[0,0,0]
	s_setprio 0
	s_setprio 3
	v_mfma_scale_f32_16x16x128_f8f6f4 v[90:93], v[18:25], v[190:197], v[90:93], v189, v189 op_sel_hi:[0,0,0]
	v_mfma_scale_f32_16x16x128_f8f6f4 v[82:85], v[26:33], v[190:197], v[82:85], v189, v189 op_sel_hi:[0,0,0]
	v_mfma_scale_f32_16x16x128_f8f6f4 v[74:77], v[18:25], v[198:205], v[74:77], v189, v189 op_sel_hi:[0,0,0]
	v_mfma_scale_f32_16x16x128_f8f6f4 v[66:69], v[26:33], v[198:205], v[66:69], v189, v189 op_sel_hi:[0,0,0]
	v_mfma_scale_f32_16x16x128_f8f6f4 v[58:61], v[18:25], v[206:213], v[58:61], v189, v189 op_sel_hi:[0,0,0]
	v_mfma_scale_f32_16x16x128_f8f6f4 v[50:53], v[26:33], v[206:213], v[50:53], v189, v189 op_sel_hi:[0,0,0]
	v_mfma_scale_f32_16x16x128_f8f6f4 v[42:45], v[18:25], v[214:221], v[42:45], v189, v189 op_sel_hi:[0,0,0]
	v_mfma_scale_f32_16x16x128_f8f6f4 v[34:37], v[26:33], v[214:221], v[34:37], v189, v189 op_sel_hi:[0,0,0]
	s_setprio 0
	s_add_i32 s81, s81, 2
	s_add_u32 s42, s42, 0x100
	s_addc_u32 s43, s43, 0
	s_add_u32 s79, s79, 0x100
	s_addc_u32 s80, s80, 0
	s_cmp_gt_u32 s81, 5
	s_cbranch_scc1 .Lpeel_exit_3
; #define PG8_STAGE(bufoff, gbase, voff) do { _Pragma("unroll") for (int _i = 0; _i < 2; ++_i) \
;         __builtin_amdgcn_global_load_lds((const unsigned*)((const char*)(gbase) + (voff)[_i]), (PG8_LAS unsigned*)(lds + (bufoff) + ldsw + _i * 8192), 16, 0, 0); } while (0)
; #define PG8_LDA(dst, b, h) do { _Pragma("unroll") for (int m = 0; m < 4; ++m) Frag<F8>::load(dst[m], lds + PG8_SA(b, h) + aoff + m * 2048); } while (0)
; #define PG8_LDB(dst, b, h) do { _Pragma("unroll") for (int n = 0; n < 2; ++n) Frag<F8>::load(dst[n], lds + PG8_SB(b, h) + boff + n * 2048); } while (0)
; #define PG8_MMA(ai, bj, At, Bt) do { __builtin_amdgcn_s_setprio(3); _Pragma("unroll") for (int m = 0; m < 4; ++m) _Pragma("unroll") for (int n = 0; n < 2; ++n) Frag<F8>::mma(acc[ai][bj][m][n], Bt[n], At[m]); \
;         __builtin_amdgcn_s_setprio(0); } while (0)
; #define PG8_WAIT_V(n) asm volatile("s_waitcnt vmcnt(" #n ")" ::: "memory")
; #define PG8_WAIT_L(n) asm volatile("s_waitcnt lgkmcnt(" #n ")" ::: "memory")
; #define PG8_BAR __builtin_amdgcn_s_barrier()
; #define PG8_SCHED __builtin_amdgcn_sched_barrier(0)
; template <class Epi, class Sched, bool ALIGN_EPI = false, bool SP2 = false, bool F8 = false>
; __device__ __forceinline__ void gemm_phase(PG8_LAS unsigned char* lds, const Gemm g, const Sched& S, const Epi& E) {
;     ...
;             PG8_LDB(B0, 0, 0); PG8_LDB(B1, 0, 1); PG8_SCHED; PG8_LDA(At, 0, 0); PG8_STAGE(PG8_SA(1, 1), a1 + hstep, voffA);
;             PG8_WAIT_V(8); PG8_WAIT_L(0); PG8_BAR; PG8_MMA(0, 0, At, B0); PG8_MMA(0, 1, At, B1); PG8_BAR; PG8_SCHED;
;             PG8_LDA(At, 0, 1); PG8_STAGE(PG8_SB(0, 0), b2, voffB); PG8_STAGE(PG8_SB(0, 1), b2 + hstep, voffB); PG8_STAGE(PG8_SA(0, 0), a2, voffA);
;             PG8_WAIT_V(8); PG8_WAIT_L(0); PG8_BAR; PG8_MMA(1, 0, At, B0); PG8_MMA(1, 1, At, B1); PG8_BAR; PG8_SCHED;
.LBB0_1310:
	s_barrier
	ds_read_b128 v[18:21], v186
	ds_read_b128 v[22:25], v186 offset:1024
	ds_read_b128 v[26:29], v186 offset:2048
	ds_read_b128 v[30:33], v186 offset:3072
	ds_read_b128 v[2:5], v187
	ds_read_b128 v[6:9], v187 offset:1024
	ds_read_b128 v[10:13], v187 offset:2048
	ds_read_b128 v[14:17], v187 offset:3072
	s_add_u32 s0, s42, 0xfffe0080
	s_addc_u32 s1, s43, -1
	s_cmp_eq_u32 s81, 4
	s_cselect_b32 s47, s25, s1
	s_cselect_b32 s46, s77, s0
	s_cselect_b32 s45, s27, s80
	s_cselect_b32 s44, s78, s79
	v_lshl_add_u64 v[214:215], s[42:43], 0, v[172:173]
	s_add_i32 m0, s39, 0xc000
	ds_read_b128 v[176:179], v188
	ds_read_b128 v[180:183], v188 offset:1024
	ds_read_b128 v[190:193], v188 offset:2048
	ds_read_b128 v[194:197], v188 offset:3072
	ds_read_b128 v[198:201], v188 offset:4096
	ds_read_b128 v[202:205], v188 offset:5120
	ds_read_b128 v[206:209], v188 offset:6144
	ds_read_b128 v[210:213], v188 offset:7168
	global_load_lds_dwordx4 v[214:215], off
	v_lshl_add_u64 v[214:215], s[42:43], 0, v[174:175]
	s_add_i32 m0, s39, 0xe000
	s_nop 0
	global_load_lds_dwordx4 v[214:215], off
	s_waitcnt vmcnt(8)
	s_waitcnt lgkmcnt(0)
	s_barrier
	s_setprio 3
	s_waitcnt lgkmcnt(0)
	v_mfma_scale_f32_16x16x128_f8f6f4 v[158:161], v[18:25], v[176:183], v[158:161], v189, v189 op_sel_hi:[0,0,0]
	v_mfma_scale_f32_16x16x128_f8f6f4 v[150:153], v[26:33], v[176:183], v[150:153], v189, v189 op_sel_hi:[0,0,0]
	v_mfma_scale_f32_16x16x128_f8f6f4 v[142:145], v[18:25], v[190:197], v[142:145], v189, v189 op_sel_hi:[0,0,0]
	v_mfma_scale_f32_16x16x128_f8f6f4 v[134:137], v[26:33], v[190:197], v[134:137], v189, v189 op_sel_hi:[0,0,0]
	v_mfma_scale_f32_16x16x128_f8f6f4 v[126:129], v[18:25], v[198:205], v[126:129], v189, v189 op_sel_hi:[0,0,0]
	v_mfma_scale_f32_16x16x128_f8f6f4 v[118:121], v[26:33], v[198:205], v[118:121], v189, v189 op_sel_hi:[0,0,0]
	v_mfma_scale_f32_16x16x128_f8f6f4 v[110:113], v[18:25], v[206:213], v[110:113], v189, v189 op_sel_hi:[0,0,0]
	v_mfma_scale_f32_16x16x128_f8f6f4 v[102:105], v[26:33], v[206:213], v[102:105], v189, v189 op_sel_hi:[0,0,0]
	s_setprio 0
	s_setprio 3
	v_mfma_scale_f32_16x16x128_f8f6f4 v[154:157], v[2:9], v[176:183], v[154:157], v189, v189 op_sel_hi:[0,0,0]
	v_mfma_scale_f32_16x16x128_f8f6f4 v[146:149], v[10:17], v[176:183], v[146:149], v189, v189 op_sel_hi:[0,0,0]
	v_mfma_scale_f32_16x16x128_f8f6f4 v[138:141], v[2:9], v[190:197], v[138:141], v189, v189 op_sel_hi:[0,0,0]
	v_mfma_scale_f32_16x16x128_f8f6f4 v[130:133], v[10:17], v[190:197], v[130:133], v189, v189 op_sel_hi:[0,0,0]
	v_mfma_scale_f32_16x16x128_f8f6f4 v[122:125], v[2:9], v[198:205], v[122:125], v189, v189 op_sel_hi:[0,0,0]
	v_mfma_scale_f32_16x16x128_f8f6f4 v[114:117], v[10:17], v[198:205], v[114:117], v189, v189 op_sel_hi:[0,0,0]
	v_mfma_scale_f32_16x16x128_f8f6f4 v[106:109], v[2:9], v[206:213], v[106:109], v189, v189 op_sel_hi:[0,0,0]
	v_mfma_scale_f32_16x16x128_f8f6f4 v[98:101], v[10:17], v[206:213], v[98:101], v189, v189 op_sel_hi:[0,0,0]
	s_setprio 0
	s_barrier
	s_add_i32 s0, s74, s52
	v_lshl_add_u64 v[176:177], s[44:45], 0, v[168:169]
	s_mov_b32 m0, s0
	ds_read_b128 v[190:193], v188 offset:16384
	ds_read_b128 v[194:197], v188 offset:17408
	ds_read_b128 v[198:201], v188 offset:18432
	ds_read_b128 v[202:205], v188 offset:19456
	ds_read_b128 v[206:209], v188 offset:20480
	ds_read_b128 v[210:213], v188 offset:21504
	ds_read_b128 v[214:217], v188 offset:22528
	ds_read_b128 v[218:221], v188 offset:23552
	global_load_lds_dwordx4 v[176:177], off
	s_add_i32 m0, s0, 0x2000
	s_add_u32 s4, s44, 0x20000
	v_lshl_add_u64 v[178:179], s[44:45], 0, v[164:165]
	s_addc_u32 s5, s45, 0
	s_add_i32 s0, s75, s52
	global_load_lds_dwordx4 v[178:179], off
	v_lshl_add_u64 v[180:181], s[4:5], 0, v[168:169]
	s_mov_b32 m0, s0
	v_lshl_add_u64 v[182:183], s[46:47], 0, v[166:167]
	global_load_lds_dwordx4 v[180:181], off
	v_lshl_add_u64 v[180:181], s[4:5], 0, v[164:165]
	s_add_i32 m0, s0, 0x2000
	s_nop 0
	global_load_lds_dwordx4 v[180:181], off
	v_lshl_add_u64 v[180:181], s[46:47], 0, v[170:171]
	s_mov_b32 m0, s39
	s_nop 0
	global_load_lds_dwordx4 v[180:181], off
	s_mov_b32 m0, s41
	s_nop 0
	global_load_lds_dwordx4 v[182:183], off
	s_waitcnt vmcnt(8)
	s_waitcnt lgkmcnt(0)
	s_barrier
	s_setprio 3
	s_waitcnt lgkmcnt(0)
	v_mfma_scale_f32_16x16x128_f8f6f4 v[94:97], v[18:25], v[190:197], v[94:97], v189, v189 op_sel_hi:[0,0,0]
	v_mfma_scale_f32_16x16x128_f8f6f4 v[86:89], v[26:33], v[190:197], v[86:89], v189, v189 op_sel_hi:[0,0,0]
	v_mfma_scale_f32_16x16x128_f8f6f4 v[78:81], v[18:25], v[198:205], v[78:81], v189, v189 op_sel_hi:[0,0,0]
	v_mfma_scale_f32_16x16x128_f8f6f4 v[70:73], v[26:33], v[198:205], v[70:73], v189, v189 op_sel_hi:[0,0,0]
	v_mfma_scale_f32_16x16x128_f8f6f4 v[62:65], v[18:25], v[206:213], v[62:65], v189, v189 op_sel_hi:[0,0,0]
	v_mfma_scale_f32_16x16x128_f8f6f4 v[54:57], v[26:33], v[206:213], v[54:57], v189, v189 op_sel_hi:[0,0,0]
	v_mfma_scale_f32_16x16x128_f8f6f4 v[46:49], v[18:25], v[214:221], v[46:49], v189, v189 op_sel_hi:[0,0,0]
	v_mfma_scale_f32_16x16x128_f8f6f4 v[38:41], v[26:33], v[214:221], v[38:41], v189, v189 op_sel_hi:[0,0,0]
	s_setprio 0
	s_setprio 3
	v_mfma_scale_f32_16x16x128_f8f6f4 v[90:93], v[2:9], v[190:197], v[90:93], v189, v189 op_sel_hi:[0,0,0]
	v_mfma_scale_f32_16x16x128_f8f6f4 v[82:85], v[10:17], v[190:197], v[82:85], v189, v189 op_sel_hi:[0,0,0]
	v_mfma_scale_f32_16x16x128_f8f6f4 v[74:77], v[2:9], v[198:205], v[74:77], v189, v189 op_sel_hi:[0,0,0]
	v_mfma_scale_f32_16x16x128_f8f6f4 v[66:69], v[10:17], v[198:205], v[66:69], v189, v189 op_sel_hi:[0,0,0]
	v_mfma_scale_f32_16x16x128_f8f6f4 v[58:61], v[2:9], v[206:213], v[58:61], v189, v189 op_sel_hi:[0,0,0]
	v_mfma_scale_f32_16x16x128_f8f6f4 v[50:53], v[10:17], v[206:213], v[50:53], v189, v189 op_sel_hi:[0,0,0]
	v_mfma_scale_f32_16x16x128_f8f6f4 v[42:45], v[2:9], v[214:221], v[42:45], v189, v189 op_sel_hi:[0,0,0]
	v_mfma_scale_f32_16x16x128_f8f6f4 v[34:37], v[10:17], v[214:221], v[34:37], v189, v189 op_sel_hi:[0,0,0]
	s_setprio 0
	s_barrier
; #define PG8_STAGE(bufoff, gbase, voff) do { _Pragma("unroll") for (int _i = 0; _i < 2; ++_i) \
;         __builtin_amdgcn_global_load_lds((const unsigned*)((const char*)(gbase) + (voff)[_i]), (PG8_LAS unsigned*)(lds + (bufoff) + ldsw + _i * 8192), 16, 0, 0); } while (0)
; #define PG8_LDA(dst, b, h) do { _Pragma("unroll") for (int m = 0; m < 4; ++m) Frag<F8>::load(dst[m], lds + PG8_SA(b, h) + aoff + m * 2048); } while (0)
; #define PG8_LDB(dst, b, h) do { _Pragma("unroll") for (int n = 0; n < 2; ++n) Frag<F8>::load(dst[n], lds + PG8_SB(b, h) + boff + n * 2048); } while (0)
; #define PG8_MMA(ai, bj, At, Bt) do { __builtin_amdgcn_s_setprio(3); _Pragma("unroll") for (int m = 0; m < 4; ++m) _Pragma("unroll") for (int n = 0; n < 2; ++n) Frag<F8>::mma(acc[ai][bj][m][n], Bt[n], At[m]); \
;         __builtin_amdgcn_s_setprio(0); } while (0)
; #define PG8_WAIT_V(n) asm volatile("s_waitcnt vmcnt(" #n ")" ::: "memory")
; #define PG8_WAIT_L(n) asm volatile("s_waitcnt lgkmcnt(" #n ")" ::: "memory")
; #define PG8_BAR __builtin_amdgcn_s_barrier()
; #define PG8_SCHED __builtin_amdgcn_sched_barrier(0)
; template <class Epi, class Sched, bool ALIGN_EPI = false, bool SP2 = false, bool F8 = false>
; __device__ __forceinline__ void gemm_phase(PG8_LAS unsigned char* lds, const Gemm g, const Sched& S, const Epi& E) {
;     ...
;         for (int t = 0; t < nt; t += 2) {
;     ...
;             PG8_LDB(B0, 1, 0); PG8_LDB(B1, 1, 1); PG8_SCHED; PG8_LDA(At, 1, 0); PG8_STAGE(PG8_SA(0, 1), a2 + hstep, voffA);
;             PG8_WAIT_V(8); PG8_WAIT_L(0); PG8_BAR; PG8_MMA(0, 0, At, B0); PG8_MMA(0, 1, At, B1); PG8_BAR; PG8_SCHED;
;             PG8_LDA(At, 1, 1); PG8_STAGE(PG8_SB(1, 0), b3, voffB); PG8_STAGE(PG8_SB(1, 1), b3 + hstep, voffB); PG8_STAGE(PG8_SA(1, 0), a3, voffA);
;             PG8_WAIT_V(8); PG8_WAIT_L(0); PG8_BAR; PG8_MMA(1, 0, At, B0); PG8_MMA(1, 1, At, B1); PG8_BAR; PG8_SCHED;
	s_add_i32 s0, 0, 0x18000
	s_add_i32 s1, 0, 0x1c000
	v_add_u32_e32 v14, s0, v184
	v_add_u32_e32 v30, s1, v184
	ds_read_b128 v[2:5], v14
	ds_read_b128 v[6:9], v14 offset:1024
	ds_read_b128 v[10:13], v14 offset:2048
	ds_read_b128 v[14:17], v14 offset:3072
	ds_read_b128 v[18:21], v30
	ds_read_b128 v[22:25], v30 offset:1024
	ds_read_b128 v[26:29], v30 offset:2048
	ds_read_b128 v[30:33], v30 offset:3072
	s_add_u32 s4, s46, 0x20000
	s_addc_u32 s5, s47, 0
	s_mov_b32 m0, s58
	v_lshl_add_u64 v[222:223], s[4:5], 0, v[170:171]
	ds_read_b128 v[190:193], v188 offset:32768
	ds_read_b128 v[194:197], v188 offset:33792
	ds_read_b128 v[198:201], v188 offset:34816
	ds_read_b128 v[202:205], v188 offset:35840
	ds_read_b128 v[206:209], v188 offset:36864
	ds_read_b128 v[210:213], v188 offset:37888
	ds_read_b128 v[214:217], v188 offset:38912
	ds_read_b128 v[218:221], v188 offset:39936
	global_load_lds_dwordx4 v[222:223], off
	v_lshl_add_u64 v[222:223], s[4:5], 0, v[166:167]
	s_mov_b32 m0, s59
	s_nop 0
	global_load_lds_dwordx4 v[222:223], off
	s_waitcnt vmcnt(8)
	s_waitcnt lgkmcnt(0)
	s_barrier
	s_setprio 3
	s_waitcnt lgkmcnt(0)
	v_mfma_scale_f32_16x16x128_f8f6f4 v[158:161], v[2:9], v[190:197], v[158:161], v189, v189 op_sel_hi:[0,0,0]
	v_mfma_scale_f32_16x16x128_f8f6f4 v[150:153], v[10:17], v[190:197], v[150:153], v189, v189 op_sel_hi:[0,0,0]
	v_mfma_scale_f32_16x16x128_f8f6f4 v[142:145], v[2:9], v[198:205], v[142:145], v189, v189 op_sel_hi:[0,0,0]
	v_mfma_scale_f32_16x16x128_f8f6f4 v[134:137], v[10:17], v[198:205], v[134:137], v189, v189 op_sel_hi:[0,0,0]
	v_mfma_scale_f32_16x16x128_f8f6f4 v[126:129], v[2:9], v[206:213], v[126:129], v189, v189 op_sel_hi:[0,0,0]
	v_mfma_scale_f32_16x16x128_f8f6f4 v[118:121], v[10:17], v[206:213], v[118:121], v189, v189 op_sel_hi:[0,0,0]
	v_mfma_scale_f32_16x16x128_f8f6f4 v[110:113], v[2:9], v[214:221], v[110:113], v189, v189 op_sel_hi:[0,0,0]
	v_mfma_scale_f32_16x16x128_f8f6f4 v[102:105], v[10:17], v[214:221], v[102:105], v189, v189 op_sel_hi:[0,0,0]
	s_setprio 0
	s_setprio 3
	v_mfma_scale_f32_16x16x128_f8f6f4 v[154:157], v[18:25], v[190:197], v[154:157], v189, v189 op_sel_hi:[0,0,0]
	v_mfma_scale_f32_16x16x128_f8f6f4 v[146:149], v[26:33], v[190:197], v[146:149], v189, v189 op_sel_hi:[0,0,0]
	v_mfma_scale_f32_16x16x128_f8f6f4 v[138:141], v[18:25], v[198:205], v[138:141], v189, v189 op_sel_hi:[0,0,0]
	v_mfma_scale_f32_16x16x128_f8f6f4 v[130:133], v[26:33], v[198:205], v[130:133], v189, v189 op_sel_hi:[0,0,0]
	v_mfma_scale_f32_16x16x128_f8f6f4 v[122:125], v[18:25], v[206:213], v[122:125], v189, v189 op_sel_hi:[0,0,0]
	v_mfma_scale_f32_16x16x128_f8f6f4 v[114:117], v[26:33], v[206:213], v[114:117], v189, v189 op_sel_hi:[0,0,0]
	v_mfma_scale_f32_16x16x128_f8f6f4 v[106:109], v[18:25], v[214:221], v[106:109], v189, v189 op_sel_hi:[0,0,0]
	v_mfma_scale_f32_16x16x128_f8f6f4 v[98:101], v[26:33], v[214:221], v[98:101], v189, v189 op_sel_hi:[0,0,0]
	s_setprio 0
	s_barrier
	s_add_i32 s0, s0, s52
	v_lshl_add_u64 v[176:177], v[176:177], 0, s[14:15]
	s_mov_b32 m0, s0
	ds_read_b128 v[190:193], v188 offset:49152
	ds_read_b128 v[194:197], v188 offset:50176
	ds_read_b128 v[198:201], v188 offset:51200
	ds_read_b128 v[202:205], v188 offset:52224
	ds_read_b128 v[206:209], v188 offset:53248
	ds_read_b128 v[210:213], v188 offset:54272
	ds_read_b128 v[214:217], v188 offset:55296
	ds_read_b128 v[218:221], v188 offset:56320
	global_load_lds_dwordx4 v[176:177], off
	s_add_i32 m0, s0, 0x2000
	s_add_u32 s4, s44, 0x20080
	v_lshl_add_u64 v[176:177], v[178:179], 0, s[14:15]
	s_addc_u32 s5, s45, 0
	s_add_i32 s0, s1, s52
	global_load_lds_dwordx4 v[176:177], off
	v_lshl_add_u64 v[176:177], s[4:5], 0, v[168:169]
	s_mov_b32 m0, s0
	s_nop 0
	global_load_lds_dwordx4 v[176:177], off
	v_lshl_add_u64 v[176:177], s[4:5], 0, v[164:165]
	s_add_i32 m0, s0, 0x2000
	s_nop 0
	global_load_lds_dwordx4 v[176:177], off
	v_lshl_add_u64 v[176:177], v[180:181], 0, s[14:15]
	s_mov_b32 m0, s60
	s_nop 0
	global_load_lds_dwordx4 v[176:177], off
	v_lshl_add_u64 v[176:177], v[182:183], 0, s[14:15]
	s_mov_b32 m0, s61
	s_nop 0
	global_load_lds_dwordx4 v[176:177], off
	s_waitcnt vmcnt(8)
	s_waitcnt lgkmcnt(0)
	s_barrier
	s_setprio 3
	s_waitcnt lgkmcnt(0)
	v_mfma_scale_f32_16x16x128_f8f6f4 v[94:97], v[2:9], v[190:197], v[94:97], v189, v189 op_sel_hi:[0,0,0]
	v_mfma_scale_f32_16x16x128_f8f6f4 v[86:89], v[10:17], v[190:197], v[86:89], v189, v189 op_sel_hi:[0,0,0]
	v_mfma_scale_f32_16x16x128_f8f6f4 v[78:81], v[2:9], v[198:205], v[78:81], v189, v189 op_sel_hi:[0,0,0]
	v_mfma_scale_f32_16x16x128_f8f6f4 v[70:73], v[10:17], v[198:205], v[70:73], v189, v189 op_sel_hi:[0,0,0]
	v_mfma_scale_f32_16x16x128_f8f6f4 v[62:65], v[2:9], v[206:213], v[62:65], v189, v189 op_sel_hi:[0,0,0]
	v_mfma_scale_f32_16x16x128_f8f6f4 v[54:57], v[10:17], v[206:213], v[54:57], v189, v189 op_sel_hi:[0,0,0]
	v_mfma_scale_f32_16x16x128_f8f6f4 v[46:49], v[2:9], v[214:221], v[46:49], v189, v189 op_sel_hi:[0,0,0]
	v_mfma_scale_f32_16x16x128_f8f6f4 v[38:41], v[10:17], v[214:221], v[38:41], v189, v189 op_sel_hi:[0,0,0]
	s_setprio 0
	s_setprio 3
	v_mfma_scale_f32_16x16x128_f8f6f4 v[90:93], v[18:25], v[190:197], v[90:93], v189, v189 op_sel_hi:[0,0,0]
	v_mfma_scale_f32_16x16x128_f8f6f4 v[82:85], v[26:33], v[190:197], v[82:85], v189, v189 op_sel_hi:[0,0,0]
	v_mfma_scale_f32_16x16x128_f8f6f4 v[74:77], v[18:25], v[198:205], v[74:77], v189, v189 op_sel_hi:[0,0,0]
	v_mfma_scale_f32_16x16x128_f8f6f4 v[66:69], v[26:33], v[198:205], v[66:69], v189, v189 op_sel_hi:[0,0,0]
	v_mfma_scale_f32_16x16x128_f8f6f4 v[58:61], v[18:25], v[206:213], v[58:61], v189, v189 op_sel_hi:[0,0,0]
	v_mfma_scale_f32_16x16x128_f8f6f4 v[50:53], v[26:33], v[206:213], v[50:53], v189, v189 op_sel_hi:[0,0,0]
	v_mfma_scale_f32_16x16x128_f8f6f4 v[42:45], v[18:25], v[214:221], v[42:45], v189, v189 op_sel_hi:[0,0,0]
	v_mfma_scale_f32_16x16x128_f8f6f4 v[34:37], v[26:33], v[214:221], v[34:37], v189, v189 op_sel_hi:[0,0,0]
	s_setprio 0
	s_add_i32 s81, s81, 2
	s_add_u32 s42, s42, 0x100
	s_addc_u32 s43, s43, 0
	s_add_u32 s79, s79, 0x100
	s_addc_u32 s80, s80, 0
	s_cmp_gt_u32 s81, 5
	s_cbranch_scc0 .LBB0_1310

; __device__ __forceinline__ unsigned pk4_fp8(float a, float b, float c, float d) { int w = 0; w = __builtin_amdgcn_cvt_pk_fp8_f32(a, b, w, false); w = __builtin_amdgcn_cvt_pk_fp8_f32(c, d, w, true); return (unsigned)w; }
; __device__ __forceinline__ f32x2 silu_mul2(f32x2 g, f32x2 u, float c1, float k) {
;     const f32x2 a = g * c1; f32x2 e; e[0] = __builtin_amdgcn_exp2f(a[0]); e[1] = __builtin_amdgcn_exp2f(a[1]);
;     const f32x2 kk = {k, k}; const f32x2 d = __builtin_elementwise_fma(e, kk, kk); f32x2 r; r[0] = __builtin_amdgcn_rcpf(d[0]); r[1] = __builtin_amdgcn_rcpf(d[1]);
;     return (g * u) * r;
; }
;     __device__ __forceinline__ void operator()(const f32x4 (&acc)[2][2][4][2], const Unit& u, int wr, int wc, int fr, int fq) const {
;         const int row0 = u.pm * BM + wr * 64 + fr, col0 = (u.pn % 28) * HALF + wc * 32 + 8 * fq;
; #pragma unroll
;         for (int ai = 0; ai < 2; ++ai)
; #pragma unroll
;             for (int m = 0; m < 4; ++m) { unsigned char* rowp = O + (size_t)(row0 + ai * HALF + m * 16) * ldc + col0;
;                 const float c1 = sc * -1.4426950408889634f, k = 1.0f / (sc * sc);
;                 const f32x4 g0 = acc[ai][0][m][0], g1 = acc[ai][0][m][1], u0 = acc[ai][1][m][0], u1 = acc[ai][1][m][1];
;                 const f32x2 o0 = silu_mul2(g0.xy, u0.xy, c1, k), o1 = silu_mul2(g0.zw, u0.zw, c1, k), o2 = silu_mul2(g1.xy, u1.xy, c1, k), o3 = silu_mul2(g1.zw, u1.zw, c1, k);
;                 u32x2 w; w.x = pk4_fp8(o0[0], o0[1], o1[0], o1[1]); w.y = pk4_fp8(o2[0], o2[1], o3[0], o3[1]);
;                 *(u32x2*)rowp = w; }
.LBB0_1313:
	s_nop 15
	s_nop 15
	v_pk_mul_f32 v[2:3], v[158:159], s[18:19] op_sel_hi:[1,0]
	v_pk_mul_f32 v[12:13], v[158:159], v[154:155]
	v_exp_f32_e32 v4, v2
	v_exp_f32_e32 v5, v3
	v_pk_mul_f32 v[14:15], v[150:151], s[18:19] op_sel_hi:[1,0]
	v_pk_mul_f32 v[16:17], v[152:153], s[18:19] op_sel_hi:[1,0]
	v_exp_f32_e32 v14, v14
	v_pk_fma_f32 v[4:5], v[4:5], s[20:21], s[20:21] op_sel_hi:[1,0,0]
	v_exp_f32_e32 v15, v15
	v_rcp_f32_e32 v8, v4
	v_rcp_f32_e32 v9, v5
	v_exp_f32_e32 v16, v16
	v_pk_fma_f32 v[14:15], v[14:15], s[20:21], s[20:21] op_sel_hi:[1,0,0]
	v_exp_f32_e32 v17, v17
	v_pk_mul_f32 v[8:9], v[8:9], v[12:13]
	v_pk_mul_f32 v[12:13], v[160:161], s[18:19] op_sel_hi:[1,0]
	v_rcp_f32_e32 v14, v14
	v_exp_f32_e32 v12, v12
	v_exp_f32_e32 v13, v13
	v_rcp_f32_e32 v15, v15
	v_pk_mul_f32 v[10:11], v[160:161], v[156:157]
	s_mul_hi_i32 s0, s40, 0x92492493
	v_pk_fma_f32 v[12:13], v[12:13], s[20:21], s[20:21] op_sel_hi:[1,0,0]
	s_add_i32 s0, s0, s40
	v_rcp_f32_e32 v12, v12
	v_rcp_f32_e32 v13, v13
	s_lshr_b32 s1, s0, 31
	s_lshr_b32 s0, s0, 4
	s_add_i32 s0, s0, s1
	v_pk_mul_f32 v[10:11], v[12:13], v[10:11]
	v_pk_mul_f32 v[12:13], v[150:151], v[146:147]
	s_mul_i32 s0, s0, 28
	v_pk_mul_f32 v[12:13], v[14:15], v[12:13]
	v_pk_fma_f32 v[14:15], v[16:17], s[20:21], s[20:21] op_sel_hi:[1,0,0]
	v_mov_b32_e32 v17, 0
	v_rcp_f32_e32 v14, v14
	v_rcp_f32_e32 v15, v15
	v_cvt_pk_fp8_f32 v17, v12, v13
	v_mov_b32_e32 v16, 0
	v_cvt_pk_fp8_f32 v16, v8, v9
	v_pk_mul_f32 v[8:9], v[152:153], v[148:149]
	v_pk_mul_f32 v[12:13], v[142:143], v[138:139]
	v_pk_mul_f32 v[8:9], v[14:15], v[8:9]
	v_pk_mul_f32 v[14:15], v[134:135], s[18:19] op_sel_hi:[1,0]
	v_cvt_pk_fp8_f32 v17, v8, v9 op_sel:[0,0,1]
	v_pk_mul_f32 v[8:9], v[142:143], s[18:19] op_sel_hi:[1,0]
	s_sub_i32 s0, s40, s0
	v_exp_f32_e32 v8, v8
	v_exp_f32_e32 v9, v9
	v_cvt_pk_fp8_f32 v16, v10, v11 op_sel:[0,0,1]
	v_exp_f32_e32 v14, v14
	v_exp_f32_e32 v15, v15
	v_pk_fma_f32 v[8:9], v[8:9], s[20:21], s[20:21] op_sel_hi:[1,0,0]
	v_lshl_add_u32 v6, s38, 8, v1
	v_rcp_f32_e32 v8, v8
	v_rcp_f32_e32 v9, v9
	v_lshl_or_b32 v2, s0, 7, v185
	v_mov_b64_e32 v[4:5], s[12:13]
	v_ashrrev_i32_e32 v3, 31, v2
	v_pk_mul_f32 v[8:9], v[8:9], v[12:13]
	v_pk_mul_f32 v[12:13], v[144:145], s[18:19] op_sel_hi:[1,0]
	v_mad_i64_i32 v[10:11], s[4:5], v6, s76, v[4:5]
	v_exp_f32_e32 v12, v12
	v_exp_f32_e32 v13, v13
	v_lshl_add_u64 v[10:11], v[10:11], 0, v[2:3]
	global_store_dwordx2 v[10:11], v[16:17], off
	v_pk_fma_f32 v[14:15], v[14:15], s[20:21], s[20:21] op_sel_hi:[1,0,0]
	v_pk_fma_f32 v[12:13], v[12:13], s[20:21], s[20:21] op_sel_hi:[1,0,0]
	v_pk_mul_f32 v[16:17], v[136:137], s[18:19] op_sel_hi:[1,0]
	v_rcp_f32_e32 v12, v12
	v_rcp_f32_e32 v13, v13
	v_rcp_f32_e32 v14, v14
	v_rcp_f32_e32 v15, v15
	v_exp_f32_e32 v16, v16
	v_exp_f32_e32 v17, v17
	v_pk_mul_f32 v[10:11], v[144:145], v[140:141]
	v_or_b32_e32 v7, 16, v6
	v_pk_mul_f32 v[10:11], v[12:13], v[10:11]
	v_pk_mul_f32 v[12:13], v[134:135], v[130:131]
	s_andn2_b64 vcc, exec, s[22:23]
	v_pk_mul_f32 v[12:13], v[14:15], v[12:13]
	v_pk_fma_f32 v[14:15], v[16:17], s[20:21], s[20:21] op_sel_hi:[1,0,0]
	v_mov_b32_e32 v17, 0
	v_rcp_f32_e32 v14, v14
	v_rcp_f32_e32 v15, v15
	v_cvt_pk_fp8_f32 v17, v12, v13
	v_mov_b32_e32 v16, 0
	v_cvt_pk_fp8_f32 v16, v8, v9
	v_pk_mul_f32 v[8:9], v[136:137], v[132:133]
	v_pk_mul_f32 v[12:13], v[126:127], v[122:123]
	v_pk_mul_f32 v[8:9], v[14:15], v[8:9]
	v_pk_mul_f32 v[14:15], v[118:119], s[18:19] op_sel_hi:[1,0]
	v_cvt_pk_fp8_f32 v17, v8, v9 op_sel:[0,0,1]
	v_pk_mul_f32 v[8:9], v[126:127], s[18:19] op_sel_hi:[1,0]
	v_cvt_pk_fp8_f32 v16, v10, v11 op_sel:[0,0,1]
	v_exp_f32_e32 v8, v8
	v_exp_f32_e32 v9, v9
	v_exp_f32_e32 v14, v14
	v_exp_f32_e32 v15, v15
	v_mad_i64_i32 v[10:11], s[4:5], v7, s76, v[4:5]
	v_pk_fma_f32 v[8:9], v[8:9], s[20:21], s[20:21] op_sel_hi:[1,0,0]
	v_lshl_add_u64 v[10:11], v[10:11], 0, v[2:3]
	v_rcp_f32_e32 v8, v8
	v_rcp_f32_e32 v9, v9
	global_store_dwordx2 v[10:11], v[16:17], off
	v_pk_fma_f32 v[14:15], v[14:15], s[20:21], s[20:21] op_sel_hi:[1,0,0]
	v_pk_mul_f32 v[16:17], v[120:121], s[18:19] op_sel_hi:[1,0]
	v_pk_mul_f32 v[8:9], v[8:9], v[12:13]
	v_pk_mul_f32 v[12:13], v[128:129], s[18:19] op_sel_hi:[1,0]
	v_rcp_f32_e32 v14, v14
	v_exp_f32_e32 v12, v12
	v_exp_f32_e32 v13, v13
	v_rcp_f32_e32 v15, v15
	v_exp_f32_e32 v16, v16
	v_exp_f32_e32 v17, v17
	v_pk_fma_f32 v[12:13], v[12:13], s[20:21], s[20:21] op_sel_hi:[1,0,0]
	v_pk_mul_f32 v[10:11], v[128:129], v[124:125]
	v_rcp_f32_e32 v12, v12
	v_rcp_f32_e32 v13, v13
	v_or_b32_e32 v7, 32, v6
	s_mov_b64 s[22:23], -1
	v_pk_mul_f32 v[10:11], v[12:13], v[10:11]
	v_pk_mul_f32 v[12:13], v[118:119], v[114:115]
	s_nop 0
	v_pk_mul_f32 v[12:13], v[14:15], v[12:13]
	v_pk_fma_f32 v[14:15], v[16:17], s[20:21], s[20:21] op_sel_hi:[1,0,0]
	v_mov_b32_e32 v17, 0
	v_rcp_f32_e32 v14, v14
	v_rcp_f32_e32 v15, v15
	v_cvt_pk_fp8_f32 v17, v12, v13
	v_mov_b32_e32 v16, 0
	v_cvt_pk_fp8_f32 v16, v8, v9
	v_pk_mul_f32 v[8:9], v[120:121], v[116:117]
	v_pk_mul_f32 v[12:13], v[110:111], v[106:107]
	v_pk_mul_f32 v[8:9], v[14:15], v[8:9]
	v_pk_mul_f32 v[14:15], v[102:103], s[18:19] op_sel_hi:[1,0]
	v_cvt_pk_fp8_f32 v17, v8, v9 op_sel:[0,0,1]
	v_pk_mul_f32 v[8:9], v[110:111], s[18:19] op_sel_hi:[1,0]
	v_cvt_pk_fp8_f32 v16, v10, v11 op_sel:[0,0,1]
	v_exp_f32_e32 v8, v8
	v_exp_f32_e32 v9, v9
	v_exp_f32_e32 v14, v14
	v_exp_f32_e32 v15, v15
	v_mad_i64_i32 v[10:11], s[4:5], v7, s76, v[4:5]
	v_pk_fma_f32 v[8:9], v[8:9], s[20:21], s[20:21] op_sel_hi:[1,0,0]
	v_lshl_add_u64 v[10:11], v[10:11], 0, v[2:3]
	v_rcp_f32_e32 v8, v8
	v_rcp_f32_e32 v9, v9
	global_store_dwordx2 v[10:11], v[16:17], off
	v_pk_fma_f32 v[14:15], v[14:15], s[20:21], s[20:21] op_sel_hi:[1,0,0]
; __device__ __forceinline__ unsigned pk4_fp8(float a, float b, float c, float d) { int w = 0; w = __builtin_amdgcn_cvt_pk_fp8_f32(a, b, w, false); w = __builtin_amdgcn_cvt_pk_fp8_f32(c, d, w, true); return (unsigned)w; }
; __device__ __forceinline__ float silu_mul(float g, float u) { return g * __builtin_amdgcn_rcpf(1.0f + __builtin_amdgcn_exp2f(g * -1.4426950408889634f)) * u; }
; __device__ __forceinline__ f32x2 silu_mul2(f32x2 g, f32x2 u, float c1, float k) {
;     const f32x2 a = g * c1; f32x2 e; e[0] = __builtin_amdgcn_exp2f(a[0]); e[1] = __builtin_amdgcn_exp2f(a[1]);
;     const f32x2 kk = {k, k}; const f32x2 d = __builtin_elementwise_fma(e, kk, kk); f32x2 r; r[0] = __builtin_amdgcn_rcpf(d[0]); r[1] = __builtin_amdgcn_rcpf(d[1]);
;     return (g * u) * r;
; }
;     __device__ __forceinline__ void operator()(const f32x4 (&acc)[2][2][4][2], const Unit& u, int wr, int wc, int fr, int fq) const {
;         const int row0 = u.pm * BM + wr * 64 + fr, col0 = (u.pn % 28) * HALF + wc * 32 + 8 * fq;
; #pragma unroll
;         for (int ai = 0; ai < 2; ++ai)
; #pragma unroll
;             for (int m = 0; m < 4; ++m) { unsigned char* rowp = O + (size_t)(row0 + ai * HALF + m * 16) * ldc + col0;
;                 const float c1 = sc * -1.4426950408889634f, k = 1.0f / (sc * sc);
;                 const f32x4 g0 = acc[ai][0][m][0], g1 = acc[ai][0][m][1], u0 = acc[ai][1][m][0], u1 = acc[ai][1][m][1];
;                 const f32x2 o0 = silu_mul2(g0.xy, u0.xy, c1, k), o1 = silu_mul2(g0.zw, u0.zw, c1, k), o2 = silu_mul2(g1.xy, u1.xy, c1, k), o3 = silu_mul2(g1.zw, u1.zw, c1, k);
;                 u32x2 w; w.x = pk4_fp8(o0[0], o0[1], o1[0], o1[1]); w.y = pk4_fp8(o2[0], o2[1], o3[0], o3[1]);
;                 *(u32x2*)rowp = w; }
	v_pk_mul_f32 v[16:17], v[104:105], s[18:19] op_sel_hi:[1,0]
	v_pk_mul_f32 v[8:9], v[8:9], v[12:13]
	v_pk_mul_f32 v[12:13], v[112:113], s[18:19] op_sel_hi:[1,0]
	v_rcp_f32_e32 v14, v14
	v_exp_f32_e32 v12, v12
	v_exp_f32_e32 v13, v13
	v_rcp_f32_e32 v15, v15
	v_exp_f32_e32 v16, v16
	v_exp_f32_e32 v17, v17
	v_pk_fma_f32 v[12:13], v[12:13], s[20:21], s[20:21] op_sel_hi:[1,0,0]
	v_pk_mul_f32 v[10:11], v[112:113], v[108:109]
	v_rcp_f32_e32 v12, v12
	v_rcp_f32_e32 v13, v13
	v_or_b32_e32 v7, 48, v6
	v_pk_mul_f32 v[10:11], v[12:13], v[10:11]
	v_pk_mul_f32 v[12:13], v[102:103], v[98:99]
	s_nop 0
	v_pk_mul_f32 v[12:13], v[14:15], v[12:13]
	v_pk_fma_f32 v[14:15], v[16:17], s[20:21], s[20:21] op_sel_hi:[1,0,0]
	v_mov_b32_e32 v17, 0
	v_rcp_f32_e32 v14, v14
	v_rcp_f32_e32 v15, v15
	v_cvt_pk_fp8_f32 v17, v12, v13
	v_mov_b32_e32 v16, 0
	v_cvt_pk_fp8_f32 v16, v8, v9
	v_pk_mul_f32 v[8:9], v[104:105], v[100:101]
	v_pk_mul_f32 v[12:13], v[94:95], v[90:91]
	v_pk_mul_f32 v[8:9], v[14:15], v[8:9]
	v_pk_mul_f32 v[14:15], v[86:87], s[18:19] op_sel_hi:[1,0]
	v_cvt_pk_fp8_f32 v17, v8, v9 op_sel:[0,0,1]
	v_pk_mul_f32 v[8:9], v[94:95], s[18:19] op_sel_hi:[1,0]
	v_cvt_pk_fp8_f32 v16, v10, v11 op_sel:[0,0,1]
	v_exp_f32_e32 v8, v8
	v_exp_f32_e32 v9, v9
	v_exp_f32_e32 v14, v14
	v_exp_f32_e32 v15, v15
	v_mad_i64_i32 v[10:11], s[4:5], v7, s76, v[4:5]
	v_pk_fma_f32 v[8:9], v[8:9], s[20:21], s[20:21] op_sel_hi:[1,0,0]
	v_lshl_add_u64 v[10:11], v[10:11], 0, v[2:3]
	v_rcp_f32_e32 v8, v8
	v_rcp_f32_e32 v9, v9
	global_store_dwordx2 v[10:11], v[16:17], off
	v_pk_fma_f32 v[14:15], v[14:15], s[20:21], s[20:21] op_sel_hi:[1,0,0]
	v_pk_mul_f32 v[16:17], v[88:89], s[18:19] op_sel_hi:[1,0]
	v_pk_mul_f32 v[8:9], v[8:9], v[12:13]
	v_pk_mul_f32 v[12:13], v[96:97], s[18:19] op_sel_hi:[1,0]
	v_rcp_f32_e32 v14, v14
	v_exp_f32_e32 v12, v12
	v_exp_f32_e32 v13, v13
	v_rcp_f32_e32 v15, v15
	v_exp_f32_e32 v16, v16
	v_exp_f32_e32 v17, v17
	v_pk_fma_f32 v[12:13], v[12:13], s[20:21], s[20:21] op_sel_hi:[1,0,0]
	v_pk_mul_f32 v[10:11], v[96:97], v[92:93]
	v_rcp_f32_e32 v12, v12
	v_rcp_f32_e32 v13, v13
	v_add_u32_e32 v7, 0x80, v6
	v_pk_mul_f32 v[10:11], v[12:13], v[10:11]
	v_pk_mul_f32 v[12:13], v[86:87], v[82:83]
	s_nop 0
	v_pk_mul_f32 v[12:13], v[14:15], v[12:13]
	v_pk_fma_f32 v[14:15], v[16:17], s[20:21], s[20:21] op_sel_hi:[1,0,0]
	v_mov_b32_e32 v17, 0
	v_rcp_f32_e32 v14, v14
	v_rcp_f32_e32 v15, v15
	v_cvt_pk_fp8_f32 v17, v12, v13
	v_mov_b32_e32 v16, 0
	v_cvt_pk_fp8_f32 v16, v8, v9
	v_pk_mul_f32 v[8:9], v[88:89], v[84:85]
	v_pk_mul_f32 v[12:13], v[78:79], v[74:75]
	v_pk_mul_f32 v[8:9], v[14:15], v[8:9]
	v_pk_mul_f32 v[14:15], v[70:71], s[18:19] op_sel_hi:[1,0]
	v_cvt_pk_fp8_f32 v17, v8, v9 op_sel:[0,0,1]
	v_pk_mul_f32 v[8:9], v[78:79], s[18:19] op_sel_hi:[1,0]
	v_cvt_pk_fp8_f32 v16, v10, v11 op_sel:[0,0,1]
	v_exp_f32_e32 v8, v8
	v_exp_f32_e32 v9, v9
	v_exp_f32_e32 v14, v14
	v_exp_f32_e32 v15, v15
	v_mad_i64_i32 v[10:11], s[4:5], v7, s76, v[4:5]
	v_pk_fma_f32 v[8:9], v[8:9], s[20:21], s[20:21] op_sel_hi:[1,0,0]
	v_lshl_add_u64 v[10:11], v[10:11], 0, v[2:3]
	v_rcp_f32_e32 v8, v8
	v_rcp_f32_e32 v9, v9
	global_store_dwordx2 v[10:11], v[16:17], off
	v_pk_fma_f32 v[14:15], v[14:15], s[20:21], s[20:21] op_sel_hi:[1,0,0]
	v_pk_mul_f32 v[16:17], v[72:73], s[18:19] op_sel_hi:[1,0]
	v_pk_mul_f32 v[8:9], v[8:9], v[12:13]
	v_pk_mul_f32 v[12:13], v[80:81], s[18:19] op_sel_hi:[1,0]
	v_rcp_f32_e32 v14, v14
	v_exp_f32_e32 v12, v12
	v_exp_f32_e32 v13, v13
	v_rcp_f32_e32 v15, v15
	v_exp_f32_e32 v16, v16
	v_exp_f32_e32 v17, v17
	v_pk_fma_f32 v[12:13], v[12:13], s[20:21], s[20:21] op_sel_hi:[1,0,0]
	v_pk_mul_f32 v[10:11], v[80:81], v[76:77]
	v_rcp_f32_e32 v12, v12
	v_rcp_f32_e32 v13, v13
	v_add_u32_e32 v7, 0x90, v6
	v_pk_mul_f32 v[10:11], v[12:13], v[10:11]
	v_pk_mul_f32 v[12:13], v[70:71], v[66:67]
	s_nop 0
	v_pk_mul_f32 v[12:13], v[14:15], v[12:13]
; __device__ __forceinline__ unsigned pk4_fp8(float a, float b, float c, float d) { int w = 0; w = __builtin_amdgcn_cvt_pk_fp8_f32(a, b, w, false); w = __builtin_amdgcn_cvt_pk_fp8_f32(c, d, w, true); return (unsigned)w; }
; #define PG8_BAR __builtin_amdgcn_s_barrier()
;     __device__ __forceinline__ void operator()(const f32x4 (&acc)[2][2][4][2], const Unit& u, int wr, int wc, int fr, int fq) const {
;     ...
;             for (int m = 0; m < 4; ++m) { unsigned char* rowp = O + (size_t)(row0 + ai * HALF + m * 16) * ldc + col0;
;                 const float c1 = sc * -1.4426950408889634f, k = 1.0f / (sc * sc);
;                 const f32x4 g0 = acc[ai][0][m][0], g1 = acc[ai][0][m][1], u0 = acc[ai][1][m][0], u1 = acc[ai][1][m][1];
;                 const f32x2 o0 = silu_mul2(g0.xy, u0.xy, c1, k), o1 = silu_mul2(g0.zw, u0.zw, c1, k), o2 = silu_mul2(g1.xy, u1.xy, c1, k), o3 = silu_mul2(g1.zw, u1.zw, c1, k);
;                 u32x2 w; w.x = pk4_fp8(o0[0], o0[1], o1[0], o1[1]); w.y = pk4_fp8(o2[0], o2[1], o3[0], o3[1]);
;                 *(u32x2*)rowp = w; }
; template <class Epi, class Sched, bool ALIGN_EPI = false, bool SP2 = false, bool F8 = false>
; __device__ __forceinline__ void gemm_phase(PG8_LAS unsigned char* lds, const Gemm g, const Sched& S, const Epi& E) {
;     ...
;         if constexpr (!Epi::AFTER_DRAIN) { E(acc, cur, wr, wc, fr, fq); S.done(cur); }
;         if (!has_next) break;
; #pragma unroll
;         for (int a = 0; a < 2; ++a)
; #pragma unroll
;             for (int b = 0; b < 2; ++b)
; #pragma unroll
;                 for (int m = 0; m < 4; ++m)
; #pragma unroll
;                     for (int n = 0; n < 2; ++n) acc[a][b][m][n] = (f32x4){0.f, 0.f, 0.f, 0.f};
;         cur = nxt; cA = nA; cB = nB; ++ui;
;         if constexpr (ALIGN_EPI) { if (wr == 1) PG8_BAR; }
	v_pk_fma_f32 v[14:15], v[16:17], s[20:21], s[20:21] op_sel_hi:[1,0,0]
	v_mov_b32_e32 v17, 0
	v_rcp_f32_e32 v14, v14
	v_rcp_f32_e32 v15, v15
	v_cvt_pk_fp8_f32 v17, v12, v13
	v_mov_b32_e32 v16, 0
	v_cvt_pk_fp8_f32 v16, v8, v9
	v_pk_mul_f32 v[8:9], v[72:73], v[68:69]
	v_pk_mul_f32 v[12:13], v[62:63], v[58:59]
	v_pk_mul_f32 v[8:9], v[14:15], v[8:9]
	v_pk_mul_f32 v[14:15], v[54:55], s[18:19] op_sel_hi:[1,0]
	v_cvt_pk_fp8_f32 v17, v8, v9 op_sel:[0,0,1]
	v_pk_mul_f32 v[8:9], v[62:63], s[18:19] op_sel_hi:[1,0]
	v_cvt_pk_fp8_f32 v16, v10, v11 op_sel:[0,0,1]
	v_exp_f32_e32 v8, v8
	v_exp_f32_e32 v9, v9
	v_exp_f32_e32 v14, v14
	v_exp_f32_e32 v15, v15
	v_mad_i64_i32 v[10:11], s[4:5], v7, s76, v[4:5]
	v_pk_fma_f32 v[8:9], v[8:9], s[20:21], s[20:21] op_sel_hi:[1,0,0]
	v_lshl_add_u64 v[10:11], v[10:11], 0, v[2:3]
	v_rcp_f32_e32 v8, v8
	v_rcp_f32_e32 v9, v9
	global_store_dwordx2 v[10:11], v[16:17], off
	v_pk_fma_f32 v[14:15], v[14:15], s[20:21], s[20:21] op_sel_hi:[1,0,0]
	v_pk_mul_f32 v[16:17], v[56:57], s[18:19] op_sel_hi:[1,0]
	v_pk_mul_f32 v[8:9], v[8:9], v[12:13]
	v_pk_mul_f32 v[12:13], v[64:65], s[18:19] op_sel_hi:[1,0]
	v_rcp_f32_e32 v14, v14
	v_exp_f32_e32 v12, v12
	v_exp_f32_e32 v13, v13
	v_rcp_f32_e32 v15, v15
	v_exp_f32_e32 v16, v16
	v_exp_f32_e32 v17, v17
	v_pk_fma_f32 v[12:13], v[12:13], s[20:21], s[20:21] op_sel_hi:[1,0,0]
	v_pk_mul_f32 v[10:11], v[64:65], v[60:61]
	v_rcp_f32_e32 v12, v12
	v_rcp_f32_e32 v13, v13
	v_add_u32_e32 v7, 0xa0, v6
	v_pk_mul_f32 v[10:11], v[12:13], v[10:11]
	v_pk_mul_f32 v[12:13], v[54:55], v[50:51]
	s_nop 0
	v_pk_mul_f32 v[12:13], v[14:15], v[12:13]
	v_pk_fma_f32 v[14:15], v[16:17], s[20:21], s[20:21] op_sel_hi:[1,0,0]
	v_mov_b32_e32 v17, 0
	v_rcp_f32_e32 v14, v14
	v_rcp_f32_e32 v15, v15
	v_cvt_pk_fp8_f32 v17, v12, v13
	v_mov_b32_e32 v16, 0
	v_cvt_pk_fp8_f32 v16, v8, v9
	v_pk_mul_f32 v[8:9], v[56:57], v[52:53]
	v_pk_mul_f32 v[12:13], v[38:39], s[18:19] op_sel_hi:[1,0]
	v_pk_mul_f32 v[8:9], v[14:15], v[8:9]
	v_cvt_pk_fp8_f32 v16, v10, v11 op_sel:[0,0,1]
	v_cvt_pk_fp8_f32 v17, v8, v9 op_sel:[0,0,1]
	v_pk_mul_f32 v[8:9], v[46:47], s[18:19] op_sel_hi:[1,0]
	v_mad_i64_i32 v[10:11], s[4:5], v7, s76, v[4:5]
	v_exp_f32_e32 v8, v8
	v_exp_f32_e32 v9, v9
	v_lshl_add_u64 v[10:11], v[10:11], 0, v[2:3]
	global_store_dwordx2 v[10:11], v[16:17], off
	v_pk_mul_f32 v[10:11], v[46:47], v[42:43]
	v_pk_fma_f32 v[8:9], v[8:9], s[20:21], s[20:21] op_sel_hi:[1,0,0]
	v_exp_f32_e32 v12, v12
	v_rcp_f32_e32 v8, v8
	v_rcp_f32_e32 v9, v9
	v_exp_f32_e32 v13, v13
	v_pk_mul_f32 v[14:15], v[40:41], s[18:19] op_sel_hi:[1,0]
	v_add_u32_e32 v16, 0xb0, v6
	v_pk_mul_f32 v[8:9], v[8:9], v[10:11]
	v_pk_mul_f32 v[10:11], v[48:49], s[18:19] op_sel_hi:[1,0]
	v_pk_fma_f32 v[12:13], v[12:13], s[20:21], s[20:21] op_sel_hi:[1,0,0]
	v_exp_f32_e32 v10, v10
	v_exp_f32_e32 v11, v11
	v_rcp_f32_e32 v12, v12
	v_rcp_f32_e32 v13, v13
	v_exp_f32_e32 v14, v14
	v_pk_fma_f32 v[10:11], v[10:11], s[20:21], s[20:21] op_sel_hi:[1,0,0]
	v_exp_f32_e32 v15, v15
	v_rcp_f32_e32 v10, v10
	v_rcp_f32_e32 v11, v11
	v_pk_mul_f32 v[6:7], v[48:49], v[44:45]
	v_mad_i64_i32 v[4:5], s[4:5], v16, s76, v[4:5]
	v_pk_mul_f32 v[6:7], v[10:11], v[6:7]
	v_pk_mul_f32 v[10:11], v[38:39], v[34:35]
	v_lshl_add_u64 v[2:3], v[4:5], 0, v[2:3]
	v_pk_mul_f32 v[10:11], v[12:13], v[10:11]
	v_pk_fma_f32 v[12:13], v[14:15], s[20:21], s[20:21] op_sel_hi:[1,0,0]
	v_mov_b32_e32 v14, 0
	v_rcp_f32_e32 v12, v12
	v_rcp_f32_e32 v13, v13
	v_mov_b32_e32 v15, 0
	v_cvt_pk_fp8_f32 v14, v8, v9
	v_cvt_pk_fp8_f32 v15, v10, v11
	v_pk_mul_f32 v[8:9], v[40:41], v[36:37]
	v_cvt_pk_fp8_f32 v14, v6, v7 op_sel:[0,0,1]
	v_pk_mul_f32 v[8:9], v[12:13], v[8:9]
	s_nop 0
	v_cvt_pk_fp8_f32 v15, v8, v9 op_sel:[0,0,1]
	global_store_dwordx2 v[2:3], v[14:15], off
	s_barrier
	s_cbranch_vccnz .LBB0_1306
	s_andn2_b64 vcc, exec, s[10:11]
	s_cbranch_vccnz .LBB0_1305
	s_barrier
	s_branch .LBB0_1305

; #define PG8_STAGE(bufoff, gbase, voff) do { _Pragma("unroll") for (int _i = 0; _i < 2; ++_i) \
;         __builtin_amdgcn_global_load_lds((const unsigned*)((const char*)(gbase) + (voff)[_i]), (PG8_LAS unsigned*)(lds + (bufoff) + ldsw + _i * 8192), 16, 0, 0); } while (0)
; #define PG8_LDA(dst, b, h) do { _Pragma("unroll") for (int m = 0; m < 4; ++m) Frag<F8>::load(dst[m], lds + PG8_SA(b, h) + aoff + m * 2048); } while (0)
; #define PG8_LDB(dst, b, h) do { _Pragma("unroll") for (int n = 0; n < 2; ++n) Frag<F8>::load(dst[n], lds + PG8_SB(b, h) + boff + n * 2048); } while (0)
; #define PG8_MMA(ai, bj, At, Bt) do { __builtin_amdgcn_s_setprio(3); _Pragma("unroll") for (int m = 0; m < 4; ++m) _Pragma("unroll") for (int n = 0; n < 2; ++n) Frag<F8>::mma(acc[ai][bj][m][n], Bt[n], At[m]); \
;         __builtin_amdgcn_s_setprio(0); } while (0)
; #define PG8_WAIT_V(n) asm volatile("s_waitcnt vmcnt(" #n ")" ::: "memory")
; #define PG8_WAIT_L(n) asm volatile("s_waitcnt lgkmcnt(" #n ")" ::: "memory")
; #define PG8_BAR __builtin_amdgcn_s_barrier()
; #define PG8_SCHED __builtin_amdgcn_sched_barrier(0)
; template <class Epi, class Sched, bool ALIGN_EPI = false, bool SP2 = false, bool F8 = false>
; __device__ __forceinline__ void gemm_phase(PG8_LAS unsigned char* lds, const Gemm g, const Sched& S, const Epi& E) {
;     ...
;             const bool last = (t == nt - 2);
;             const char* a1 = cA + (size_t)(t + 1) * kstep;
;             const char* a2 = last ? nA : cA + (size_t)(t + 2) * kstep; const char* b2 = last ? nB : cB + (size_t)(t + 2) * kstep;
;             const char* a3 = a2 + kstep; const char* b3 = b2 + kstep;
;             if (last && has_next) S.a_ready(nxt);
;             if constexpr (SP2) {
;             PG8_LDB(B0, 0, 0); PG8_LDB(B1, 0, 1); PG8_SCHED; PG8_LDA(At, 0, 0); PG8_STAGE(PG8_SA(1, 1), a1 + hstep, voffA);
;             PG8_WAIT_V(8); PG8_WAIT_L(0); PG8_BAR; PG8_MMA(0, 0, At, B0); PG8_MMA(0, 1, At, B1); PG8_BAR; PG8_SCHED;
;             PG8_LDA(At, 0, 1); PG8_STAGE(PG8_SB(0, 0), b2, voffB); PG8_STAGE(PG8_SB(0, 1), b2 + hstep, voffB); PG8_STAGE(PG8_SA(0, 0), a2, voffA);
;             PG8_WAIT_V(8); PG8_WAIT_L(0); PG8_BAR; PG8_MMA(1, 0, At, B0); PG8_MMA(1, 1, At, B1); PG8_BAR; PG8_SCHED;
.LBB0_1391:
	v_lshl_add_u64 v[180:181], v[2:3], 0, s[24:25]
	s_mov_b32 s76, -2
	ds_read_b128 v[18:21], v192
	ds_read_b128 v[22:25], v192 offset:1024
	ds_read_b128 v[26:29], v192 offset:2048
	ds_read_b128 v[30:33], v192 offset:3072
	ds_read_b128 v[2:5], v193
	ds_read_b128 v[6:9], v193 offset:1024
	ds_read_b128 v[10:13], v193 offset:2048
	ds_read_b128 v[14:17], v193 offset:3072
	s_add_u32 s30, s36, 0x100
	s_addc_u32 s31, s37, 0
	s_cmp_eq_u32 s76, 24
	s_cselect_b64 vcc, -1, 0
	s_cselect_b32 s39, s27, s31
	s_cselect_b32 s38, s26, s30
	v_cndmask_b32_e32 v183, v181, v179, vcc
	v_cndmask_b32_e32 v182, v180, v178, vcc
	s_mov_b32 m0, s56
	v_lshl_add_u64 v[224:225], s[36:37], 0, v[174:175]
	ds_read_b128 v[184:187], v194
	ds_read_b128 v[188:191], v194 offset:1024
	ds_read_b128 v[200:203], v194 offset:2048
	ds_read_b128 v[204:207], v194 offset:3072
	ds_read_b128 v[208:211], v194 offset:4096
	ds_read_b128 v[212:215], v194 offset:5120
	ds_read_b128 v[216:219], v194 offset:6144
	ds_read_b128 v[220:223], v194 offset:7168
	global_load_lds_dwordx4 v[224:225], off
	v_lshl_add_u64 v[224:225], s[36:37], 0, v[176:177]
	s_mov_b32 m0, s57
	s_nop 0
	global_load_lds_dwordx4 v[224:225], off
	s_waitcnt vmcnt(8)
	s_waitcnt lgkmcnt(0)
	s_barrier
	s_setprio 3
	s_waitcnt lgkmcnt(0)
	v_mfma_scale_f32_16x16x128_f8f6f4 v[158:161], v[18:25], v[184:191], 0, v195, v195 op_sel_hi:[0, 0, 0]
	v_mfma_scale_f32_16x16x128_f8f6f4 v[154:157], v[26:33], v[184:191], 0, v195, v195 op_sel_hi:[0, 0, 0]
	v_mfma_scale_f32_16x16x128_f8f6f4 v[142:145], v[18:25], v[200:207], 0, v195, v195 op_sel_hi:[0, 0, 0]
	v_mfma_scale_f32_16x16x128_f8f6f4 v[138:141], v[26:33], v[200:207], 0, v195, v195 op_sel_hi:[0, 0, 0]
	v_mfma_scale_f32_16x16x128_f8f6f4 v[126:129], v[18:25], v[208:215], 0, v195, v195 op_sel_hi:[0, 0, 0]
	v_mfma_scale_f32_16x16x128_f8f6f4 v[122:125], v[26:33], v[208:215], 0, v195, v195 op_sel_hi:[0, 0, 0]
	v_mfma_scale_f32_16x16x128_f8f6f4 v[110:113], v[18:25], v[216:223], 0, v195, v195 op_sel_hi:[0, 0, 0]
	v_mfma_scale_f32_16x16x128_f8f6f4 v[106:109], v[26:33], v[216:223], 0, v195, v195 op_sel_hi:[0, 0, 0]
	s_setprio 0
	s_setprio 3
	v_mfma_scale_f32_16x16x128_f8f6f4 v[150:153], v[2:9], v[184:191], 0, v195, v195 op_sel_hi:[0, 0, 0]
	v_mfma_scale_f32_16x16x128_f8f6f4 v[146:149], v[10:17], v[184:191], 0, v195, v195 op_sel_hi:[0, 0, 0]
	v_mfma_scale_f32_16x16x128_f8f6f4 v[134:137], v[2:9], v[200:207], 0, v195, v195 op_sel_hi:[0, 0, 0]
	v_mfma_scale_f32_16x16x128_f8f6f4 v[130:133], v[10:17], v[200:207], 0, v195, v195 op_sel_hi:[0, 0, 0]
	v_mfma_scale_f32_16x16x128_f8f6f4 v[118:121], v[2:9], v[208:215], 0, v195, v195 op_sel_hi:[0, 0, 0]
	v_mfma_scale_f32_16x16x128_f8f6f4 v[114:117], v[10:17], v[208:215], 0, v195, v195 op_sel_hi:[0, 0, 0]
	v_mfma_scale_f32_16x16x128_f8f6f4 v[102:105], v[2:9], v[216:223], 0, v195, v195 op_sel_hi:[0, 0, 0]
	v_mfma_scale_f32_16x16x128_f8f6f4 v[98:101], v[10:17], v[216:223], 0, v195, v195 op_sel_hi:[0, 0, 0]
	s_setprio 0
	s_barrier
	s_mov_b32 m0, s58
	v_lshl_add_u64 v[184:185], v[182:183], 0, v[166:167]
	ds_read_b128 v[200:203], v194 offset:16384
	ds_read_b128 v[204:207], v194 offset:17408
	ds_read_b128 v[208:211], v194 offset:18432
	ds_read_b128 v[212:215], v194 offset:19456
	ds_read_b128 v[216:219], v194 offset:20480
	ds_read_b128 v[220:223], v194 offset:21504
	ds_read_b128 v[224:227], v194 offset:22528
	ds_read_b128 v[228:231], v194 offset:23552
	global_load_lds_dwordx4 v[184:185], off
	v_lshl_add_u64 v[186:187], v[182:183], 0, v[170:171]
	s_mov_b32 m0, s59
	v_lshl_add_u64 v[188:189], v[182:183], 0, s[10:11]
	global_load_lds_dwordx4 v[186:187], off
	v_lshl_add_u64 v[190:191], v[188:189], 0, v[166:167]
	s_mov_b32 m0, s60
	v_lshl_add_u64 v[188:189], v[188:189], 0, v[170:171]
	global_load_lds_dwordx4 v[190:191], off
	s_mov_b32 m0, s61
	v_lshl_add_u64 v[190:191], s[38:39], 0, v[168:169]
	global_load_lds_dwordx4 v[188:189], off
	v_lshl_add_u64 v[188:189], s[38:39], 0, v[164:165]
	s_mov_b32 m0, s45
	s_nop 0
	global_load_lds_dwordx4 v[188:189], off
	s_mov_b32 m0, s46
	s_nop 0
	global_load_lds_dwordx4 v[190:191], off
	s_waitcnt vmcnt(8)
	s_waitcnt lgkmcnt(0)
	s_barrier
	s_setprio 3
	s_waitcnt lgkmcnt(0)
	v_mfma_scale_f32_16x16x128_f8f6f4 v[94:97], v[18:25], v[200:207], 0, v195, v195 op_sel_hi:[0, 0, 0]
	v_mfma_scale_f32_16x16x128_f8f6f4 v[90:93], v[26:33], v[200:207], 0, v195, v195 op_sel_hi:[0, 0, 0]
	v_mfma_scale_f32_16x16x128_f8f6f4 v[78:81], v[18:25], v[208:215], 0, v195, v195 op_sel_hi:[0, 0, 0]
	v_mfma_scale_f32_16x16x128_f8f6f4 v[74:77], v[26:33], v[208:215], 0, v195, v195 op_sel_hi:[0, 0, 0]
	v_mfma_scale_f32_16x16x128_f8f6f4 v[62:65], v[18:25], v[216:223], 0, v195, v195 op_sel_hi:[0, 0, 0]
	v_mfma_scale_f32_16x16x128_f8f6f4 v[58:61], v[26:33], v[216:223], 0, v195, v195 op_sel_hi:[0, 0, 0]
	v_mfma_scale_f32_16x16x128_f8f6f4 v[46:49], v[18:25], v[224:231], 0, v195, v195 op_sel_hi:[0, 0, 0]
	v_mfma_scale_f32_16x16x128_f8f6f4 v[42:45], v[26:33], v[224:231], 0, v195, v195 op_sel_hi:[0, 0, 0]
	s_setprio 0
	s_setprio 3
	v_mfma_scale_f32_16x16x128_f8f6f4 v[86:89], v[2:9], v[200:207], 0, v195, v195 op_sel_hi:[0, 0, 0]
	v_mfma_scale_f32_16x16x128_f8f6f4 v[82:85], v[10:17], v[200:207], 0, v195, v195 op_sel_hi:[0, 0, 0]
	v_mfma_scale_f32_16x16x128_f8f6f4 v[70:73], v[2:9], v[208:215], 0, v195, v195 op_sel_hi:[0, 0, 0]
	v_mfma_scale_f32_16x16x128_f8f6f4 v[66:69], v[10:17], v[208:215], 0, v195, v195 op_sel_hi:[0, 0, 0]
	v_mfma_scale_f32_16x16x128_f8f6f4 v[54:57], v[2:9], v[216:223], 0, v195, v195 op_sel_hi:[0, 0, 0]
	v_mfma_scale_f32_16x16x128_f8f6f4 v[50:53], v[10:17], v[216:223], 0, v195, v195 op_sel_hi:[0, 0, 0]
	v_mfma_scale_f32_16x16x128_f8f6f4 v[38:41], v[2:9], v[224:231], 0, v195, v195 op_sel_hi:[0, 0, 0]
	v_mfma_scale_f32_16x16x128_f8f6f4 v[34:37], v[10:17], v[224:231], 0, v195, v195 op_sel_hi:[0, 0, 0]
	s_setprio 0
	s_barrier
; #define PG8_STAGE(bufoff, gbase, voff) do { _Pragma("unroll") for (int _i = 0; _i < 2; ++_i) \
;         __builtin_amdgcn_global_load_lds((const unsigned*)((const char*)(gbase) + (voff)[_i]), (PG8_LAS unsigned*)(lds + (bufoff) + ldsw + _i * 8192), 16, 0, 0); } while (0)
; #define PG8_LDA(dst, b, h) do { _Pragma("unroll") for (int m = 0; m < 4; ++m) Frag<F8>::load(dst[m], lds + PG8_SA(b, h) + aoff + m * 2048); } while (0)
; #define PG8_LDB(dst, b, h) do { _Pragma("unroll") for (int n = 0; n < 2; ++n) Frag<F8>::load(dst[n], lds + PG8_SB(b, h) + boff + n * 2048); } while (0)
; #define PG8_MMA(ai, bj, At, Bt) do { __builtin_amdgcn_s_setprio(3); _Pragma("unroll") for (int m = 0; m < 4; ++m) _Pragma("unroll") for (int n = 0; n < 2; ++n) Frag<F8>::mma(acc[ai][bj][m][n], Bt[n], At[m]); \
;         __builtin_amdgcn_s_setprio(0); } while (0)
; #define PG8_WAIT_V(n) asm volatile("s_waitcnt vmcnt(" #n ")" ::: "memory")
; #define PG8_WAIT_L(n) asm volatile("s_waitcnt lgkmcnt(" #n ")" ::: "memory")
; #define PG8_BAR __builtin_amdgcn_s_barrier()
; #define PG8_SCHED __builtin_amdgcn_sched_barrier(0)
; template <class Epi, class Sched, bool ALIGN_EPI = false, bool SP2 = false, bool F8 = false>
; __device__ __forceinline__ void gemm_phase(PG8_LAS unsigned char* lds, const Gemm g, const Sched& S, const Epi& E) {
;     ...
;             PG8_LDB(B0, 1, 0); PG8_LDB(B1, 1, 1); PG8_SCHED; PG8_LDA(At, 1, 0); PG8_STAGE(PG8_SA(0, 1), a2 + hstep, voffA);
;             PG8_WAIT_V(8); PG8_WAIT_L(0); PG8_BAR; PG8_MMA(0, 0, At, B0); PG8_MMA(0, 1, At, B1); PG8_BAR; PG8_SCHED;
;             PG8_LDA(At, 1, 1); PG8_STAGE(PG8_SB(1, 0), b3, voffB); PG8_STAGE(PG8_SB(1, 1), b3 + hstep, voffB); PG8_STAGE(PG8_SA(1, 0), a3, voffA);
;             PG8_WAIT_V(8); PG8_WAIT_L(0); PG8_BAR; PG8_MMA(1, 0, At, B0); PG8_MMA(1, 1, At, B1); PG8_BAR; PG8_SCHED;
	ds_read_b128 v[2:5], v196
	ds_read_b128 v[6:9], v196 offset:1024
	ds_read_b128 v[10:13], v196 offset:2048
	ds_read_b128 v[14:17], v196 offset:3072
	ds_read_b128 v[18:21], v197
	ds_read_b128 v[22:25], v197 offset:1024
	ds_read_b128 v[26:29], v197 offset:2048
	ds_read_b128 v[30:33], v197 offset:3072
	s_add_u32 s4, s38, 0x70000
	s_addc_u32 s5, s39, 0
	s_mov_b32 m0, s47
	v_lshl_add_u64 v[232:233], s[4:5], 0, v[164:165]
	ds_read_b128 v[200:203], v194 offset:32768
	ds_read_b128 v[204:207], v194 offset:33792
	ds_read_b128 v[208:211], v194 offset:34816
	ds_read_b128 v[212:215], v194 offset:35840
	ds_read_b128 v[216:219], v194 offset:36864
	ds_read_b128 v[220:223], v194 offset:37888
	ds_read_b128 v[224:227], v194 offset:38912
	ds_read_b128 v[228:231], v194 offset:39936
	global_load_lds_dwordx4 v[232:233], off
	v_lshl_add_u64 v[232:233], s[4:5], 0, v[168:169]
	s_mov_b32 m0, s48
	s_nop 0
	global_load_lds_dwordx4 v[232:233], off
	s_waitcnt vmcnt(8)
	s_waitcnt lgkmcnt(0)
	s_barrier
	s_setprio 3
	s_waitcnt lgkmcnt(0)
	v_mfma_scale_f32_16x16x128_f8f6f4 v[158:161], v[2:9], v[200:207], v[158:161], v195, v195 op_sel_hi:[0,0,0]
	v_mfma_scale_f32_16x16x128_f8f6f4 v[154:157], v[10:17], v[200:207], v[154:157], v195, v195 op_sel_hi:[0,0,0]
	v_mfma_scale_f32_16x16x128_f8f6f4 v[142:145], v[2:9], v[208:215], v[142:145], v195, v195 op_sel_hi:[0,0,0]
	v_mfma_scale_f32_16x16x128_f8f6f4 v[138:141], v[10:17], v[208:215], v[138:141], v195, v195 op_sel_hi:[0,0,0]
	v_mfma_scale_f32_16x16x128_f8f6f4 v[126:129], v[2:9], v[216:223], v[126:129], v195, v195 op_sel_hi:[0,0,0]
	v_mfma_scale_f32_16x16x128_f8f6f4 v[122:125], v[10:17], v[216:223], v[122:125], v195, v195 op_sel_hi:[0,0,0]
	v_mfma_scale_f32_16x16x128_f8f6f4 v[110:113], v[2:9], v[224:231], v[110:113], v195, v195 op_sel_hi:[0,0,0]
	v_mfma_scale_f32_16x16x128_f8f6f4 v[106:109], v[10:17], v[224:231], v[106:109], v195, v195 op_sel_hi:[0,0,0]
	s_setprio 0
	s_setprio 3
	v_mfma_scale_f32_16x16x128_f8f6f4 v[150:153], v[18:25], v[200:207], v[150:153], v195, v195 op_sel_hi:[0,0,0]
	v_mfma_scale_f32_16x16x128_f8f6f4 v[146:149], v[26:33], v[200:207], v[146:149], v195, v195 op_sel_hi:[0,0,0]
	v_mfma_scale_f32_16x16x128_f8f6f4 v[134:137], v[18:25], v[208:215], v[134:137], v195, v195 op_sel_hi:[0,0,0]
	v_mfma_scale_f32_16x16x128_f8f6f4 v[130:133], v[26:33], v[208:215], v[130:133], v195, v195 op_sel_hi:[0,0,0]
	v_mfma_scale_f32_16x16x128_f8f6f4 v[118:121], v[18:25], v[216:223], v[118:121], v195, v195 op_sel_hi:[0,0,0]
	v_mfma_scale_f32_16x16x128_f8f6f4 v[114:117], v[26:33], v[216:223], v[114:117], v195, v195 op_sel_hi:[0,0,0]
	v_mfma_scale_f32_16x16x128_f8f6f4 v[102:105], v[18:25], v[224:231], v[102:105], v195, v195 op_sel_hi:[0,0,0]
	v_mfma_scale_f32_16x16x128_f8f6f4 v[98:101], v[26:33], v[224:231], v[98:101], v195, v195 op_sel_hi:[0,0,0]
	s_setprio 0
	s_barrier
	s_mov_b32 m0, s67
	v_lshl_add_u64 v[184:185], v[184:185], 0, s[18:19]
	ds_read_b128 v[200:203], v194 offset:49152
	ds_read_b128 v[204:207], v194 offset:50176
	ds_read_b128 v[208:211], v194 offset:51200
	ds_read_b128 v[212:215], v194 offset:52224
	ds_read_b128 v[216:219], v194 offset:53248
	ds_read_b128 v[220:223], v194 offset:54272
	ds_read_b128 v[224:227], v194 offset:55296
	ds_read_b128 v[228:231], v194 offset:56320
	global_load_lds_dwordx4 v[184:185], off
	v_lshl_add_u64 v[184:185], v[186:187], 0, s[18:19]
	s_mov_b32 m0, s70
	v_lshl_add_u64 v[182:183], v[182:183], 0, s[20:21]
	global_load_lds_dwordx4 v[184:185], off
	v_lshl_add_u64 v[184:185], v[182:183], 0, v[166:167]
	s_mov_b32 m0, s71
	v_lshl_add_u64 v[182:183], v[182:183], 0, v[170:171]
	global_load_lds_dwordx4 v[184:185], off
	s_mov_b32 m0, s72
	s_nop 0
	global_load_lds_dwordx4 v[182:183], off
	v_lshl_add_u64 v[182:183], v[188:189], 0, s[18:19]
	s_mov_b32 m0, s49
	s_nop 0
	global_load_lds_dwordx4 v[182:183], off
	v_lshl_add_u64 v[182:183], v[190:191], 0, s[18:19]
	s_mov_b32 m0, s50
	s_nop 0
	global_load_lds_dwordx4 v[182:183], off
	s_waitcnt vmcnt(8)
	s_waitcnt lgkmcnt(0)
	s_barrier
	s_setprio 3
	s_waitcnt lgkmcnt(0)
	v_mfma_scale_f32_16x16x128_f8f6f4 v[94:97], v[2:9], v[200:207], v[94:97], v195, v195 op_sel_hi:[0,0,0]
	v_mfma_scale_f32_16x16x128_f8f6f4 v[90:93], v[10:17], v[200:207], v[90:93], v195, v195 op_sel_hi:[0,0,0]
	v_mfma_scale_f32_16x16x128_f8f6f4 v[78:81], v[2:9], v[208:215], v[78:81], v195, v195 op_sel_hi:[0,0,0]
	v_mfma_scale_f32_16x16x128_f8f6f4 v[74:77], v[10:17], v[208:215], v[74:77], v195, v195 op_sel_hi:[0,0,0]
	v_mfma_scale_f32_16x16x128_f8f6f4 v[62:65], v[2:9], v[216:223], v[62:65], v195, v195 op_sel_hi:[0,0,0]
	v_mfma_scale_f32_16x16x128_f8f6f4 v[58:61], v[10:17], v[216:223], v[58:61], v195, v195 op_sel_hi:[0,0,0]
	v_mfma_scale_f32_16x16x128_f8f6f4 v[46:49], v[2:9], v[224:231], v[46:49], v195, v195 op_sel_hi:[0,0,0]
	v_mfma_scale_f32_16x16x128_f8f6f4 v[42:45], v[10:17], v[224:231], v[42:45], v195, v195 op_sel_hi:[0,0,0]
	s_setprio 0
	s_setprio 3
	v_mfma_scale_f32_16x16x128_f8f6f4 v[86:89], v[18:25], v[200:207], v[86:89], v195, v195 op_sel_hi:[0,0,0]
	v_mfma_scale_f32_16x16x128_f8f6f4 v[82:85], v[26:33], v[200:207], v[82:85], v195, v195 op_sel_hi:[0,0,0]
	v_mfma_scale_f32_16x16x128_f8f6f4 v[70:73], v[18:25], v[208:215], v[70:73], v195, v195 op_sel_hi:[0,0,0]
	v_mfma_scale_f32_16x16x128_f8f6f4 v[66:69], v[26:33], v[208:215], v[66:69], v195, v195 op_sel_hi:[0,0,0]
	v_mfma_scale_f32_16x16x128_f8f6f4 v[54:57], v[18:25], v[216:223], v[54:57], v195, v195 op_sel_hi:[0,0,0]
	v_mfma_scale_f32_16x16x128_f8f6f4 v[50:53], v[26:33], v[216:223], v[50:53], v195, v195 op_sel_hi:[0,0,0]
	v_mfma_scale_f32_16x16x128_f8f6f4 v[38:41], v[18:25], v[224:231], v[38:41], v195, v195 op_sel_hi:[0,0,0]
	v_mfma_scale_f32_16x16x128_f8f6f4 v[34:37], v[26:33], v[224:231], v[34:37], v195, v195 op_sel_hi:[0,0,0]
	s_setprio 0
	s_add_i32 s76, s76, 2
	v_lshl_add_u64 v[180:181], v[180:181], 0, s[24:25]
	s_cmp_gt_u32 s76, 25
	s_mov_b64 s[36:37], s[30:31]
	s_cbranch_scc1 .Lpeel_exit_4
; #define PG8_STAGE(bufoff, gbase, voff) do { _Pragma("unroll") for (int _i = 0; _i < 2; ++_i) \
;         __builtin_amdgcn_global_load_lds((const unsigned*)((const char*)(gbase) + (voff)[_i]), (PG8_LAS unsigned*)(lds + (bufoff) + ldsw + _i * 8192), 16, 0, 0); } while (0)
; #define PG8_LDA(dst, b, h) do { _Pragma("unroll") for (int m = 0; m < 4; ++m) Frag<F8>::load(dst[m], lds + PG8_SA(b, h) + aoff + m * 2048); } while (0)
; #define PG8_LDB(dst, b, h) do { _Pragma("unroll") for (int n = 0; n < 2; ++n) Frag<F8>::load(dst[n], lds + PG8_SB(b, h) + boff + n * 2048); } while (0)
; #define PG8_MMA(ai, bj, At, Bt) do { __builtin_amdgcn_s_setprio(3); _Pragma("unroll") for (int m = 0; m < 4; ++m) _Pragma("unroll") for (int n = 0; n < 2; ++n) Frag<F8>::mma(acc[ai][bj][m][n], Bt[n], At[m]); \
;         __builtin_amdgcn_s_setprio(0); } while (0)
; #define PG8_WAIT_V(n) asm volatile("s_waitcnt vmcnt(" #n ")" ::: "memory")
; #define PG8_WAIT_L(n) asm volatile("s_waitcnt lgkmcnt(" #n ")" ::: "memory")
; #define PG8_BAR __builtin_amdgcn_s_barrier()
; #define PG8_SCHED __builtin_amdgcn_sched_barrier(0)
; template <class Epi, class Sched, bool ALIGN_EPI = false, bool SP2 = false, bool F8 = false>
; __device__ __forceinline__ void gemm_phase(PG8_LAS unsigned char* lds, const Gemm g, const Sched& S, const Epi& E) {
;     ...
;             const bool last = (t == nt - 2);
;             const char* a1 = cA + (size_t)(t + 1) * kstep;
;             const char* a2 = last ? nA : cA + (size_t)(t + 2) * kstep; const char* b2 = last ? nB : cB + (size_t)(t + 2) * kstep;
;             const char* a3 = a2 + kstep; const char* b3 = b2 + kstep;
;             if (last && has_next) S.a_ready(nxt);
;             if constexpr (SP2) {
;             PG8_LDB(B0, 0, 0); PG8_LDB(B1, 0, 1); PG8_SCHED; PG8_LDA(At, 0, 0); PG8_STAGE(PG8_SA(1, 1), a1 + hstep, voffA);
;             PG8_WAIT_V(8); PG8_WAIT_L(0); PG8_BAR; PG8_MMA(0, 0, At, B0); PG8_MMA(0, 1, At, B1); PG8_BAR; PG8_SCHED;
;             PG8_LDA(At, 0, 1); PG8_STAGE(PG8_SB(0, 0), b2, voffB); PG8_STAGE(PG8_SB(0, 1), b2 + hstep, voffB); PG8_STAGE(PG8_SA(0, 0), a2, voffA);
;             PG8_WAIT_V(8); PG8_WAIT_L(0); PG8_BAR; PG8_MMA(1, 0, At, B0); PG8_MMA(1, 1, At, B1); PG8_BAR; PG8_SCHED;
.LBB0_1392:
	s_barrier
	ds_read_b128 v[18:21], v192
	ds_read_b128 v[22:25], v192 offset:1024
	ds_read_b128 v[26:29], v192 offset:2048
	ds_read_b128 v[30:33], v192 offset:3072
	ds_read_b128 v[2:5], v193
	ds_read_b128 v[6:9], v193 offset:1024
	ds_read_b128 v[10:13], v193 offset:2048
	ds_read_b128 v[14:17], v193 offset:3072
	s_add_u32 s30, s36, 0x100
	s_addc_u32 s31, s37, 0
	s_cmp_eq_u32 s76, 24
	s_cselect_b64 vcc, -1, 0
	s_cselect_b32 s39, s27, s31
	s_cselect_b32 s38, s26, s30
	v_cndmask_b32_e32 v183, v181, v179, vcc
	v_cndmask_b32_e32 v182, v180, v178, vcc
	s_mov_b32 m0, s56
	v_lshl_add_u64 v[224:225], s[36:37], 0, v[174:175]
	ds_read_b128 v[184:187], v194
	ds_read_b128 v[188:191], v194 offset:1024
	ds_read_b128 v[200:203], v194 offset:2048
	ds_read_b128 v[204:207], v194 offset:3072
	ds_read_b128 v[208:211], v194 offset:4096
	ds_read_b128 v[212:215], v194 offset:5120
	ds_read_b128 v[216:219], v194 offset:6144
	ds_read_b128 v[220:223], v194 offset:7168
	global_load_lds_dwordx4 v[224:225], off
	v_lshl_add_u64 v[224:225], s[36:37], 0, v[176:177]
	s_mov_b32 m0, s57
	s_nop 0
	global_load_lds_dwordx4 v[224:225], off
	s_waitcnt vmcnt(8)
	s_waitcnt lgkmcnt(0)
	s_barrier
	s_setprio 3
	s_waitcnt lgkmcnt(0)
	v_mfma_scale_f32_16x16x128_f8f6f4 v[158:161], v[18:25], v[184:191], v[158:161], v195, v195 op_sel_hi:[0,0,0]
	v_mfma_scale_f32_16x16x128_f8f6f4 v[154:157], v[26:33], v[184:191], v[154:157], v195, v195 op_sel_hi:[0,0,0]
	v_mfma_scale_f32_16x16x128_f8f6f4 v[142:145], v[18:25], v[200:207], v[142:145], v195, v195 op_sel_hi:[0,0,0]
	v_mfma_scale_f32_16x16x128_f8f6f4 v[138:141], v[26:33], v[200:207], v[138:141], v195, v195 op_sel_hi:[0,0,0]
	v_mfma_scale_f32_16x16x128_f8f6f4 v[126:129], v[18:25], v[208:215], v[126:129], v195, v195 op_sel_hi:[0,0,0]
	v_mfma_scale_f32_16x16x128_f8f6f4 v[122:125], v[26:33], v[208:215], v[122:125], v195, v195 op_sel_hi:[0,0,0]
	v_mfma_scale_f32_16x16x128_f8f6f4 v[110:113], v[18:25], v[216:223], v[110:113], v195, v195 op_sel_hi:[0,0,0]
	v_mfma_scale_f32_16x16x128_f8f6f4 v[106:109], v[26:33], v[216:223], v[106:109], v195, v195 op_sel_hi:[0,0,0]
	s_setprio 0
	s_setprio 3
	v_mfma_scale_f32_16x16x128_f8f6f4 v[150:153], v[2:9], v[184:191], v[150:153], v195, v195 op_sel_hi:[0,0,0]
	v_mfma_scale_f32_16x16x128_f8f6f4 v[146:149], v[10:17], v[184:191], v[146:149], v195, v195 op_sel_hi:[0,0,0]
	v_mfma_scale_f32_16x16x128_f8f6f4 v[134:137], v[2:9], v[200:207], v[134:137], v195, v195 op_sel_hi:[0,0,0]
	v_mfma_scale_f32_16x16x128_f8f6f4 v[130:133], v[10:17], v[200:207], v[130:133], v195, v195 op_sel_hi:[0,0,0]
	v_mfma_scale_f32_16x16x128_f8f6f4 v[118:121], v[2:9], v[208:215], v[118:121], v195, v195 op_sel_hi:[0,0,0]
	v_mfma_scale_f32_16x16x128_f8f6f4 v[114:117], v[10:17], v[208:215], v[114:117], v195, v195 op_sel_hi:[0,0,0]
	v_mfma_scale_f32_16x16x128_f8f6f4 v[102:105], v[2:9], v[216:223], v[102:105], v195, v195 op_sel_hi:[0,0,0]
	v_mfma_scale_f32_16x16x128_f8f6f4 v[98:101], v[10:17], v[216:223], v[98:101], v195, v195 op_sel_hi:[0,0,0]
	s_setprio 0
	s_barrier
	s_mov_b32 m0, s58
	v_lshl_add_u64 v[184:185], v[182:183], 0, v[166:167]
	ds_read_b128 v[200:203], v194 offset:16384
	ds_read_b128 v[204:207], v194 offset:17408
	ds_read_b128 v[208:211], v194 offset:18432
	ds_read_b128 v[212:215], v194 offset:19456
	ds_read_b128 v[216:219], v194 offset:20480
	ds_read_b128 v[220:223], v194 offset:21504
	ds_read_b128 v[224:227], v194 offset:22528
	ds_read_b128 v[228:231], v194 offset:23552
	global_load_lds_dwordx4 v[184:185], off
	v_lshl_add_u64 v[186:187], v[182:183], 0, v[170:171]
	s_mov_b32 m0, s59
	v_lshl_add_u64 v[188:189], v[182:183], 0, s[10:11]
	global_load_lds_dwordx4 v[186:187], off
	v_lshl_add_u64 v[190:191], v[188:189], 0, v[166:167]
	s_mov_b32 m0, s60
	v_lshl_add_u64 v[188:189], v[188:189], 0, v[170:171]
	global_load_lds_dwordx4 v[190:191], off
	s_mov_b32 m0, s61
	v_lshl_add_u64 v[190:191], s[38:39], 0, v[168:169]
	global_load_lds_dwordx4 v[188:189], off
	v_lshl_add_u64 v[188:189], s[38:39], 0, v[164:165]
	s_mov_b32 m0, s45
	s_nop 0
	global_load_lds_dwordx4 v[188:189], off
	s_mov_b32 m0, s46
	s_nop 0
	global_load_lds_dwordx4 v[190:191], off
	s_waitcnt vmcnt(8)
	s_waitcnt lgkmcnt(0)
	s_barrier
	s_setprio 3
	s_waitcnt lgkmcnt(0)
	v_mfma_scale_f32_16x16x128_f8f6f4 v[94:97], v[18:25], v[200:207], v[94:97], v195, v195 op_sel_hi:[0,0,0]
	v_mfma_scale_f32_16x16x128_f8f6f4 v[90:93], v[26:33], v[200:207], v[90:93], v195, v195 op_sel_hi:[0,0,0]
	v_mfma_scale_f32_16x16x128_f8f6f4 v[78:81], v[18:25], v[208:215], v[78:81], v195, v195 op_sel_hi:[0,0,0]
	v_mfma_scale_f32_16x16x128_f8f6f4 v[74:77], v[26:33], v[208:215], v[74:77], v195, v195 op_sel_hi:[0,0,0]
	v_mfma_scale_f32_16x16x128_f8f6f4 v[62:65], v[18:25], v[216:223], v[62:65], v195, v195 op_sel_hi:[0,0,0]
	v_mfma_scale_f32_16x16x128_f8f6f4 v[58:61], v[26:33], v[216:223], v[58:61], v195, v195 op_sel_hi:[0,0,0]
	v_mfma_scale_f32_16x16x128_f8f6f4 v[46:49], v[18:25], v[224:231], v[46:49], v195, v195 op_sel_hi:[0,0,0]
	v_mfma_scale_f32_16x16x128_f8f6f4 v[42:45], v[26:33], v[224:231], v[42:45], v195, v195 op_sel_hi:[0,0,0]
	s_setprio 0
	s_setprio 3
	v_mfma_scale_f32_16x16x128_f8f6f4 v[86:89], v[2:9], v[200:207], v[86:89], v195, v195 op_sel_hi:[0,0,0]
	v_mfma_scale_f32_16x16x128_f8f6f4 v[82:85], v[10:17], v[200:207], v[82:85], v195, v195 op_sel_hi:[0,0,0]
	v_mfma_scale_f32_16x16x128_f8f6f4 v[70:73], v[2:9], v[208:215], v[70:73], v195, v195 op_sel_hi:[0,0,0]
	v_mfma_scale_f32_16x16x128_f8f6f4 v[66:69], v[10:17], v[208:215], v[66:69], v195, v195 op_sel_hi:[0,0,0]
	v_mfma_scale_f32_16x16x128_f8f6f4 v[54:57], v[2:9], v[216:223], v[54:57], v195, v195 op_sel_hi:[0,0,0]
	v_mfma_scale_f32_16x16x128_f8f6f4 v[50:53], v[10:17], v[216:223], v[50:53], v195, v195 op_sel_hi:[0,0,0]
	v_mfma_scale_f32_16x16x128_f8f6f4 v[38:41], v[2:9], v[224:231], v[38:41], v195, v195 op_sel_hi:[0,0,0]
	v_mfma_scale_f32_16x16x128_f8f6f4 v[34:37], v[10:17], v[224:231], v[34:37], v195, v195 op_sel_hi:[0,0,0]
	s_setprio 0
	s_barrier
; #define PG8_STAGE(bufoff, gbase, voff) do { _Pragma("unroll") for (int _i = 0; _i < 2; ++_i) \
;         __builtin_amdgcn_global_load_lds((const unsigned*)((const char*)(gbase) + (voff)[_i]), (PG8_LAS unsigned*)(lds + (bufoff) + ldsw + _i * 8192), 16, 0, 0); } while (0)
; #define PG8_LDA(dst, b, h) do { _Pragma("unroll") for (int m = 0; m < 4; ++m) Frag<F8>::load(dst[m], lds + PG8_SA(b, h) + aoff + m * 2048); } while (0)
; #define PG8_LDB(dst, b, h) do { _Pragma("unroll") for (int n = 0; n < 2; ++n) Frag<F8>::load(dst[n], lds + PG8_SB(b, h) + boff + n * 2048); } while (0)
; #define PG8_MMA(ai, bj, At, Bt) do { __builtin_amdgcn_s_setprio(3); _Pragma("unroll") for (int m = 0; m < 4; ++m) _Pragma("unroll") for (int n = 0; n < 2; ++n) Frag<F8>::mma(acc[ai][bj][m][n], Bt[n], At[m]); \
;         __builtin_amdgcn_s_setprio(0); } while (0)
; #define PG8_WAIT_V(n) asm volatile("s_waitcnt vmcnt(" #n ")" ::: "memory")
; #define PG8_WAIT_L(n) asm volatile("s_waitcnt lgkmcnt(" #n ")" ::: "memory")
; #define PG8_BAR __builtin_amdgcn_s_barrier()
; #define PG8_SCHED __builtin_amdgcn_sched_barrier(0)
; template <class Epi, class Sched, bool ALIGN_EPI = false, bool SP2 = false, bool F8 = false>
; __device__ __forceinline__ void gemm_phase(PG8_LAS unsigned char* lds, const Gemm g, const Sched& S, const Epi& E) {
;     ...
;             PG8_LDB(B0, 1, 0); PG8_LDB(B1, 1, 1); PG8_SCHED; PG8_LDA(At, 1, 0); PG8_STAGE(PG8_SA(0, 1), a2 + hstep, voffA);
;             PG8_WAIT_V(8); PG8_WAIT_L(0); PG8_BAR; PG8_MMA(0, 0, At, B0); PG8_MMA(0, 1, At, B1); PG8_BAR; PG8_SCHED;
;             PG8_LDA(At, 1, 1); PG8_STAGE(PG8_SB(1, 0), b3, voffB); PG8_STAGE(PG8_SB(1, 1), b3 + hstep, voffB); PG8_STAGE(PG8_SA(1, 0), a3, voffA);
;             PG8_WAIT_V(8); PG8_WAIT_L(0); PG8_BAR; PG8_MMA(1, 0, At, B0); PG8_MMA(1, 1, At, B1); PG8_BAR; PG8_SCHED;
	ds_read_b128 v[2:5], v196
	ds_read_b128 v[6:9], v196 offset:1024
	ds_read_b128 v[10:13], v196 offset:2048
	ds_read_b128 v[14:17], v196 offset:3072
	ds_read_b128 v[18:21], v197
	ds_read_b128 v[22:25], v197 offset:1024
	ds_read_b128 v[26:29], v197 offset:2048
	ds_read_b128 v[30:33], v197 offset:3072
	s_add_u32 s4, s38, 0x70000
	s_addc_u32 s5, s39, 0
	s_mov_b32 m0, s47
	v_lshl_add_u64 v[232:233], s[4:5], 0, v[164:165]
	ds_read_b128 v[200:203], v194 offset:32768
	ds_read_b128 v[204:207], v194 offset:33792
	ds_read_b128 v[208:211], v194 offset:34816
	ds_read_b128 v[212:215], v194 offset:35840
	ds_read_b128 v[216:219], v194 offset:36864
	ds_read_b128 v[220:223], v194 offset:37888
	ds_read_b128 v[224:227], v194 offset:38912
	ds_read_b128 v[228:231], v194 offset:39936
	global_load_lds_dwordx4 v[232:233], off
	v_lshl_add_u64 v[232:233], s[4:5], 0, v[168:169]
	s_mov_b32 m0, s48
	s_nop 0
	global_load_lds_dwordx4 v[232:233], off
	s_waitcnt vmcnt(8)
	s_waitcnt lgkmcnt(0)
	s_barrier
	s_setprio 3
	s_waitcnt lgkmcnt(0)
	v_mfma_scale_f32_16x16x128_f8f6f4 v[158:161], v[2:9], v[200:207], v[158:161], v195, v195 op_sel_hi:[0,0,0]
	v_mfma_scale_f32_16x16x128_f8f6f4 v[154:157], v[10:17], v[200:207], v[154:157], v195, v195 op_sel_hi:[0,0,0]
	v_mfma_scale_f32_16x16x128_f8f6f4 v[142:145], v[2:9], v[208:215], v[142:145], v195, v195 op_sel_hi:[0,0,0]
	v_mfma_scale_f32_16x16x128_f8f6f4 v[138:141], v[10:17], v[208:215], v[138:141], v195, v195 op_sel_hi:[0,0,0]
	v_mfma_scale_f32_16x16x128_f8f6f4 v[126:129], v[2:9], v[216:223], v[126:129], v195, v195 op_sel_hi:[0,0,0]
	v_mfma_scale_f32_16x16x128_f8f6f4 v[122:125], v[10:17], v[216:223], v[122:125], v195, v195 op_sel_hi:[0,0,0]
	v_mfma_scale_f32_16x16x128_f8f6f4 v[110:113], v[2:9], v[224:231], v[110:113], v195, v195 op_sel_hi:[0,0,0]
	v_mfma_scale_f32_16x16x128_f8f6f4 v[106:109], v[10:17], v[224:231], v[106:109], v195, v195 op_sel_hi:[0,0,0]
	s_setprio 0
	s_setprio 3
	v_mfma_scale_f32_16x16x128_f8f6f4 v[150:153], v[18:25], v[200:207], v[150:153], v195, v195 op_sel_hi:[0,0,0]
	v_mfma_scale_f32_16x16x128_f8f6f4 v[146:149], v[26:33], v[200:207], v[146:149], v195, v195 op_sel_hi:[0,0,0]
	v_mfma_scale_f32_16x16x128_f8f6f4 v[134:137], v[18:25], v[208:215], v[134:137], v195, v195 op_sel_hi:[0,0,0]
	v_mfma_scale_f32_16x16x128_f8f6f4 v[130:133], v[26:33], v[208:215], v[130:133], v195, v195 op_sel_hi:[0,0,0]
	v_mfma_scale_f32_16x16x128_f8f6f4 v[118:121], v[18:25], v[216:223], v[118:121], v195, v195 op_sel_hi:[0,0,0]
	v_mfma_scale_f32_16x16x128_f8f6f4 v[114:117], v[26:33], v[216:223], v[114:117], v195, v195 op_sel_hi:[0,0,0]
	v_mfma_scale_f32_16x16x128_f8f6f4 v[102:105], v[18:25], v[224:231], v[102:105], v195, v195 op_sel_hi:[0,0,0]
	v_mfma_scale_f32_16x16x128_f8f6f4 v[98:101], v[26:33], v[224:231], v[98:101], v195, v195 op_sel_hi:[0,0,0]
	s_setprio 0
	s_barrier
	s_mov_b32 m0, s67
	v_lshl_add_u64 v[184:185], v[184:185], 0, s[18:19]
	ds_read_b128 v[200:203], v194 offset:49152
	ds_read_b128 v[204:207], v194 offset:50176
	ds_read_b128 v[208:211], v194 offset:51200
	ds_read_b128 v[212:215], v194 offset:52224
	ds_read_b128 v[216:219], v194 offset:53248
	ds_read_b128 v[220:223], v194 offset:54272
	ds_read_b128 v[224:227], v194 offset:55296
	ds_read_b128 v[228:231], v194 offset:56320
	global_load_lds_dwordx4 v[184:185], off
	v_lshl_add_u64 v[184:185], v[186:187], 0, s[18:19]
	s_mov_b32 m0, s70
	v_lshl_add_u64 v[182:183], v[182:183], 0, s[20:21]
	global_load_lds_dwordx4 v[184:185], off
	v_lshl_add_u64 v[184:185], v[182:183], 0, v[166:167]
	s_mov_b32 m0, s71
	v_lshl_add_u64 v[182:183], v[182:183], 0, v[170:171]
	global_load_lds_dwordx4 v[184:185], off
	s_mov_b32 m0, s72
	s_nop 0
	global_load_lds_dwordx4 v[182:183], off
	v_lshl_add_u64 v[182:183], v[188:189], 0, s[18:19]
	s_mov_b32 m0, s49
	s_nop 0
	global_load_lds_dwordx4 v[182:183], off
	v_lshl_add_u64 v[182:183], v[190:191], 0, s[18:19]
	s_mov_b32 m0, s50
	s_nop 0
	global_load_lds_dwordx4 v[182:183], off
	s_waitcnt vmcnt(8)
	s_waitcnt lgkmcnt(0)
	s_barrier
	s_setprio 3
	s_waitcnt lgkmcnt(0)
	v_mfma_scale_f32_16x16x128_f8f6f4 v[94:97], v[2:9], v[200:207], v[94:97], v195, v195 op_sel_hi:[0,0,0]
	v_mfma_scale_f32_16x16x128_f8f6f4 v[90:93], v[10:17], v[200:207], v[90:93], v195, v195 op_sel_hi:[0,0,0]
	v_mfma_scale_f32_16x16x128_f8f6f4 v[78:81], v[2:9], v[208:215], v[78:81], v195, v195 op_sel_hi:[0,0,0]
	v_mfma_scale_f32_16x16x128_f8f6f4 v[74:77], v[10:17], v[208:215], v[74:77], v195, v195 op_sel_hi:[0,0,0]
	v_mfma_scale_f32_16x16x128_f8f6f4 v[62:65], v[2:9], v[216:223], v[62:65], v195, v195 op_sel_hi:[0,0,0]
	v_mfma_scale_f32_16x16x128_f8f6f4 v[58:61], v[10:17], v[216:223], v[58:61], v195, v195 op_sel_hi:[0,0,0]
	v_mfma_scale_f32_16x16x128_f8f6f4 v[46:49], v[2:9], v[224:231], v[46:49], v195, v195 op_sel_hi:[0,0,0]
	v_mfma_scale_f32_16x16x128_f8f6f4 v[42:45], v[10:17], v[224:231], v[42:45], v195, v195 op_sel_hi:[0,0,0]
	s_setprio 0
	s_setprio 3
	v_mfma_scale_f32_16x16x128_f8f6f4 v[86:89], v[18:25], v[200:207], v[86:89], v195, v195 op_sel_hi:[0,0,0]
	v_mfma_scale_f32_16x16x128_f8f6f4 v[82:85], v[26:33], v[200:207], v[82:85], v195, v195 op_sel_hi:[0,0,0]
	v_mfma_scale_f32_16x16x128_f8f6f4 v[70:73], v[18:25], v[208:215], v[70:73], v195, v195 op_sel_hi:[0,0,0]
	v_mfma_scale_f32_16x16x128_f8f6f4 v[66:69], v[26:33], v[208:215], v[66:69], v195, v195 op_sel_hi:[0,0,0]
	v_mfma_scale_f32_16x16x128_f8f6f4 v[54:57], v[18:25], v[216:223], v[54:57], v195, v195 op_sel_hi:[0,0,0]
	v_mfma_scale_f32_16x16x128_f8f6f4 v[50:53], v[26:33], v[216:223], v[50:53], v195, v195 op_sel_hi:[0,0,0]
	v_mfma_scale_f32_16x16x128_f8f6f4 v[38:41], v[18:25], v[224:231], v[38:41], v195, v195 op_sel_hi:[0,0,0]
	v_mfma_scale_f32_16x16x128_f8f6f4 v[34:37], v[26:33], v[224:231], v[34:37], v195, v195 op_sel_hi:[0,0,0]
	s_setprio 0
	s_add_i32 s76, s76, 2
	v_lshl_add_u64 v[180:181], v[180:181], 0, s[24:25]
	s_cmp_gt_u32 s76, 25
	s_mov_b64 s[36:37], s[30:31]
	s_cbranch_scc0 .LBB0_1392

; __device__ __forceinline__ unsigned pk4_fp8(float a, float b, float c, float d) { int w = 0; w = __builtin_amdgcn_cvt_pk_fp8_f32(a, b, w, false); w = __builtin_amdgcn_cvt_pk_fp8_f32(c, d, w, true); return (unsigned)w; }
; #define PG8_BAR __builtin_amdgcn_s_barrier()
;     __device__ __forceinline__ void operator()(const f32x4 (&acc)[2][2][4][2], const Unit& u, int wr, int wc, int fr, int fq) const {
;     ...
;                 if (d >= 0) { const float gt = gtab[rl]; unsigned char* rowp = O + (size_t)d * 1024 + col0;
; #pragma unroll
;                     for (int bj = 0; bj < 2; ++bj) { const f32x4 v0 = acc[ai][bj][m][0] * gt, v1 = acc[ai][bj][m][1] * gt;
;                         u32x2 w; w.x = pk4_fp8(v0[0], v0[1], v0[2], v0[3]); w.y = pk4_fp8(v1[0], v1[1], v1[2], v1[3]);
;                         *(u32x2*)(rowp + bj * HALF) = w; } } }
;         ++ui;
; template <class Epi, class Sched, bool ALIGN_EPI = false, bool SP2 = false, bool F8 = false>
; __device__ __forceinline__ void gemm_phase(PG8_LAS unsigned char* lds, const Gemm g, const Sched& S, const Epi& E) {
;     ...
;         if constexpr (!Epi::AFTER_DRAIN) { E(acc, cur, wr, wc, fr, fq); S.done(cur); }
;         if (!has_next) break;
; #pragma unroll
;         for (int a = 0; a < 2; ++a)
; #pragma unroll
;             for (int b = 0; b < 2; ++b)
; #pragma unroll
;                 for (int m = 0; m < 4; ++m)
; #pragma unroll
;                     for (int n = 0; n < 2; ++n) acc[a][b][m][n] = (f32x4){0.f, 0.f, 0.f, 0.f};
;         cur = nxt; cA = nA; cB = nB; ++ui;
;         if constexpr (ALIGN_EPI) { if (wr == 1) PG8_BAR; }
.LBB0_1411:
	s_or_b64 exec, exec, s[30:31]
	s_and_b64 vcc, exec, s[6:7]
	s_mov_b64 s[6:7], -1
	s_barrier
	s_cbranch_vccnz .LBB0_1384
	s_andn2_b64 vcc, exec, s[14:15]
	s_cbranch_vccnz .LBB0_1383
	s_barrier
	s_branch .LBB0_1383
